# GEMM K-loops: removed back-to-back s_setprio 0/1 between the two MFMA blocks of a super-phase
# baseline (speedup 1.0000x reference)
; #define PG8_STAGE(bufoff, gbase, voff) do { _Pragma("unroll") for (int _i = 0; _i < 2; ++_i) \
;         __builtin_amdgcn_global_load_lds((const unsigned*)((const char*)(gbase) + (voff)[_i]), (PG8_LAS unsigned*)(lds + (bufoff) + ldsw + _i * 8192), 16, 0, 0); } while (0)
; #define PG8_LDA(dst, b, h) do { if constexpr (DT != 1) { _Pragma("unroll") for (int m = 0; m < 4; ++m) _Pragma("unroll") for (int k = 0; k < 2; ++k) dst[m][k] = *(const PG8_LAS bf16x8*)(lds + PG8_SA(b, h) + aoff + m * 2048 + k * 1024); } \
;         else { _Pragma("unroll") for (int m = 0; m < 4; ++m) dst##8[m] = ld32(lds + PG8_SA(b, h) + aoff + m * 2048); } } while (0)
; #define PG8_LDB(dst, b, h) do { if constexpr (DT != 1) { _Pragma("unroll") for (int n = 0; n < 2; ++n) _Pragma("unroll") for (int k = 0; k < 2; ++k) dst[n][k] = *(const PG8_LAS bf16x8*)(lds + PG8_SB(b, h) + boff + n * 2048 + k * 1024); } \
;         else { _Pragma("unroll") for (int n = 0; n < 2; ++n) dst##8[n] = ld32(lds + PG8_SB(b, h) + boff + n * 2048); } } while (0)
; #define PG8_WAIT_V(n) asm volatile("s_waitcnt vmcnt(" #n ")" ::: "memory")
; #define PG8_WAIT_L(n) asm volatile("s_waitcnt lgkmcnt(" #n ")" ::: "memory")
; #define PG8_BAR __builtin_amdgcn_s_barrier()
; #define PG8_SCHED __builtin_amdgcn_sched_barrier(0)
;     ...
;             PG8_LDB(B0, 0, 0); PG8_LDB(B1, 0, 1); PG8_SCHED; PG8_LDA(At, 0, 0); PG8_STAGE(PG8_SA(1, 1), a1 + hstepA, voffA);
;             PG8_WAIT_V(8); PG8_WAIT_L(0); PG8_BAR; PG8_MMA(0, 0, At, B0); PG8_MMA(0, 1, At, B1); PG8_BAR; PG8_SCHED;
;             PG8_LDA(At, 0, 1); PG8_STAGE(PG8_SB(0, 0), b2, voffB); PG8_STAGE(PG8_SB(0, 1), b2 + hstepB, voffB); PG8_STAGE(PG8_SA(0, 0), a2, voffA);
;             PG8_WAIT_V(8); PG8_WAIT_L(0); PG8_BAR; PG8_MMA(1, 0, At, B0); PG8_MMA(1, 1, At, B1); PG8_BAR; PG8_SCHED;
.LBB0_227:
	v_add_u32_e32 v142, s35, v164
	v_add_u32_e32 v180, s36, v164
	ds_read_b128 v[130:133], v142
	ds_read_b128 v[134:137], v142 offset:1024
	ds_read_b128 v[138:141], v142 offset:2048
	ds_read_b128 v[142:145], v142 offset:3072
	ds_read_b128 v[168:171], v180
	ds_read_b128 v[172:175], v180 offset:1024
	ds_read_b128 v[176:179], v180 offset:2048
	ds_read_b128 v[180:183], v180 offset:3072
	s_add_i32 s68, s26, 2
	s_add_u32 s27, s24, 0xfffc0080
	s_addc_u32 s28, s25, -1
	s_cmp_eq_u32 s61, s26
	s_cselect_b32 s26, s65, s66
	s_cselect_b32 s29, s15, s28
	s_cselect_b32 s28, s17, s27
	s_cselect_b32 s27, s64, s67
	s_add_i32 m0, s46, 0xc000
	ds_read_b128 v[184:187], v167
	ds_read_b128 v[188:191], v167 offset:1024
	ds_read_b128 v[192:195], v167 offset:2048
	ds_read_b128 v[196:199], v167 offset:3072
	ds_read_b128 v[200:203], v167 offset:4096
	ds_read_b128 v[204:207], v167 offset:5120
	ds_read_b128 v[208:211], v167 offset:6144
	ds_read_b128 v[212:215], v167 offset:7168
	global_load_lds_dwordx4 v158, s[24:25]
	s_add_i32 m0, s46, 0xe000
	s_nop 0
	global_load_lds_dwordx4 v156, s[24:25]
	s_waitcnt vmcnt(8)
	s_waitcnt lgkmcnt(0)
	s_barrier
	s_setprio 1
	s_waitcnt lgkmcnt(0)
	v_mfma_i32_16x16x64_i8 v[126:129], v[130:133], v[184:187], v[126:129]
	v_mfma_i32_16x16x64_i8 v[118:121], v[138:141], v[184:187], v[118:121]
	v_mfma_i32_16x16x64_i8 v[110:113], v[130:133], v[192:195], v[110:113]
	v_mfma_i32_16x16x64_i8 v[102:105], v[138:141], v[192:195], v[102:105]
	v_mfma_i32_16x16x64_i8 v[94:97], v[130:133], v[200:203], v[94:97]
	v_mfma_i32_16x16x64_i8 v[86:89], v[138:141], v[200:203], v[86:89]
	v_mfma_i32_16x16x64_i8 v[78:81], v[130:133], v[208:211], v[78:81]
	v_mfma_i32_16x16x64_i8 v[70:73], v[138:141], v[208:211], v[70:73]
	v_mfma_i32_16x16x64_i8 v[126:129], v[134:137], v[188:191], v[126:129]
	v_mfma_i32_16x16x64_i8 v[118:121], v[142:145], v[188:191], v[118:121]
	v_mfma_i32_16x16x64_i8 v[110:113], v[134:137], v[196:199], v[110:113]
	v_mfma_i32_16x16x64_i8 v[102:105], v[142:145], v[196:199], v[102:105]
	v_mfma_i32_16x16x64_i8 v[94:97], v[134:137], v[204:207], v[94:97]
	v_mfma_i32_16x16x64_i8 v[86:89], v[142:145], v[204:207], v[86:89]
	v_mfma_i32_16x16x64_i8 v[78:81], v[134:137], v[212:215], v[78:81]
	v_mfma_i32_16x16x64_i8 v[70:73], v[142:145], v[212:215], v[70:73]
	v_mfma_i32_16x16x64_i8 v[122:125], v[168:171], v[184:187], v[122:125]
	v_mfma_i32_16x16x64_i8 v[114:117], v[176:179], v[184:187], v[114:117]
	v_mfma_i32_16x16x64_i8 v[106:109], v[168:171], v[192:195], v[106:109]
	v_mfma_i32_16x16x64_i8 v[98:101], v[176:179], v[192:195], v[98:101]
	v_mfma_i32_16x16x64_i8 v[90:93], v[168:171], v[200:203], v[90:93]
	v_mfma_i32_16x16x64_i8 v[82:85], v[176:179], v[200:203], v[82:85]
	v_mfma_i32_16x16x64_i8 v[74:77], v[168:171], v[208:211], v[74:77]
	v_mfma_i32_16x16x64_i8 v[66:69], v[176:179], v[208:211], v[66:69]
	v_mfma_i32_16x16x64_i8 v[122:125], v[172:175], v[188:191], v[122:125]
	v_mfma_i32_16x16x64_i8 v[114:117], v[180:183], v[188:191], v[114:117]
	v_mfma_i32_16x16x64_i8 v[106:109], v[172:175], v[196:199], v[106:109]
	v_mfma_i32_16x16x64_i8 v[98:101], v[180:183], v[196:199], v[98:101]
	v_mfma_i32_16x16x64_i8 v[90:93], v[172:175], v[204:207], v[90:93]
	v_mfma_i32_16x16x64_i8 v[82:85], v[180:183], v[204:207], v[82:85]
	v_mfma_i32_16x16x64_i8 v[74:77], v[172:175], v[212:215], v[74:77]
	v_mfma_i32_16x16x64_i8 v[66:69], v[180:183], v[212:215], v[66:69]
	s_setprio 0
	s_barrier
	s_mov_b32 m0, s23
	s_add_u32 s98, s26, 0x80
	s_addc_u32 s99, s27, 0
	s_add_u32 s70, s26, 0x40000
	ds_read_b128 v[184:187], v167 offset:16384
	ds_read_b128 v[188:191], v167 offset:17408
	ds_read_b128 v[192:195], v167 offset:18432
	ds_read_b128 v[196:199], v167 offset:19456
	ds_read_b128 v[200:203], v167 offset:20480
	ds_read_b128 v[204:207], v167 offset:21504
	ds_read_b128 v[208:211], v167 offset:22528
	ds_read_b128 v[212:215], v167 offset:23552
	global_load_lds_dwordx4 v148, s[26:27]
	s_mov_b32 m0, s43
	s_addc_u32 s71, s27, 0
	global_load_lds_dwordx4 v152, s[26:27]
	s_mov_b32 m0, s44
	s_nop 0
	global_load_lds_dwordx4 v148, s[70:71]
	s_mov_b32 m0, s45
	s_nop 0
	global_load_lds_dwordx4 v152, s[70:71]
	s_add_u32 s100, s28, 0x80
	s_addc_u32 s101, s29, 0
	s_mov_b32 m0, s46
	s_nop 0
	global_load_lds_dwordx4 v146, s[28:29]
	s_mov_b32 m0, s47
	s_nop 0
	global_load_lds_dwordx4 v150, s[28:29]
	s_waitcnt vmcnt(8)
	s_waitcnt lgkmcnt(0)
	s_barrier
	s_setprio 1
	s_waitcnt lgkmcnt(0)
	v_mfma_i32_16x16x64_i8 v[62:65], v[130:133], v[184:187], v[62:65]
	v_mfma_i32_16x16x64_i8 v[54:57], v[138:141], v[184:187], v[54:57]
	v_mfma_i32_16x16x64_i8 v[46:49], v[130:133], v[192:195], v[46:49]
	v_mfma_i32_16x16x64_i8 v[38:41], v[138:141], v[192:195], v[38:41]
	v_mfma_i32_16x16x64_i8 v[30:33], v[130:133], v[200:203], v[30:33]
	v_mfma_i32_16x16x64_i8 v[22:25], v[138:141], v[200:203], v[22:25]
	v_mfma_i32_16x16x64_i8 v[14:17], v[130:133], v[208:211], v[14:17]
	v_mfma_i32_16x16x64_i8 v[6:9], v[138:141], v[208:211], v[6:9]
	v_mfma_i32_16x16x64_i8 v[62:65], v[134:137], v[188:191], v[62:65]
	v_mfma_i32_16x16x64_i8 v[54:57], v[142:145], v[188:191], v[54:57]
	v_mfma_i32_16x16x64_i8 v[46:49], v[134:137], v[196:199], v[46:49]
	v_mfma_i32_16x16x64_i8 v[38:41], v[142:145], v[196:199], v[38:41]
	v_mfma_i32_16x16x64_i8 v[30:33], v[134:137], v[204:207], v[30:33]
	v_mfma_i32_16x16x64_i8 v[22:25], v[142:145], v[204:207], v[22:25]
	v_mfma_i32_16x16x64_i8 v[14:17], v[134:137], v[212:215], v[14:17]
	v_mfma_i32_16x16x64_i8 v[6:9], v[142:145], v[212:215], v[6:9]
	v_mfma_i32_16x16x64_i8 v[58:61], v[168:171], v[184:187], v[58:61]
	v_mfma_i32_16x16x64_i8 v[50:53], v[176:179], v[184:187], v[50:53]
	v_mfma_i32_16x16x64_i8 v[42:45], v[168:171], v[192:195], v[42:45]
	v_mfma_i32_16x16x64_i8 v[34:37], v[176:179], v[192:195], v[34:37]
	v_mfma_i32_16x16x64_i8 v[26:29], v[168:171], v[200:203], v[26:29]
	v_mfma_i32_16x16x64_i8 v[18:21], v[176:179], v[200:203], v[18:21]
	v_mfma_i32_16x16x64_i8 v[10:13], v[168:171], v[208:211], v[10:13]
	v_mfma_i32_16x16x64_i8 v[2:5], v[176:179], v[208:211], v[2:5]
	v_mfma_i32_16x16x64_i8 v[58:61], v[172:175], v[188:191], v[58:61]
	v_mfma_i32_16x16x64_i8 v[50:53], v[180:183], v[188:191], v[50:53]
	v_mfma_i32_16x16x64_i8 v[42:45], v[172:175], v[196:199], v[42:45]
	v_mfma_i32_16x16x64_i8 v[34:37], v[180:183], v[196:199], v[34:37]
	v_mfma_i32_16x16x64_i8 v[26:29], v[172:175], v[204:207], v[26:29]
	v_mfma_i32_16x16x64_i8 v[18:21], v[180:183], v[204:207], v[18:21]
	v_mfma_i32_16x16x64_i8 v[10:13], v[172:175], v[212:215], v[10:13]
	v_mfma_i32_16x16x64_i8 v[2:5], v[180:183], v[212:215], v[2:5]
	s_setprio 0
	s_barrier
; #define PG8_STAGE(bufoff, gbase, voff) do { _Pragma("unroll") for (int _i = 0; _i < 2; ++_i) \
;         __builtin_amdgcn_global_load_lds((const unsigned*)((const char*)(gbase) + (voff)[_i]), (PG8_LAS unsigned*)(lds + (bufoff) + ldsw + _i * 8192), 16, 0, 0); } while (0)
; #define PG8_LDA(dst, b, h) do { if constexpr (DT != 1) { _Pragma("unroll") for (int m = 0; m < 4; ++m) _Pragma("unroll") for (int k = 0; k < 2; ++k) dst[m][k] = *(const PG8_LAS bf16x8*)(lds + PG8_SA(b, h) + aoff + m * 2048 + k * 1024); } \
;         else { _Pragma("unroll") for (int m = 0; m < 4; ++m) dst##8[m] = ld32(lds + PG8_SA(b, h) + aoff + m * 2048); } } while (0)
; #define PG8_LDB(dst, b, h) do { if constexpr (DT != 1) { _Pragma("unroll") for (int n = 0; n < 2; ++n) _Pragma("unroll") for (int k = 0; k < 2; ++k) dst[n][k] = *(const PG8_LAS bf16x8*)(lds + PG8_SB(b, h) + boff + n * 2048 + k * 1024); } \
;         else { _Pragma("unroll") for (int n = 0; n < 2; ++n) dst##8[n] = ld32(lds + PG8_SB(b, h) + boff + n * 2048); } } while (0)
; #define PG8_WAIT_V(n) asm volatile("s_waitcnt vmcnt(" #n ")" ::: "memory")
; #define PG8_WAIT_L(n) asm volatile("s_waitcnt lgkmcnt(" #n ")" ::: "memory")
; #define PG8_BAR __builtin_amdgcn_s_barrier()
; #define PG8_SCHED __builtin_amdgcn_sched_barrier(0)
;     ...
;             PG8_LDB(B0, 1, 0); PG8_LDB(B1, 1, 1); PG8_SCHED; PG8_LDA(At, 1, 0); PG8_STAGE(PG8_SA(0, 1), a2 + hstepA, voffA);
;             PG8_WAIT_V(8); PG8_WAIT_L(0); PG8_BAR; PG8_MMA(0, 0, At, B0); PG8_MMA(0, 1, At, B1); PG8_BAR; PG8_SCHED;
;             PG8_LDA(At, 1, 1); PG8_STAGE(PG8_SB(1, 0), b3, voffB); PG8_STAGE(PG8_SB(1, 1), b3 + hstepB, voffB); PG8_STAGE(PG8_SA(1, 0), a3, voffA);
;             PG8_WAIT_V(8); PG8_WAIT_L(0); PG8_BAR; PG8_MMA(1, 0, At, B0); PG8_MMA(1, 1, At, B1); PG8_BAR; PG8_SCHED;
	v_add_u32_e32 v142, s51, v164
	v_add_u32_e32 v180, s52, v164
	ds_read_b128 v[130:133], v142
	ds_read_b128 v[134:137], v142 offset:1024
	ds_read_b128 v[138:141], v142 offset:2048
	ds_read_b128 v[142:145], v142 offset:3072
	ds_read_b128 v[168:171], v180
	ds_read_b128 v[172:175], v180 offset:1024
	ds_read_b128 v[176:179], v180 offset:2048
	ds_read_b128 v[180:183], v180 offset:3072
	s_add_u32 s28, s28, 0x40000
	s_addc_u32 s29, s29, 0
	s_mov_b32 m0, s48
	ds_read_b128 v[184:187], v167 offset:32768
	ds_read_b128 v[188:191], v167 offset:33792
	ds_read_b128 v[192:195], v167 offset:34816
	ds_read_b128 v[196:199], v167 offset:35840
	ds_read_b128 v[200:203], v167 offset:36864
	ds_read_b128 v[204:207], v167 offset:37888
	ds_read_b128 v[208:211], v167 offset:38912
	ds_read_b128 v[212:215], v167 offset:39936
	global_load_lds_dwordx4 v146, s[28:29]
	s_mov_b32 m0, s49
	s_nop 0
	global_load_lds_dwordx4 v150, s[28:29]
	s_waitcnt vmcnt(8)
	s_waitcnt lgkmcnt(0)
	s_barrier
	s_setprio 1
	s_waitcnt lgkmcnt(0)
	v_mfma_i32_16x16x64_i8 v[126:129], v[130:133], v[184:187], v[126:129]
	v_mfma_i32_16x16x64_i8 v[118:121], v[138:141], v[184:187], v[118:121]
	v_mfma_i32_16x16x64_i8 v[110:113], v[130:133], v[192:195], v[110:113]
	v_mfma_i32_16x16x64_i8 v[102:105], v[138:141], v[192:195], v[102:105]
	v_mfma_i32_16x16x64_i8 v[94:97], v[130:133], v[200:203], v[94:97]
	v_mfma_i32_16x16x64_i8 v[86:89], v[138:141], v[200:203], v[86:89]
	v_mfma_i32_16x16x64_i8 v[78:81], v[130:133], v[208:211], v[78:81]
	v_mfma_i32_16x16x64_i8 v[70:73], v[138:141], v[208:211], v[70:73]
	v_mfma_i32_16x16x64_i8 v[126:129], v[134:137], v[188:191], v[126:129]
	v_mfma_i32_16x16x64_i8 v[118:121], v[142:145], v[188:191], v[118:121]
	v_mfma_i32_16x16x64_i8 v[110:113], v[134:137], v[196:199], v[110:113]
	v_mfma_i32_16x16x64_i8 v[102:105], v[142:145], v[196:199], v[102:105]
	v_mfma_i32_16x16x64_i8 v[94:97], v[134:137], v[204:207], v[94:97]
	v_mfma_i32_16x16x64_i8 v[86:89], v[142:145], v[204:207], v[86:89]
	v_mfma_i32_16x16x64_i8 v[78:81], v[134:137], v[212:215], v[78:81]
	v_mfma_i32_16x16x64_i8 v[70:73], v[142:145], v[212:215], v[70:73]
	v_mfma_i32_16x16x64_i8 v[122:125], v[168:171], v[184:187], v[122:125]
	v_mfma_i32_16x16x64_i8 v[114:117], v[176:179], v[184:187], v[114:117]
	v_mfma_i32_16x16x64_i8 v[106:109], v[168:171], v[192:195], v[106:109]
	v_mfma_i32_16x16x64_i8 v[98:101], v[176:179], v[192:195], v[98:101]
	v_mfma_i32_16x16x64_i8 v[90:93], v[168:171], v[200:203], v[90:93]
	v_mfma_i32_16x16x64_i8 v[82:85], v[176:179], v[200:203], v[82:85]
	v_mfma_i32_16x16x64_i8 v[74:77], v[168:171], v[208:211], v[74:77]
	v_mfma_i32_16x16x64_i8 v[66:69], v[176:179], v[208:211], v[66:69]
	v_mfma_i32_16x16x64_i8 v[122:125], v[172:175], v[188:191], v[122:125]
	v_mfma_i32_16x16x64_i8 v[114:117], v[180:183], v[188:191], v[114:117]
	v_mfma_i32_16x16x64_i8 v[106:109], v[172:175], v[196:199], v[106:109]
	v_mfma_i32_16x16x64_i8 v[98:101], v[180:183], v[196:199], v[98:101]
	v_mfma_i32_16x16x64_i8 v[90:93], v[172:175], v[204:207], v[90:93]
	v_mfma_i32_16x16x64_i8 v[82:85], v[180:183], v[204:207], v[82:85]
	v_mfma_i32_16x16x64_i8 v[74:77], v[172:175], v[212:215], v[74:77]
	v_mfma_i32_16x16x64_i8 v[66:69], v[180:183], v[212:215], v[66:69]
	s_setprio 0
	s_barrier
	s_mov_b32 m0, s55
	s_add_u32 s26, s26, 0x40080
	ds_read_b128 v[184:187], v167 offset:49152
	ds_read_b128 v[188:191], v167 offset:50176
	ds_read_b128 v[192:195], v167 offset:51200
	ds_read_b128 v[196:199], v167 offset:52224
	ds_read_b128 v[200:203], v167 offset:53248
	ds_read_b128 v[204:207], v167 offset:54272
	ds_read_b128 v[208:211], v167 offset:55296
	ds_read_b128 v[212:215], v167 offset:56320
	global_load_lds_dwordx4 v148, s[98:99]
	s_mov_b32 m0, s56
	s_addc_u32 s27, s27, 0
	global_load_lds_dwordx4 v152, s[98:99]
	s_mov_b32 m0, s59
	s_nop 0
	global_load_lds_dwordx4 v148, s[26:27]
	s_mov_b32 m0, s60
	s_nop 0
	global_load_lds_dwordx4 v152, s[26:27]
	s_mov_b32 m0, s57
	s_nop 0
	global_load_lds_dwordx4 v146, s[100:101]
	s_mov_b32 m0, s58
	s_nop 0
	global_load_lds_dwordx4 v150, s[100:101]
	s_waitcnt vmcnt(8)
	s_waitcnt lgkmcnt(0)
	s_barrier
	s_setprio 1
	s_waitcnt lgkmcnt(0)
	v_mfma_i32_16x16x64_i8 v[62:65], v[130:133], v[184:187], v[62:65]
	v_mfma_i32_16x16x64_i8 v[54:57], v[138:141], v[184:187], v[54:57]
	v_mfma_i32_16x16x64_i8 v[46:49], v[130:133], v[192:195], v[46:49]
	v_mfma_i32_16x16x64_i8 v[38:41], v[138:141], v[192:195], v[38:41]
	v_mfma_i32_16x16x64_i8 v[30:33], v[130:133], v[200:203], v[30:33]
	v_mfma_i32_16x16x64_i8 v[22:25], v[138:141], v[200:203], v[22:25]
	v_mfma_i32_16x16x64_i8 v[14:17], v[130:133], v[208:211], v[14:17]
	v_mfma_i32_16x16x64_i8 v[6:9], v[138:141], v[208:211], v[6:9]
	v_mfma_i32_16x16x64_i8 v[62:65], v[134:137], v[188:191], v[62:65]
	v_mfma_i32_16x16x64_i8 v[54:57], v[142:145], v[188:191], v[54:57]
	v_mfma_i32_16x16x64_i8 v[46:49], v[134:137], v[196:199], v[46:49]
	v_mfma_i32_16x16x64_i8 v[38:41], v[142:145], v[196:199], v[38:41]
	v_mfma_i32_16x16x64_i8 v[30:33], v[134:137], v[204:207], v[30:33]
	v_mfma_i32_16x16x64_i8 v[22:25], v[142:145], v[204:207], v[22:25]
	v_mfma_i32_16x16x64_i8 v[14:17], v[134:137], v[212:215], v[14:17]
	v_mfma_i32_16x16x64_i8 v[6:9], v[142:145], v[212:215], v[6:9]
	v_mfma_i32_16x16x64_i8 v[58:61], v[168:171], v[184:187], v[58:61]
	v_mfma_i32_16x16x64_i8 v[50:53], v[176:179], v[184:187], v[50:53]
	v_mfma_i32_16x16x64_i8 v[42:45], v[168:171], v[192:195], v[42:45]
	v_mfma_i32_16x16x64_i8 v[34:37], v[176:179], v[192:195], v[34:37]
	v_mfma_i32_16x16x64_i8 v[26:29], v[168:171], v[200:203], v[26:29]
	v_mfma_i32_16x16x64_i8 v[18:21], v[176:179], v[200:203], v[18:21]
	v_mfma_i32_16x16x64_i8 v[10:13], v[168:171], v[208:211], v[10:13]
	v_mfma_i32_16x16x64_i8 v[2:5], v[176:179], v[208:211], v[2:5]
	v_mfma_i32_16x16x64_i8 v[58:61], v[172:175], v[188:191], v[58:61]
	v_mfma_i32_16x16x64_i8 v[50:53], v[180:183], v[188:191], v[50:53]
	v_mfma_i32_16x16x64_i8 v[42:45], v[172:175], v[196:199], v[42:45]
	v_mfma_i32_16x16x64_i8 v[34:37], v[180:183], v[196:199], v[34:37]
	v_mfma_i32_16x16x64_i8 v[26:29], v[172:175], v[204:207], v[26:29]
	v_mfma_i32_16x16x64_i8 v[18:21], v[180:183], v[204:207], v[18:21]
	v_mfma_i32_16x16x64_i8 v[10:13], v[172:175], v[212:215], v[10:13]
	v_mfma_i32_16x16x64_i8 v[2:5], v[180:183], v[212:215], v[2:5]
	s_setprio 0
	s_barrier
	s_add_u32 s66, s66, 0x100
	s_addc_u32 s67, s67, 0
	s_add_u32 s24, s24, 0x100
	s_addc_u32 s25, s25, 0
	s_cmp_ge_i32 s68, s54
	s_mov_b32 s26, s68
	s_cbranch_scc0 .LBB0_227

; #define PG8_STAGE(bufoff, gbase, voff) do { _Pragma("unroll") for (int _i = 0; _i < 2; ++_i) \
;         __builtin_amdgcn_global_load_lds((const unsigned*)((const char*)(gbase) + (voff)[_i]), (PG8_LAS unsigned*)(lds + (bufoff) + ldsw + _i * 8192), 16, 0, 0); } while (0)
; #define PG8_LDA(dst, b, h) do { if constexpr (DT != 1) { _Pragma("unroll") for (int m = 0; m < 4; ++m) _Pragma("unroll") for (int k = 0; k < 2; ++k) dst[m][k] = *(const PG8_LAS bf16x8*)(lds + PG8_SA(b, h) + aoff + m * 2048 + k * 1024); } \
;         else { _Pragma("unroll") for (int m = 0; m < 4; ++m) dst##8[m] = ld32(lds + PG8_SA(b, h) + aoff + m * 2048); } } while (0)
; #define PG8_LDB(dst, b, h) do { if constexpr (DT != 1) { _Pragma("unroll") for (int n = 0; n < 2; ++n) _Pragma("unroll") for (int k = 0; k < 2; ++k) dst[n][k] = *(const PG8_LAS bf16x8*)(lds + PG8_SB(b, h) + boff + n * 2048 + k * 1024); } \
;         else { _Pragma("unroll") for (int n = 0; n < 2; ++n) dst##8[n] = ld32(lds + PG8_SB(b, h) + boff + n * 2048); } } while (0)
; #define PG8_WAIT_V(n) asm volatile("s_waitcnt vmcnt(" #n ")" ::: "memory")
; #define PG8_WAIT_L(n) asm volatile("s_waitcnt lgkmcnt(" #n ")" ::: "memory")
; #define PG8_BAR __builtin_amdgcn_s_barrier()
; #define PG8_SCHED __builtin_amdgcn_sched_barrier(0)
;     ...
;             PG8_LDB(B0, 0, 0); PG8_LDB(B1, 0, 1); PG8_SCHED; PG8_LDA(At, 0, 0); PG8_STAGE(PG8_SA(1, 1), a1 + hstepA, voffA);
;             PG8_WAIT_V(8); PG8_WAIT_L(0); PG8_BAR; PG8_MMA(0, 0, At, B0); PG8_MMA(0, 1, At, B1); PG8_BAR; PG8_SCHED;
;             PG8_LDA(At, 0, 1); PG8_STAGE(PG8_SB(0, 0), b2, voffB); PG8_STAGE(PG8_SB(0, 1), b2 + hstepB, voffB); PG8_STAGE(PG8_SA(0, 0), a2, voffA);
;             PG8_WAIT_V(8); PG8_WAIT_L(0); PG8_BAR; PG8_MMA(1, 0, At, B0); PG8_MMA(1, 1, At, B1); PG8_BAR; PG8_SCHED;
.LBB0_303:
	ds_read_b128 v[146:149], v159
	ds_read_b128 v[150:153], v159 offset:1024
	ds_read_b128 v[154:157], v159 offset:2048
	ds_read_b128 v[164:167], v159 offset:3072
	ds_read_b128 v[168:171], v160
	ds_read_b128 v[172:175], v160 offset:1024
	ds_read_b128 v[176:179], v160 offset:2048
	ds_read_b128 v[180:183], v160 offset:3072
	s_add_i32 s69, s34, 2
	s_add_u32 s30, s28, 0x100
	s_addc_u32 s31, s29, 0
	s_cmp_eq_u32 s60, s34
	s_cselect_b32 s34, s26, s67
	s_cselect_b32 s37, s3, s31
	s_cselect_b32 s36, s2, s30
	s_cselect_b32 s35, s27, s68
	v_lshl_add_u64 v[216:217], s[28:29], 0, v[140:141]
	s_add_i32 m0, s48, 0xc000
	ds_read_b128 v[184:187], v161
	ds_read_b128 v[188:191], v161 offset:1024
	ds_read_b128 v[192:195], v161 offset:2048
	ds_read_b128 v[196:199], v161 offset:3072
	ds_read_b128 v[200:203], v161 offset:4096
	ds_read_b128 v[204:207], v161 offset:5120
	ds_read_b128 v[208:211], v161 offset:6144
	ds_read_b128 v[212:215], v161 offset:7168
	global_load_lds_dwordx4 v[216:217], off
	v_lshl_add_u64 v[216:217], s[28:29], 0, v[138:139]
	s_add_i32 m0, s48, 0xe000
	s_nop 0
	global_load_lds_dwordx4 v[216:217], off
	s_waitcnt vmcnt(8)
	s_waitcnt lgkmcnt(0)
	s_barrier
	s_setprio 1
	s_waitcnt lgkmcnt(0)
	v_mfma_f32_16x16x32_bf16 v[126:129], v[146:149], v[184:187], v[126:129]
	v_mfma_f32_16x16x32_bf16 v[122:125], v[154:157], v[184:187], v[122:125]
	v_mfma_f32_16x16x32_bf16 v[118:121], v[146:149], v[192:195], v[118:121]
	v_mfma_f32_16x16x32_bf16 v[114:117], v[154:157], v[192:195], v[114:117]
	v_mfma_f32_16x16x32_bf16 v[106:109], v[146:149], v[200:203], v[106:109]
	v_mfma_f32_16x16x32_bf16 v[98:101], v[154:157], v[200:203], v[98:101]
	v_mfma_f32_16x16x32_bf16 v[90:93], v[146:149], v[208:211], v[90:93]
	v_mfma_f32_16x16x32_bf16 v[82:85], v[154:157], v[208:211], v[82:85]
	v_mfma_f32_16x16x32_bf16 v[126:129], v[150:153], v[188:191], v[126:129]
	v_mfma_f32_16x16x32_bf16 v[122:125], v[164:167], v[188:191], v[122:125]
	v_mfma_f32_16x16x32_bf16 v[118:121], v[150:153], v[196:199], v[118:121]
	v_mfma_f32_16x16x32_bf16 v[114:117], v[164:167], v[196:199], v[114:117]
	v_mfma_f32_16x16x32_bf16 v[106:109], v[150:153], v[204:207], v[106:109]
	v_mfma_f32_16x16x32_bf16 v[98:101], v[164:167], v[204:207], v[98:101]
	v_mfma_f32_16x16x32_bf16 v[90:93], v[150:153], v[212:215], v[90:93]
	v_mfma_f32_16x16x32_bf16 v[82:85], v[164:167], v[212:215], v[82:85]
	v_mfma_f32_16x16x32_bf16 v[110:113], v[168:171], v[184:187], v[110:113]
	v_mfma_f32_16x16x32_bf16 v[102:105], v[176:179], v[184:187], v[102:105]
	v_mfma_f32_16x16x32_bf16 v[94:97], v[168:171], v[192:195], v[94:97]
	v_mfma_f32_16x16x32_bf16 v[86:89], v[176:179], v[192:195], v[86:89]
	v_mfma_f32_16x16x32_bf16 v[78:81], v[168:171], v[200:203], v[78:81]
	v_mfma_f32_16x16x32_bf16 v[74:77], v[176:179], v[200:203], v[74:77]
	v_mfma_f32_16x16x32_bf16 v[70:73], v[168:171], v[208:211], v[70:73]
	v_mfma_f32_16x16x32_bf16 v[66:69], v[176:179], v[208:211], v[66:69]
	v_mfma_f32_16x16x32_bf16 v[110:113], v[172:175], v[188:191], v[110:113]
	v_mfma_f32_16x16x32_bf16 v[102:105], v[180:183], v[188:191], v[102:105]
	v_mfma_f32_16x16x32_bf16 v[94:97], v[172:175], v[196:199], v[94:97]
	v_mfma_f32_16x16x32_bf16 v[86:89], v[180:183], v[196:199], v[86:89]
	v_mfma_f32_16x16x32_bf16 v[78:81], v[172:175], v[204:207], v[78:81]
	v_mfma_f32_16x16x32_bf16 v[74:77], v[180:183], v[204:207], v[74:77]
	v_mfma_f32_16x16x32_bf16 v[70:73], v[172:175], v[212:215], v[70:73]
	v_mfma_f32_16x16x32_bf16 v[66:69], v[180:183], v[212:215], v[66:69]
	s_setprio 0
	s_barrier
	s_mov_b32 m0, s44
	s_add_u32 s98, s34, 0x80
	s_addc_u32 s99, s35, 0
	s_add_u32 s28, s34, 0x160000
	ds_read_b128 v[184:187], v161 offset:16384
	ds_read_b128 v[188:191], v161 offset:17408
	ds_read_b128 v[192:195], v161 offset:18432
	ds_read_b128 v[196:199], v161 offset:19456
	ds_read_b128 v[200:203], v161 offset:20480
	ds_read_b128 v[204:207], v161 offset:21504
	ds_read_b128 v[208:211], v161 offset:22528
	ds_read_b128 v[212:215], v161 offset:23552
	global_load_lds_dwordx4 v132, s[34:35]
	s_mov_b32 m0, s45
	s_addc_u32 s29, s35, 0
	global_load_lds_dwordx4 v136, s[34:35]
	s_mov_b32 m0, s46
	s_nop 0
	global_load_lds_dwordx4 v132, s[28:29]
	s_mov_b32 m0, s47
	s_nop 0
	global_load_lds_dwordx4 v136, s[28:29]
	s_add_u32 s100, s36, 0x80
	s_addc_u32 s101, s37, 0
	s_mov_b32 m0, s48
	s_nop 0
	global_load_lds_dwordx4 v130, s[36:37]
	s_mov_b32 m0, s49
	s_nop 0
	global_load_lds_dwordx4 v134, s[36:37]
	s_waitcnt vmcnt(8)
	s_waitcnt lgkmcnt(0)
	s_barrier
	s_setprio 1
	s_waitcnt lgkmcnt(0)
	v_mfma_f32_16x16x32_bf16 v[62:65], v[146:149], v[184:187], v[62:65]
	v_mfma_f32_16x16x32_bf16 v[58:61], v[154:157], v[184:187], v[58:61]
	v_mfma_f32_16x16x32_bf16 v[54:57], v[146:149], v[192:195], v[54:57]
	v_mfma_f32_16x16x32_bf16 v[50:53], v[154:157], v[192:195], v[50:53]
	v_mfma_f32_16x16x32_bf16 v[42:45], v[146:149], v[200:203], v[42:45]
	v_mfma_f32_16x16x32_bf16 v[34:37], v[154:157], v[200:203], v[34:37]
	v_mfma_f32_16x16x32_bf16 v[26:29], v[146:149], v[208:211], v[26:29]
	v_mfma_f32_16x16x32_bf16 v[18:21], v[154:157], v[208:211], v[18:21]
	v_mfma_f32_16x16x32_bf16 v[62:65], v[150:153], v[188:191], v[62:65]
	v_mfma_f32_16x16x32_bf16 v[58:61], v[164:167], v[188:191], v[58:61]
	v_mfma_f32_16x16x32_bf16 v[54:57], v[150:153], v[196:199], v[54:57]
	v_mfma_f32_16x16x32_bf16 v[50:53], v[164:167], v[196:199], v[50:53]
	v_mfma_f32_16x16x32_bf16 v[42:45], v[150:153], v[204:207], v[42:45]
	v_mfma_f32_16x16x32_bf16 v[34:37], v[164:167], v[204:207], v[34:37]
	v_mfma_f32_16x16x32_bf16 v[26:29], v[150:153], v[212:215], v[26:29]
	v_mfma_f32_16x16x32_bf16 v[18:21], v[164:167], v[212:215], v[18:21]
	v_mfma_f32_16x16x32_bf16 v[46:49], v[168:171], v[184:187], v[46:49]
	v_mfma_f32_16x16x32_bf16 v[38:41], v[176:179], v[184:187], v[38:41]
	v_mfma_f32_16x16x32_bf16 v[30:33], v[168:171], v[192:195], v[30:33]
	v_mfma_f32_16x16x32_bf16 v[22:25], v[176:179], v[192:195], v[22:25]
	v_mfma_f32_16x16x32_bf16 v[14:17], v[168:171], v[200:203], v[14:17]
	v_mfma_f32_16x16x32_bf16 v[10:13], v[176:179], v[200:203], v[10:13]
	v_mfma_f32_16x16x32_bf16 v[6:9], v[168:171], v[208:211], v[6:9]
	v_mfma_f32_16x16x32_bf16 v[2:5], v[176:179], v[208:211], v[2:5]
	v_mfma_f32_16x16x32_bf16 v[46:49], v[172:175], v[188:191], v[46:49]
	v_mfma_f32_16x16x32_bf16 v[38:41], v[180:183], v[188:191], v[38:41]
	v_mfma_f32_16x16x32_bf16 v[30:33], v[172:175], v[196:199], v[30:33]
	v_mfma_f32_16x16x32_bf16 v[22:25], v[180:183], v[196:199], v[22:25]
	v_mfma_f32_16x16x32_bf16 v[14:17], v[172:175], v[204:207], v[14:17]
	v_mfma_f32_16x16x32_bf16 v[10:13], v[180:183], v[204:207], v[10:13]
	v_mfma_f32_16x16x32_bf16 v[6:9], v[172:175], v[212:215], v[6:9]
	v_mfma_f32_16x16x32_bf16 v[2:5], v[180:183], v[212:215], v[2:5]
	s_setprio 0
	s_barrier
; #define PG8_STAGE(bufoff, gbase, voff) do { _Pragma("unroll") for (int _i = 0; _i < 2; ++_i) \
;         __builtin_amdgcn_global_load_lds((const unsigned*)((const char*)(gbase) + (voff)[_i]), (PG8_LAS unsigned*)(lds + (bufoff) + ldsw + _i * 8192), 16, 0, 0); } while (0)
; #define PG8_LDA(dst, b, h) do { if constexpr (DT != 1) { _Pragma("unroll") for (int m = 0; m < 4; ++m) _Pragma("unroll") for (int k = 0; k < 2; ++k) dst[m][k] = *(const PG8_LAS bf16x8*)(lds + PG8_SA(b, h) + aoff + m * 2048 + k * 1024); } \
;         else { _Pragma("unroll") for (int m = 0; m < 4; ++m) dst##8[m] = ld32(lds + PG8_SA(b, h) + aoff + m * 2048); } } while (0)
; #define PG8_LDB(dst, b, h) do { if constexpr (DT != 1) { _Pragma("unroll") for (int n = 0; n < 2; ++n) _Pragma("unroll") for (int k = 0; k < 2; ++k) dst[n][k] = *(const PG8_LAS bf16x8*)(lds + PG8_SB(b, h) + boff + n * 2048 + k * 1024); } \
;         else { _Pragma("unroll") for (int n = 0; n < 2; ++n) dst##8[n] = ld32(lds + PG8_SB(b, h) + boff + n * 2048); } } while (0)
; #define PG8_WAIT_V(n) asm volatile("s_waitcnt vmcnt(" #n ")" ::: "memory")
; #define PG8_WAIT_L(n) asm volatile("s_waitcnt lgkmcnt(" #n ")" ::: "memory")
; #define PG8_BAR __builtin_amdgcn_s_barrier()
; #define PG8_SCHED __builtin_amdgcn_sched_barrier(0)
;     ...
;             PG8_LDB(B0, 1, 0); PG8_LDB(B1, 1, 1); PG8_SCHED; PG8_LDA(At, 1, 0); PG8_STAGE(PG8_SA(0, 1), a2 + hstepA, voffA);
;             PG8_WAIT_V(8); PG8_WAIT_L(0); PG8_BAR; PG8_MMA(0, 0, At, B0); PG8_MMA(0, 1, At, B1); PG8_BAR; PG8_SCHED;
;             PG8_LDA(At, 1, 1); PG8_STAGE(PG8_SB(1, 0), b3, voffB); PG8_STAGE(PG8_SB(1, 1), b3 + hstepB, voffB); PG8_STAGE(PG8_SA(1, 0), a3, voffA);
;             PG8_WAIT_V(8); PG8_WAIT_L(0); PG8_BAR; PG8_MMA(1, 0, At, B0); PG8_MMA(1, 1, At, B1); PG8_BAR; PG8_SCHED;
	ds_read_b128 v[146:149], v162
	ds_read_b128 v[150:153], v162 offset:1024
	ds_read_b128 v[154:157], v162 offset:2048
	ds_read_b128 v[164:167], v162 offset:3072
	ds_read_b128 v[168:171], v163
	ds_read_b128 v[172:175], v163 offset:1024
	ds_read_b128 v[176:179], v163 offset:2048
	ds_read_b128 v[180:183], v163 offset:3072
	s_add_u32 s28, s36, 0x160000
	s_addc_u32 s29, s37, 0
	s_mov_b32 m0, s50
	ds_read_b128 v[184:187], v161 offset:32768
	ds_read_b128 v[188:191], v161 offset:33792
	ds_read_b128 v[192:195], v161 offset:34816
	ds_read_b128 v[196:199], v161 offset:35840
	ds_read_b128 v[200:203], v161 offset:36864
	ds_read_b128 v[204:207], v161 offset:37888
	ds_read_b128 v[208:211], v161 offset:38912
	ds_read_b128 v[212:215], v161 offset:39936
	global_load_lds_dwordx4 v130, s[28:29]
	s_mov_b32 m0, s51
	s_nop 0
	global_load_lds_dwordx4 v134, s[28:29]
	s_waitcnt vmcnt(8)
	s_waitcnt lgkmcnt(0)
	s_barrier
	s_setprio 1
	s_waitcnt lgkmcnt(0)
	v_mfma_f32_16x16x32_bf16 v[126:129], v[146:149], v[184:187], v[126:129]
	v_mfma_f32_16x16x32_bf16 v[122:125], v[154:157], v[184:187], v[122:125]
	v_mfma_f32_16x16x32_bf16 v[118:121], v[146:149], v[192:195], v[118:121]
	v_mfma_f32_16x16x32_bf16 v[114:117], v[154:157], v[192:195], v[114:117]
	v_mfma_f32_16x16x32_bf16 v[106:109], v[146:149], v[200:203], v[106:109]
	v_mfma_f32_16x16x32_bf16 v[98:101], v[154:157], v[200:203], v[98:101]
	v_mfma_f32_16x16x32_bf16 v[90:93], v[146:149], v[208:211], v[90:93]
	v_mfma_f32_16x16x32_bf16 v[82:85], v[154:157], v[208:211], v[82:85]
	v_mfma_f32_16x16x32_bf16 v[126:129], v[150:153], v[188:191], v[126:129]
	v_mfma_f32_16x16x32_bf16 v[122:125], v[164:167], v[188:191], v[122:125]
	v_mfma_f32_16x16x32_bf16 v[118:121], v[150:153], v[196:199], v[118:121]
	v_mfma_f32_16x16x32_bf16 v[114:117], v[164:167], v[196:199], v[114:117]
	v_mfma_f32_16x16x32_bf16 v[106:109], v[150:153], v[204:207], v[106:109]
	v_mfma_f32_16x16x32_bf16 v[98:101], v[164:167], v[204:207], v[98:101]
	v_mfma_f32_16x16x32_bf16 v[90:93], v[150:153], v[212:215], v[90:93]
	v_mfma_f32_16x16x32_bf16 v[82:85], v[164:167], v[212:215], v[82:85]
	v_mfma_f32_16x16x32_bf16 v[110:113], v[168:171], v[184:187], v[110:113]
	v_mfma_f32_16x16x32_bf16 v[102:105], v[176:179], v[184:187], v[102:105]
	v_mfma_f32_16x16x32_bf16 v[94:97], v[168:171], v[192:195], v[94:97]
	v_mfma_f32_16x16x32_bf16 v[86:89], v[176:179], v[192:195], v[86:89]
	v_mfma_f32_16x16x32_bf16 v[78:81], v[168:171], v[200:203], v[78:81]
	v_mfma_f32_16x16x32_bf16 v[74:77], v[176:179], v[200:203], v[74:77]
	v_mfma_f32_16x16x32_bf16 v[70:73], v[168:171], v[208:211], v[70:73]
	v_mfma_f32_16x16x32_bf16 v[66:69], v[176:179], v[208:211], v[66:69]
	v_mfma_f32_16x16x32_bf16 v[110:113], v[172:175], v[188:191], v[110:113]
	v_mfma_f32_16x16x32_bf16 v[102:105], v[180:183], v[188:191], v[102:105]
	v_mfma_f32_16x16x32_bf16 v[94:97], v[172:175], v[196:199], v[94:97]
	v_mfma_f32_16x16x32_bf16 v[86:89], v[180:183], v[196:199], v[86:89]
	v_mfma_f32_16x16x32_bf16 v[78:81], v[172:175], v[204:207], v[78:81]
	v_mfma_f32_16x16x32_bf16 v[74:77], v[180:183], v[204:207], v[74:77]
	v_mfma_f32_16x16x32_bf16 v[70:73], v[172:175], v[212:215], v[70:73]
	v_mfma_f32_16x16x32_bf16 v[66:69], v[180:183], v[212:215], v[66:69]
	s_setprio 0
	s_barrier
	s_mov_b32 m0, s54
	s_add_u32 s28, s34, 0x160080
	ds_read_b128 v[184:187], v161 offset:49152
	ds_read_b128 v[188:191], v161 offset:50176
	ds_read_b128 v[192:195], v161 offset:51200
	ds_read_b128 v[196:199], v161 offset:52224
	ds_read_b128 v[200:203], v161 offset:53248
	ds_read_b128 v[204:207], v161 offset:54272
	ds_read_b128 v[208:211], v161 offset:55296
	ds_read_b128 v[212:215], v161 offset:56320
	global_load_lds_dwordx4 v132, s[98:99]
	s_mov_b32 m0, s55
	s_addc_u32 s29, s35, 0
	global_load_lds_dwordx4 v136, s[98:99]
	s_mov_b32 m0, s58
	s_nop 0
	global_load_lds_dwordx4 v132, s[28:29]
	s_mov_b32 m0, s59
	s_nop 0
	global_load_lds_dwordx4 v136, s[28:29]
	s_mov_b32 m0, s56
	s_nop 0
	global_load_lds_dwordx4 v130, s[100:101]
	s_mov_b32 m0, s57
	s_nop 0
	global_load_lds_dwordx4 v134, s[100:101]
	s_waitcnt vmcnt(8)
	s_waitcnt lgkmcnt(0)
	s_barrier
; #define PG8_WAIT_V(n) asm volatile("s_waitcnt vmcnt(" #n ")" ::: "memory")
; #define PG8_WAIT_L(n) asm volatile("s_waitcnt lgkmcnt(" #n ")" ::: "memory")
; #define PG8_BAR __builtin_amdgcn_s_barrier()
; #define PG8_SCHED __builtin_amdgcn_sched_barrier(0)
;     __device__ __forceinline__ void operator()(const f32x4 (&acc)[2][2][4][2], const Unit& u, int wr, int wc, int fr, int fq) const {
;     ...
;                 for (int m = 0; m < 4; ++m) { const size_t off = (size_t)(row0 + ai * HALF + m * 16) * ldc + col0;
; #pragma unroll
;                     for (int bj = 0; bj < 2; ++bj) { const h16x8_t w = wv[m][bj];
;                         const f32x4 b0 = (f32x4){(float)w[0], (float)w[1], (float)w[2], (float)w[3]}, b1 = (f32x4){(float)w[4], (float)w[5], (float)w[6], (float)w[7]};
;                         const f32x4 o0 = b0 + acc[ai][bj][m][0] * s, o1 = b1 + acc[ai][bj][m][1] * s;
;     ...
;             PG8_WAIT_V(8); PG8_WAIT_L(0); PG8_BAR; PG8_MMA(1, 0, At, B0); PG8_MMA(1, 1, At, B1); PG8_BAR; PG8_SCHED;
	s_setprio 1
	s_waitcnt lgkmcnt(0)
	v_mfma_f32_16x16x32_bf16 v[62:65], v[146:149], v[184:187], v[62:65]
	v_mfma_f32_16x16x32_bf16 v[58:61], v[154:157], v[184:187], v[58:61]
	v_mfma_f32_16x16x32_bf16 v[54:57], v[146:149], v[192:195], v[54:57]
	v_mfma_f32_16x16x32_bf16 v[50:53], v[154:157], v[192:195], v[50:53]
	v_mfma_f32_16x16x32_bf16 v[42:45], v[146:149], v[200:203], v[42:45]
	v_mfma_f32_16x16x32_bf16 v[34:37], v[154:157], v[200:203], v[34:37]
	v_mfma_f32_16x16x32_bf16 v[26:29], v[146:149], v[208:211], v[26:29]
	v_mfma_f32_16x16x32_bf16 v[18:21], v[154:157], v[208:211], v[18:21]
	v_mfma_f32_16x16x32_bf16 v[62:65], v[150:153], v[188:191], v[62:65]
	v_mfma_f32_16x16x32_bf16 v[58:61], v[164:167], v[188:191], v[58:61]
	v_mfma_f32_16x16x32_bf16 v[54:57], v[150:153], v[196:199], v[54:57]
	v_mfma_f32_16x16x32_bf16 v[50:53], v[164:167], v[196:199], v[50:53]
	v_mfma_f32_16x16x32_bf16 v[42:45], v[150:153], v[204:207], v[42:45]
	v_mfma_f32_16x16x32_bf16 v[34:37], v[164:167], v[204:207], v[34:37]
	v_mfma_f32_16x16x32_bf16 v[26:29], v[150:153], v[212:215], v[26:29]
	v_mfma_f32_16x16x32_bf16 v[18:21], v[164:167], v[212:215], v[18:21]
	v_mfma_f32_16x16x32_bf16 v[46:49], v[168:171], v[184:187], v[46:49]
	v_mfma_f32_16x16x32_bf16 v[38:41], v[176:179], v[184:187], v[38:41]
	v_mfma_f32_16x16x32_bf16 v[30:33], v[168:171], v[192:195], v[30:33]
	v_mfma_f32_16x16x32_bf16 v[22:25], v[176:179], v[192:195], v[22:25]
	v_mfma_f32_16x16x32_bf16 v[14:17], v[168:171], v[200:203], v[14:17]
	v_mfma_f32_16x16x32_bf16 v[10:13], v[176:179], v[200:203], v[10:13]
	v_mfma_f32_16x16x32_bf16 v[6:9], v[168:171], v[208:211], v[6:9]
	v_mfma_f32_16x16x32_bf16 v[2:5], v[176:179], v[208:211], v[2:5]
	v_mfma_f32_16x16x32_bf16 v[46:49], v[172:175], v[188:191], v[46:49]
	v_mfma_f32_16x16x32_bf16 v[38:41], v[180:183], v[188:191], v[38:41]
	v_mfma_f32_16x16x32_bf16 v[30:33], v[172:175], v[196:199], v[30:33]
	v_mfma_f32_16x16x32_bf16 v[22:25], v[180:183], v[196:199], v[22:25]
	v_mfma_f32_16x16x32_bf16 v[14:17], v[172:175], v[204:207], v[14:17]
	v_mfma_f32_16x16x32_bf16 v[10:13], v[180:183], v[204:207], v[10:13]
	v_mfma_f32_16x16x32_bf16 v[6:9], v[172:175], v[212:215], v[6:9]
	v_mfma_f32_16x16x32_bf16 v[2:5], v[180:183], v[212:215], v[2:5]
	s_setprio 0
	s_barrier
	s_add_u32 s67, s67, 0x100
	s_addc_u32 s68, s68, 0
	s_cmp_ge_i32 s69, s53
	s_mov_b64 s[28:29], s[30:31]
	s_mov_b32 s34, s69
	s_cbranch_scc0 .LBB0_303
	v_pk_mul_f32 v[128:129], v[128:129], 0.5 op_sel_hi:[1,0]
	v_pk_mul_f32 v[126:127], v[126:127], 0.5 op_sel_hi:[1,0]
	v_pk_mul_f32 v[146:147], v[124:125], 0.5 op_sel_hi:[1,0]
	v_pk_mul_f32 v[148:149], v[122:123], 0.5 op_sel_hi:[1,0]
	v_pk_mul_f32 v[150:151], v[112:113], 0.5 op_sel_hi:[1,0]
	v_pk_mul_f32 v[152:153], v[110:111], 0.5 op_sel_hi:[1,0]
	v_pk_mul_f32 v[154:155], v[104:105], 0.5 op_sel_hi:[1,0]
	v_pk_mul_f32 v[156:157], v[102:103], 0.5 op_sel_hi:[1,0]
	v_pk_mul_f32 v[110:111], v[120:121], 0.5 op_sel_hi:[1,0]
	v_pk_mul_f32 v[112:113], v[118:119], 0.5 op_sel_hi:[1,0]
	v_pk_mul_f32 v[116:117], v[116:117], 0.5 op_sel_hi:[1,0]
	v_pk_mul_f32 v[114:115], v[114:115], 0.5 op_sel_hi:[1,0]
	v_pk_mul_f32 v[118:119], v[96:97], 0.5 op_sel_hi:[1,0]
	v_pk_mul_f32 v[120:121], v[94:95], 0.5 op_sel_hi:[1,0]
	v_pk_mul_f32 v[122:123], v[88:89], 0.5 op_sel_hi:[1,0]
	v_pk_mul_f32 v[124:125], v[86:87], 0.5 op_sel_hi:[1,0]
	v_pk_mul_f32 v[94:95], v[108:109], 0.5 op_sel_hi:[1,0]
	v_pk_mul_f32 v[96:97], v[106:107], 0.5 op_sel_hi:[1,0]
	v_pk_mul_f32 v[100:101], v[100:101], 0.5 op_sel_hi:[1,0]
	v_pk_mul_f32 v[98:99], v[98:99], 0.5 op_sel_hi:[1,0]
	v_pk_mul_f32 v[102:103], v[80:81], 0.5 op_sel_hi:[1,0]
	v_pk_mul_f32 v[104:105], v[78:79], 0.5 op_sel_hi:[1,0]
	v_pk_mul_f32 v[106:107], v[76:77], 0.5 op_sel_hi:[1,0]
	v_pk_mul_f32 v[108:109], v[74:75], 0.5 op_sel_hi:[1,0]
	v_pk_mul_f32 v[74:75], v[92:93], 0.5 op_sel_hi:[1,0]
	v_pk_mul_f32 v[76:77], v[90:91], 0.5 op_sel_hi:[1,0]
	v_pk_mul_f32 v[78:79], v[84:85], 0.5 op_sel_hi:[1,0]
	v_pk_mul_f32 v[80:81], v[82:83], 0.5 op_sel_hi:[1,0]
	v_pk_mul_f32 v[86:87], v[72:73], 0.5 op_sel_hi:[1,0]
	v_pk_mul_f32 v[88:89], v[70:71], 0.5 op_sel_hi:[1,0]
	v_pk_mul_f32 v[90:91], v[68:69], 0.5 op_sel_hi:[1,0]
	v_pk_mul_f32 v[92:93], v[66:67], 0.5 op_sel_hi:[1,0]
	v_pk_mul_f32 v[64:65], v[64:65], 0.5 op_sel_hi:[1,0]
	v_pk_mul_f32 v[62:63], v[62:63], 0.5 op_sel_hi:[1,0]
	v_pk_mul_f32 v[66:67], v[60:61], 0.5 op_sel_hi:[1,0]
	v_pk_mul_f32 v[68:69], v[58:59], 0.5 op_sel_hi:[1,0]
	v_pk_mul_f32 v[70:71], v[48:49], 0.5 op_sel_hi:[1,0]
	v_pk_mul_f32 v[72:73], v[46:47], 0.5 op_sel_hi:[1,0]
	v_pk_mul_f32 v[82:83], v[40:41], 0.5 op_sel_hi:[1,0]
	v_pk_mul_f32 v[84:85], v[38:39], 0.5 op_sel_hi:[1,0]
	v_pk_mul_f32 v[46:47], v[56:57], 0.5 op_sel_hi:[1,0]
	v_pk_mul_f32 v[48:49], v[54:55], 0.5 op_sel_hi:[1,0]
	v_pk_mul_f32 v[52:53], v[52:53], 0.5 op_sel_hi:[1,0]
	v_pk_mul_f32 v[50:51], v[50:51], 0.5 op_sel_hi:[1,0]
	v_pk_mul_f32 v[54:55], v[32:33], 0.5 op_sel_hi:[1,0]
	v_pk_mul_f32 v[56:57], v[30:31], 0.5 op_sel_hi:[1,0]
	v_pk_mul_f32 v[58:59], v[24:25], 0.5 op_sel_hi:[1,0]
	v_pk_mul_f32 v[60:61], v[22:23], 0.5 op_sel_hi:[1,0]
	v_pk_mul_f32 v[22:23], v[44:45], 0.5 op_sel_hi:[1,0]
	v_pk_mul_f32 v[24:25], v[42:43], 0.5 op_sel_hi:[1,0]
	v_pk_mul_f32 v[30:31], v[36:37], 0.5 op_sel_hi:[1,0]
	v_pk_mul_f32 v[32:33], v[34:35], 0.5 op_sel_hi:[1,0]
	v_pk_mul_f32 v[34:35], v[16:17], 0.5 op_sel_hi:[1,0]
	v_pk_mul_f32 v[36:37], v[14:15], 0.5 op_sel_hi:[1,0]
	v_pk_mul_f32 v[38:39], v[12:13], 0.5 op_sel_hi:[1,0]
	v_pk_mul_f32 v[40:41], v[10:11], 0.5 op_sel_hi:[1,0]
	v_pk_mul_f32 v[10:11], v[28:29], 0.5 op_sel_hi:[1,0]
	v_pk_mul_f32 v[12:13], v[26:27], 0.5 op_sel_hi:[1,0]
	v_pk_mul_f32 v[14:15], v[20:21], 0.5 op_sel_hi:[1,0]
	v_pk_mul_f32 v[16:17], v[18:19], 0.5 op_sel_hi:[1,0]
	v_pk_mul_f32 v[8:9], v[8:9], 0.5 op_sel_hi:[1,0]
	v_pk_mul_f32 v[6:7], v[6:7], 0.5 op_sel_hi:[1,0]
	v_pk_mul_f32 v[4:5], v[4:5], 0.5 op_sel_hi:[1,0]
	v_pk_mul_f32 v[2:3], v[2:3], 0.5 op_sel_hi:[1,0]

; #define PG8_STAGE(bufoff, gbase, voff) do { _Pragma("unroll") for (int _i = 0; _i < 2; ++_i) \
;         __builtin_amdgcn_global_load_lds((const unsigned*)((const char*)(gbase) + (voff)[_i]), (PG8_LAS unsigned*)(lds + (bufoff) + ldsw + _i * 8192), 16, 0, 0); } while (0)
; #define PG8_LDA(dst, b, h) do { if constexpr (DT != 1) { _Pragma("unroll") for (int m = 0; m < 4; ++m) _Pragma("unroll") for (int k = 0; k < 2; ++k) dst[m][k] = *(const PG8_LAS bf16x8*)(lds + PG8_SA(b, h) + aoff + m * 2048 + k * 1024); } \
;         else { _Pragma("unroll") for (int m = 0; m < 4; ++m) dst##8[m] = ld32(lds + PG8_SA(b, h) + aoff + m * 2048); } } while (0)
; #define PG8_LDB(dst, b, h) do { if constexpr (DT != 1) { _Pragma("unroll") for (int n = 0; n < 2; ++n) _Pragma("unroll") for (int k = 0; k < 2; ++k) dst[n][k] = *(const PG8_LAS bf16x8*)(lds + PG8_SB(b, h) + boff + n * 2048 + k * 1024); } \
;         else { _Pragma("unroll") for (int n = 0; n < 2; ++n) dst##8[n] = ld32(lds + PG8_SB(b, h) + boff + n * 2048); } } while (0)
; #define PG8_WAIT_V(n) asm volatile("s_waitcnt vmcnt(" #n ")" ::: "memory")
; #define PG8_WAIT_L(n) asm volatile("s_waitcnt lgkmcnt(" #n ")" ::: "memory")
; #define PG8_BAR __builtin_amdgcn_s_barrier()
; #define PG8_SCHED __builtin_amdgcn_sched_barrier(0)
;     ...
;             PG8_LDB(B0, 0, 0); PG8_LDB(B1, 0, 1); PG8_SCHED; PG8_LDA(At, 0, 0); PG8_STAGE(PG8_SA(1, 1), a1 + hstepA, voffA);
;             PG8_WAIT_V(8); PG8_WAIT_L(0); PG8_BAR; PG8_MMA(0, 0, At, B0); PG8_MMA(0, 1, At, B1); PG8_BAR; PG8_SCHED;
;             PG8_LDA(At, 0, 1); PG8_STAGE(PG8_SB(0, 0), b2, voffB); PG8_STAGE(PG8_SB(0, 1), b2 + hstepB, voffB); PG8_STAGE(PG8_SA(0, 0), a2, voffA);
;             PG8_WAIT_V(8); PG8_WAIT_L(0); PG8_BAR; PG8_MMA(1, 0, At, B0); PG8_MMA(1, 1, At, B1); PG8_BAR; PG8_SCHED;
.LBB0_418:
	ds_read_b128 v[156:159], v150
	ds_read_b128 v[160:163], v150 offset:1024
	ds_read_b128 v[164:167], v150 offset:2048
	ds_read_b128 v[168:171], v150 offset:3072
	ds_read_b128 v[172:175], v151
	ds_read_b128 v[176:179], v151 offset:1024
	ds_read_b128 v[180:183], v151 offset:2048
	ds_read_b128 v[184:187], v151 offset:3072
	s_add_i32 s65, s28, 2
	s_add_u32 s29, s26, 0xfff80080
	s_addc_u32 s30, s27, -1
	s_cmp_eq_u32 s59, s28
	s_cselect_b32 s28, s62, s63
	s_cselect_b32 s31, s19, s30
	s_cselect_b32 s30, s21, s29
	s_cselect_b32 s29, s61, s64
	s_add_i32 m0, s45, 0xc000
	ds_read_b128 v[188:191], v152
	ds_read_b128 v[192:195], v152 offset:1024
	ds_read_b128 v[196:199], v152 offset:2048
	ds_read_b128 v[200:203], v152 offset:3072
	ds_read_b128 v[204:207], v152 offset:4096
	ds_read_b128 v[208:211], v152 offset:5120
	ds_read_b128 v[212:215], v152 offset:6144
	ds_read_b128 v[216:219], v152 offset:7168
	global_load_lds_dwordx4 v144, s[26:27]
	s_add_i32 m0, s45, 0xe000
	s_nop 0
	global_load_lds_dwordx4 v142, s[26:27]
	s_waitcnt vmcnt(8)
	s_waitcnt lgkmcnt(0)
	s_barrier
	s_setprio 1
	s_waitcnt lgkmcnt(0)
	v_mfma_f32_16x16x32_bf16 v[122:125], v[156:159], v[188:191], v[122:125]
	v_mfma_f32_16x16x32_bf16 v[126:129], v[164:167], v[188:191], v[126:129]
	v_mfma_f32_16x16x32_bf16 v[110:113], v[156:159], v[196:199], v[110:113]
	v_mfma_f32_16x16x32_bf16 v[106:109], v[164:167], v[196:199], v[106:109]
	v_mfma_f32_16x16x32_bf16 v[94:97], v[156:159], v[204:207], v[94:97]
	v_mfma_f32_16x16x32_bf16 v[90:93], v[164:167], v[204:207], v[90:93]
	v_mfma_f32_16x16x32_bf16 v[78:81], v[156:159], v[212:215], v[78:81]
	v_mfma_f32_16x16x32_bf16 v[74:77], v[164:167], v[212:215], v[74:77]
	v_mfma_f32_16x16x32_bf16 v[122:125], v[160:163], v[192:195], v[122:125]
	v_mfma_f32_16x16x32_bf16 v[126:129], v[168:171], v[192:195], v[126:129]
	v_mfma_f32_16x16x32_bf16 v[110:113], v[160:163], v[200:203], v[110:113]
	v_mfma_f32_16x16x32_bf16 v[106:109], v[168:171], v[200:203], v[106:109]
	v_mfma_f32_16x16x32_bf16 v[94:97], v[160:163], v[208:211], v[94:97]
	v_mfma_f32_16x16x32_bf16 v[90:93], v[168:171], v[208:211], v[90:93]
	v_mfma_f32_16x16x32_bf16 v[78:81], v[160:163], v[216:219], v[78:81]
	v_mfma_f32_16x16x32_bf16 v[74:77], v[168:171], v[216:219], v[74:77]
	v_mfma_f32_16x16x32_bf16 v[118:121], v[172:175], v[188:191], v[118:121]
	v_mfma_f32_16x16x32_bf16 v[114:117], v[180:183], v[188:191], v[114:117]
	v_mfma_f32_16x16x32_bf16 v[102:105], v[172:175], v[196:199], v[102:105]
	v_mfma_f32_16x16x32_bf16 v[98:101], v[180:183], v[196:199], v[98:101]
	v_mfma_f32_16x16x32_bf16 v[86:89], v[172:175], v[204:207], v[86:89]
	v_mfma_f32_16x16x32_bf16 v[82:85], v[180:183], v[204:207], v[82:85]
	v_mfma_f32_16x16x32_bf16 v[70:73], v[172:175], v[212:215], v[70:73]
	v_mfma_f32_16x16x32_bf16 v[66:69], v[180:183], v[212:215], v[66:69]
	v_mfma_f32_16x16x32_bf16 v[118:121], v[176:179], v[192:195], v[118:121]
	v_mfma_f32_16x16x32_bf16 v[114:117], v[184:187], v[192:195], v[114:117]
	v_mfma_f32_16x16x32_bf16 v[102:105], v[176:179], v[200:203], v[102:105]
	v_mfma_f32_16x16x32_bf16 v[98:101], v[184:187], v[200:203], v[98:101]
	v_mfma_f32_16x16x32_bf16 v[86:89], v[176:179], v[208:211], v[86:89]
	v_mfma_f32_16x16x32_bf16 v[82:85], v[184:187], v[208:211], v[82:85]
	v_mfma_f32_16x16x32_bf16 v[70:73], v[176:179], v[216:219], v[70:73]
	v_mfma_f32_16x16x32_bf16 v[66:69], v[184:187], v[216:219], v[66:69]
	s_setprio 0
	s_barrier
	s_mov_b32 m0, s41
	s_add_u32 s98, s28, 0x80
	s_addc_u32 s99, s29, 0
	s_add_u32 s66, s28, 0x80000
	ds_read_b128 v[188:191], v152 offset:16384
	ds_read_b128 v[192:195], v152 offset:17408
	ds_read_b128 v[196:199], v152 offset:18432
	ds_read_b128 v[200:203], v152 offset:19456
	ds_read_b128 v[204:207], v152 offset:20480
	ds_read_b128 v[208:211], v152 offset:21504
	ds_read_b128 v[212:215], v152 offset:22528
	ds_read_b128 v[216:219], v152 offset:23552
	global_load_lds_dwordx4 v132, s[28:29]
	s_mov_b32 m0, s42
	s_addc_u32 s67, s29, 0
	global_load_lds_dwordx4 v136, s[28:29]
	s_mov_b32 m0, s43
	s_nop 0
	global_load_lds_dwordx4 v132, s[66:67]
	s_mov_b32 m0, s44
	s_nop 0
	global_load_lds_dwordx4 v136, s[66:67]
	s_add_u32 s100, s30, 0x80
	s_addc_u32 s101, s31, 0
	s_mov_b32 m0, s45
	s_nop 0
	global_load_lds_dwordx4 v130, s[30:31]
	s_mov_b32 m0, s46
	s_nop 0
	global_load_lds_dwordx4 v134, s[30:31]
	s_waitcnt vmcnt(8)
	s_waitcnt lgkmcnt(0)
	s_barrier
	s_setprio 1
	s_waitcnt lgkmcnt(0)
	v_mfma_f32_16x16x32_bf16 v[62:65], v[156:159], v[188:191], v[62:65]
	v_mfma_f32_16x16x32_bf16 v[58:61], v[164:167], v[188:191], v[58:61]
	v_mfma_f32_16x16x32_bf16 v[46:49], v[156:159], v[196:199], v[46:49]
	v_mfma_f32_16x16x32_bf16 v[42:45], v[164:167], v[196:199], v[42:45]
	v_mfma_f32_16x16x32_bf16 v[30:33], v[156:159], v[204:207], v[30:33]
	v_mfma_f32_16x16x32_bf16 v[26:29], v[164:167], v[204:207], v[26:29]
	v_mfma_f32_16x16x32_bf16 v[14:17], v[156:159], v[212:215], v[14:17]
	v_mfma_f32_16x16x32_bf16 v[10:13], v[164:167], v[212:215], v[10:13]
	v_mfma_f32_16x16x32_bf16 v[62:65], v[160:163], v[192:195], v[62:65]
	v_mfma_f32_16x16x32_bf16 v[58:61], v[168:171], v[192:195], v[58:61]
	v_mfma_f32_16x16x32_bf16 v[46:49], v[160:163], v[200:203], v[46:49]
	v_mfma_f32_16x16x32_bf16 v[42:45], v[168:171], v[200:203], v[42:45]
	v_mfma_f32_16x16x32_bf16 v[30:33], v[160:163], v[208:211], v[30:33]
	v_mfma_f32_16x16x32_bf16 v[26:29], v[168:171], v[208:211], v[26:29]
	v_mfma_f32_16x16x32_bf16 v[14:17], v[160:163], v[216:219], v[14:17]
	v_mfma_f32_16x16x32_bf16 v[10:13], v[168:171], v[216:219], v[10:13]
	v_mfma_f32_16x16x32_bf16 v[54:57], v[172:175], v[188:191], v[54:57]
	v_mfma_f32_16x16x32_bf16 v[50:53], v[180:183], v[188:191], v[50:53]
	v_mfma_f32_16x16x32_bf16 v[38:41], v[172:175], v[196:199], v[38:41]
	v_mfma_f32_16x16x32_bf16 v[34:37], v[180:183], v[196:199], v[34:37]
	v_mfma_f32_16x16x32_bf16 v[22:25], v[172:175], v[204:207], v[22:25]
	v_mfma_f32_16x16x32_bf16 v[18:21], v[180:183], v[204:207], v[18:21]
	v_mfma_f32_16x16x32_bf16 v[6:9], v[172:175], v[212:215], v[6:9]
	v_mfma_f32_16x16x32_bf16 v[2:5], v[180:183], v[212:215], v[2:5]
	v_mfma_f32_16x16x32_bf16 v[54:57], v[176:179], v[192:195], v[54:57]
	v_mfma_f32_16x16x32_bf16 v[50:53], v[184:187], v[192:195], v[50:53]
	v_mfma_f32_16x16x32_bf16 v[38:41], v[176:179], v[200:203], v[38:41]
	v_mfma_f32_16x16x32_bf16 v[34:37], v[184:187], v[200:203], v[34:37]
	v_mfma_f32_16x16x32_bf16 v[22:25], v[176:179], v[208:211], v[22:25]
	v_mfma_f32_16x16x32_bf16 v[18:21], v[184:187], v[208:211], v[18:21]
	v_mfma_f32_16x16x32_bf16 v[6:9], v[176:179], v[216:219], v[6:9]
	v_mfma_f32_16x16x32_bf16 v[2:5], v[184:187], v[216:219], v[2:5]
	s_setprio 0
	s_barrier
; #define PG8_STAGE(bufoff, gbase, voff) do { _Pragma("unroll") for (int _i = 0; _i < 2; ++_i) \
;         __builtin_amdgcn_global_load_lds((const unsigned*)((const char*)(gbase) + (voff)[_i]), (PG8_LAS unsigned*)(lds + (bufoff) + ldsw + _i * 8192), 16, 0, 0); } while (0)
; #define PG8_LDA(dst, b, h) do { if constexpr (DT != 1) { _Pragma("unroll") for (int m = 0; m < 4; ++m) _Pragma("unroll") for (int k = 0; k < 2; ++k) dst[m][k] = *(const PG8_LAS bf16x8*)(lds + PG8_SA(b, h) + aoff + m * 2048 + k * 1024); } \
;         else { _Pragma("unroll") for (int m = 0; m < 4; ++m) dst##8[m] = ld32(lds + PG8_SA(b, h) + aoff + m * 2048); } } while (0)
; #define PG8_LDB(dst, b, h) do { if constexpr (DT != 1) { _Pragma("unroll") for (int n = 0; n < 2; ++n) _Pragma("unroll") for (int k = 0; k < 2; ++k) dst[n][k] = *(const PG8_LAS bf16x8*)(lds + PG8_SB(b, h) + boff + n * 2048 + k * 1024); } \
;         else { _Pragma("unroll") for (int n = 0; n < 2; ++n) dst##8[n] = ld32(lds + PG8_SB(b, h) + boff + n * 2048); } } while (0)
; #define PG8_WAIT_V(n) asm volatile("s_waitcnt vmcnt(" #n ")" ::: "memory")
; #define PG8_WAIT_L(n) asm volatile("s_waitcnt lgkmcnt(" #n ")" ::: "memory")
; #define PG8_BAR __builtin_amdgcn_s_barrier()
; #define PG8_SCHED __builtin_amdgcn_sched_barrier(0)
;     ...
;         for (int t = 0; t < nt; t += 2) {
;             const bool last = (t == nt - 2);
;             const char* a1 = cA + (size_t)(t + 1) * kstep;
;             const char* a2 = last ? nA : cA + (size_t)(t + 2) * kstep; const char* b2 = last ? nB : cB + (size_t)(t + 2) * kstep;
;     ...
;             PG8_LDB(B0, 1, 0); PG8_LDB(B1, 1, 1); PG8_SCHED; PG8_LDA(At, 1, 0); PG8_STAGE(PG8_SA(0, 1), a2 + hstepA, voffA);
;             PG8_WAIT_V(8); PG8_WAIT_L(0); PG8_BAR; PG8_MMA(0, 0, At, B0); PG8_MMA(0, 1, At, B1); PG8_BAR; PG8_SCHED;
;             PG8_LDA(At, 1, 1); PG8_STAGE(PG8_SB(1, 0), b3, voffB); PG8_STAGE(PG8_SB(1, 1), b3 + hstepB, voffB); PG8_STAGE(PG8_SA(1, 0), a3, voffA);
;             PG8_WAIT_V(8); PG8_WAIT_L(0); PG8_BAR; PG8_MMA(1, 0, At, B0); PG8_MMA(1, 1, At, B1); PG8_BAR; PG8_SCHED;
	ds_read_b128 v[156:159], v153
	ds_read_b128 v[160:163], v153 offset:1024
	ds_read_b128 v[164:167], v153 offset:2048
	ds_read_b128 v[168:171], v153 offset:3072
	ds_read_b128 v[172:175], v154
	ds_read_b128 v[176:179], v154 offset:1024
	ds_read_b128 v[180:183], v154 offset:2048
	ds_read_b128 v[184:187], v154 offset:3072
	s_add_u32 s30, s30, 0x80000
	s_addc_u32 s31, s31, 0
	s_mov_b32 m0, s47
	ds_read_b128 v[188:191], v152 offset:32768
	ds_read_b128 v[192:195], v152 offset:33792
	ds_read_b128 v[196:199], v152 offset:34816
	ds_read_b128 v[200:203], v152 offset:35840
	ds_read_b128 v[204:207], v152 offset:36864
	ds_read_b128 v[208:211], v152 offset:37888
	ds_read_b128 v[212:215], v152 offset:38912
	ds_read_b128 v[216:219], v152 offset:39936
	global_load_lds_dwordx4 v130, s[30:31]
	s_mov_b32 m0, s48
	s_nop 0
	global_load_lds_dwordx4 v134, s[30:31]
	s_waitcnt vmcnt(8)
	s_waitcnt lgkmcnt(0)
	s_barrier
	s_setprio 1
	s_waitcnt lgkmcnt(0)
	v_mfma_f32_16x16x32_bf16 v[122:125], v[156:159], v[188:191], v[122:125]
	v_mfma_f32_16x16x32_bf16 v[126:129], v[164:167], v[188:191], v[126:129]
	v_mfma_f32_16x16x32_bf16 v[110:113], v[156:159], v[196:199], v[110:113]
	v_mfma_f32_16x16x32_bf16 v[106:109], v[164:167], v[196:199], v[106:109]
	v_mfma_f32_16x16x32_bf16 v[94:97], v[156:159], v[204:207], v[94:97]
	v_mfma_f32_16x16x32_bf16 v[90:93], v[164:167], v[204:207], v[90:93]
	v_mfma_f32_16x16x32_bf16 v[78:81], v[156:159], v[212:215], v[78:81]
	v_mfma_f32_16x16x32_bf16 v[74:77], v[164:167], v[212:215], v[74:77]
	v_mfma_f32_16x16x32_bf16 v[122:125], v[160:163], v[192:195], v[122:125]
	v_mfma_f32_16x16x32_bf16 v[126:129], v[168:171], v[192:195], v[126:129]
	v_mfma_f32_16x16x32_bf16 v[110:113], v[160:163], v[200:203], v[110:113]
	v_mfma_f32_16x16x32_bf16 v[106:109], v[168:171], v[200:203], v[106:109]
	v_mfma_f32_16x16x32_bf16 v[94:97], v[160:163], v[208:211], v[94:97]
	v_mfma_f32_16x16x32_bf16 v[90:93], v[168:171], v[208:211], v[90:93]
	v_mfma_f32_16x16x32_bf16 v[78:81], v[160:163], v[216:219], v[78:81]
	v_mfma_f32_16x16x32_bf16 v[74:77], v[168:171], v[216:219], v[74:77]
	v_mfma_f32_16x16x32_bf16 v[118:121], v[172:175], v[188:191], v[118:121]
	v_mfma_f32_16x16x32_bf16 v[114:117], v[180:183], v[188:191], v[114:117]
	v_mfma_f32_16x16x32_bf16 v[102:105], v[172:175], v[196:199], v[102:105]
	v_mfma_f32_16x16x32_bf16 v[98:101], v[180:183], v[196:199], v[98:101]
	v_mfma_f32_16x16x32_bf16 v[86:89], v[172:175], v[204:207], v[86:89]
	v_mfma_f32_16x16x32_bf16 v[82:85], v[180:183], v[204:207], v[82:85]
	v_mfma_f32_16x16x32_bf16 v[70:73], v[172:175], v[212:215], v[70:73]
	v_mfma_f32_16x16x32_bf16 v[66:69], v[180:183], v[212:215], v[66:69]
	v_mfma_f32_16x16x32_bf16 v[118:121], v[176:179], v[192:195], v[118:121]
	v_mfma_f32_16x16x32_bf16 v[114:117], v[184:187], v[192:195], v[114:117]
	v_mfma_f32_16x16x32_bf16 v[102:105], v[176:179], v[200:203], v[102:105]
	v_mfma_f32_16x16x32_bf16 v[98:101], v[184:187], v[200:203], v[98:101]
	v_mfma_f32_16x16x32_bf16 v[86:89], v[176:179], v[208:211], v[86:89]
	v_mfma_f32_16x16x32_bf16 v[82:85], v[184:187], v[208:211], v[82:85]
	v_mfma_f32_16x16x32_bf16 v[70:73], v[176:179], v[216:219], v[70:73]
	v_mfma_f32_16x16x32_bf16 v[66:69], v[184:187], v[216:219], v[66:69]
	s_setprio 0
	s_barrier
	s_mov_b32 m0, s50
	s_add_u32 s28, s28, 0x80080
	ds_read_b128 v[188:191], v152 offset:49152
	ds_read_b128 v[192:195], v152 offset:50176
	ds_read_b128 v[196:199], v152 offset:51200
	ds_read_b128 v[200:203], v152 offset:52224
	ds_read_b128 v[204:207], v152 offset:53248
	ds_read_b128 v[208:211], v152 offset:54272
	ds_read_b128 v[212:215], v152 offset:55296
	ds_read_b128 v[216:219], v152 offset:56320
	global_load_lds_dwordx4 v132, s[98:99]
	s_mov_b32 m0, s51
	s_addc_u32 s29, s29, 0
	global_load_lds_dwordx4 v136, s[98:99]
	s_mov_b32 m0, s54
	s_nop 0
	global_load_lds_dwordx4 v132, s[28:29]
	s_mov_b32 m0, s55
	s_nop 0
	global_load_lds_dwordx4 v136, s[28:29]
	s_mov_b32 m0, s52
	s_nop 0
	global_load_lds_dwordx4 v130, s[100:101]
	s_mov_b32 m0, s53
	s_nop 0
	global_load_lds_dwordx4 v134, s[100:101]
	s_waitcnt vmcnt(8)
	s_waitcnt lgkmcnt(0)
	s_barrier
	s_setprio 1
	s_waitcnt lgkmcnt(0)
	v_mfma_f32_16x16x32_bf16 v[62:65], v[156:159], v[188:191], v[62:65]
	v_mfma_f32_16x16x32_bf16 v[58:61], v[164:167], v[188:191], v[58:61]
	v_mfma_f32_16x16x32_bf16 v[46:49], v[156:159], v[196:199], v[46:49]
	v_mfma_f32_16x16x32_bf16 v[42:45], v[164:167], v[196:199], v[42:45]
	v_mfma_f32_16x16x32_bf16 v[30:33], v[156:159], v[204:207], v[30:33]
	v_mfma_f32_16x16x32_bf16 v[26:29], v[164:167], v[204:207], v[26:29]
	v_mfma_f32_16x16x32_bf16 v[14:17], v[156:159], v[212:215], v[14:17]
	v_mfma_f32_16x16x32_bf16 v[10:13], v[164:167], v[212:215], v[10:13]
	v_mfma_f32_16x16x32_bf16 v[62:65], v[160:163], v[192:195], v[62:65]
	v_mfma_f32_16x16x32_bf16 v[58:61], v[168:171], v[192:195], v[58:61]
	v_mfma_f32_16x16x32_bf16 v[46:49], v[160:163], v[200:203], v[46:49]
	v_mfma_f32_16x16x32_bf16 v[42:45], v[168:171], v[200:203], v[42:45]
	v_mfma_f32_16x16x32_bf16 v[30:33], v[160:163], v[208:211], v[30:33]
	v_mfma_f32_16x16x32_bf16 v[26:29], v[168:171], v[208:211], v[26:29]
	v_mfma_f32_16x16x32_bf16 v[14:17], v[160:163], v[216:219], v[14:17]
	v_mfma_f32_16x16x32_bf16 v[10:13], v[168:171], v[216:219], v[10:13]
	v_mfma_f32_16x16x32_bf16 v[54:57], v[172:175], v[188:191], v[54:57]
	v_mfma_f32_16x16x32_bf16 v[50:53], v[180:183], v[188:191], v[50:53]
	v_mfma_f32_16x16x32_bf16 v[38:41], v[172:175], v[196:199], v[38:41]
	v_mfma_f32_16x16x32_bf16 v[34:37], v[180:183], v[196:199], v[34:37]
	v_mfma_f32_16x16x32_bf16 v[22:25], v[172:175], v[204:207], v[22:25]
	v_mfma_f32_16x16x32_bf16 v[18:21], v[180:183], v[204:207], v[18:21]
	v_mfma_f32_16x16x32_bf16 v[6:9], v[172:175], v[212:215], v[6:9]
	v_mfma_f32_16x16x32_bf16 v[2:5], v[180:183], v[212:215], v[2:5]
	v_mfma_f32_16x16x32_bf16 v[54:57], v[176:179], v[192:195], v[54:57]
	v_mfma_f32_16x16x32_bf16 v[50:53], v[184:187], v[192:195], v[50:53]
	v_mfma_f32_16x16x32_bf16 v[38:41], v[176:179], v[200:203], v[38:41]
	v_mfma_f32_16x16x32_bf16 v[34:37], v[184:187], v[200:203], v[34:37]
	v_mfma_f32_16x16x32_bf16 v[22:25], v[176:179], v[208:211], v[22:25]
	v_mfma_f32_16x16x32_bf16 v[18:21], v[184:187], v[208:211], v[18:21]
	v_mfma_f32_16x16x32_bf16 v[6:9], v[176:179], v[216:219], v[6:9]
	v_mfma_f32_16x16x32_bf16 v[2:5], v[184:187], v[216:219], v[2:5]
	s_setprio 0
	s_barrier
	s_add_u32 s63, s63, 0x100
	s_addc_u32 s64, s64, 0
	s_add_u32 s26, s26, 0x100
	s_addc_u32 s27, s27, 0
	s_cmp_ge_i32 s65, s49
	s_mov_b32 s28, s65
	s_cbranch_scc0 .LBB0_418

; #define PG8_STAGE(bufoff, gbase, voff) do { _Pragma("unroll") for (int _i = 0; _i < 2; ++_i) \
;         __builtin_amdgcn_global_load_lds((const unsigned*)((const char*)(gbase) + (voff)[_i]), (PG8_LAS unsigned*)(lds + (bufoff) + ldsw + _i * 8192), 16, 0, 0); } while (0)
; #define PG8_LDA(dst, b, h) do { if constexpr (DT != 1) { _Pragma("unroll") for (int m = 0; m < 4; ++m) _Pragma("unroll") for (int k = 0; k < 2; ++k) dst[m][k] = *(const PG8_LAS bf16x8*)(lds + PG8_SA(b, h) + aoff + m * 2048 + k * 1024); } \
;         else { _Pragma("unroll") for (int m = 0; m < 4; ++m) dst##8[m] = ld32(lds + PG8_SA(b, h) + aoff + m * 2048); } } while (0)
; #define PG8_LDB(dst, b, h) do { if constexpr (DT != 1) { _Pragma("unroll") for (int n = 0; n < 2; ++n) _Pragma("unroll") for (int k = 0; k < 2; ++k) dst[n][k] = *(const PG8_LAS bf16x8*)(lds + PG8_SB(b, h) + boff + n * 2048 + k * 1024); } \
;         else { _Pragma("unroll") for (int n = 0; n < 2; ++n) dst##8[n] = ld32(lds + PG8_SB(b, h) + boff + n * 2048); } } while (0)
; #define PG8_WAIT_V(n) asm volatile("s_waitcnt vmcnt(" #n ")" ::: "memory")
; #define PG8_WAIT_L(n) asm volatile("s_waitcnt lgkmcnt(" #n ")" ::: "memory")
; #define PG8_BAR __builtin_amdgcn_s_barrier()
; #define PG8_SCHED __builtin_amdgcn_sched_barrier(0)
;     ...
;             PG8_LDB(B0, 0, 0); PG8_LDB(B1, 0, 1); PG8_SCHED; PG8_LDA(At, 0, 0); PG8_STAGE(PG8_SA(1, 1), a1 + hstepA, voffA);
;             PG8_WAIT_V(8); PG8_WAIT_L(0); PG8_BAR; PG8_MMA(0, 0, At, B0); PG8_MMA(0, 1, At, B1); PG8_BAR; PG8_SCHED;
;             PG8_LDA(At, 0, 1); PG8_STAGE(PG8_SB(0, 0), b2, voffB); PG8_STAGE(PG8_SB(0, 1), b2 + hstepB, voffB); PG8_STAGE(PG8_SA(0, 0), a2, voffA);
;             PG8_WAIT_V(8); PG8_WAIT_L(0); PG8_BAR; PG8_MMA(1, 0, At, B0); PG8_MMA(1, 1, At, B1); PG8_BAR; PG8_SCHED;
.LBB0_713:
	ds_read_b128 v[130:133], v173
	ds_read_b128 v[134:137], v173 offset:1024
	ds_read_b128 v[138:141], v173 offset:2048
	ds_read_b128 v[142:145], v173 offset:3072
	ds_read_b128 v[162:165], v174
	ds_read_b128 v[166:169], v174 offset:1024
	ds_read_b128 v[178:181], v174 offset:2048
	ds_read_b128 v[182:185], v174 offset:3072
	s_add_i32 s69, s36, 2
	s_add_u32 s37, s34, 0xfff80080
	s_addc_u32 s38, s35, -1
	s_cmp_eq_u32 s61, s36
	s_cselect_b32 s36, s66, s67
	s_cselect_b32 s39, s23, s38
	s_cselect_b32 s38, s25, s37
	s_cselect_b32 s37, s65, s68
	s_add_i32 m0, s49, 0xc000
	ds_read_b128 v[186:189], v175
	ds_read_b128 v[190:193], v175 offset:1024
	ds_read_b128 v[194:197], v175 offset:2048
	ds_read_b128 v[198:201], v175 offset:3072
	ds_read_b128 v[202:205], v175 offset:4096
	ds_read_b128 v[206:209], v175 offset:5120
	ds_read_b128 v[210:213], v175 offset:6144
	ds_read_b128 v[214:217], v175 offset:7168
	global_load_lds_dwordx4 v156, s[34:35]
	s_add_i32 m0, s49, 0xe000
	s_nop 0
	global_load_lds_dwordx4 v154, s[34:35]
	s_waitcnt vmcnt(8)
	s_waitcnt lgkmcnt(0)
	s_barrier
	s_setprio 1
	s_waitcnt lgkmcnt(0)
	v_mfma_f32_16x16x32_bf16 v[122:125], v[130:133], v[186:189], v[122:125]
	v_mfma_f32_16x16x32_bf16 v[126:129], v[138:141], v[186:189], v[126:129]
	v_mfma_f32_16x16x32_bf16 v[110:113], v[130:133], v[194:197], v[110:113]
	v_mfma_f32_16x16x32_bf16 v[106:109], v[138:141], v[194:197], v[106:109]
	v_mfma_f32_16x16x32_bf16 v[94:97], v[130:133], v[202:205], v[94:97]
	v_mfma_f32_16x16x32_bf16 v[90:93], v[138:141], v[202:205], v[90:93]
	v_mfma_f32_16x16x32_bf16 v[78:81], v[130:133], v[210:213], v[78:81]
	v_mfma_f32_16x16x32_bf16 v[74:77], v[138:141], v[210:213], v[74:77]
	v_mfma_f32_16x16x32_bf16 v[122:125], v[134:137], v[190:193], v[122:125]
	v_mfma_f32_16x16x32_bf16 v[126:129], v[142:145], v[190:193], v[126:129]
	v_mfma_f32_16x16x32_bf16 v[110:113], v[134:137], v[198:201], v[110:113]
	v_mfma_f32_16x16x32_bf16 v[106:109], v[142:145], v[198:201], v[106:109]
	v_mfma_f32_16x16x32_bf16 v[94:97], v[134:137], v[206:209], v[94:97]
	v_mfma_f32_16x16x32_bf16 v[90:93], v[142:145], v[206:209], v[90:93]
	v_mfma_f32_16x16x32_bf16 v[78:81], v[134:137], v[214:217], v[78:81]
	v_mfma_f32_16x16x32_bf16 v[74:77], v[142:145], v[214:217], v[74:77]
	v_mfma_f32_16x16x32_bf16 v[118:121], v[162:165], v[186:189], v[118:121]
	v_mfma_f32_16x16x32_bf16 v[114:117], v[178:181], v[186:189], v[114:117]
	v_mfma_f32_16x16x32_bf16 v[102:105], v[162:165], v[194:197], v[102:105]
	v_mfma_f32_16x16x32_bf16 v[98:101], v[178:181], v[194:197], v[98:101]
	v_mfma_f32_16x16x32_bf16 v[86:89], v[162:165], v[202:205], v[86:89]
	v_mfma_f32_16x16x32_bf16 v[82:85], v[178:181], v[202:205], v[82:85]
	v_mfma_f32_16x16x32_bf16 v[70:73], v[162:165], v[210:213], v[70:73]
	v_mfma_f32_16x16x32_bf16 v[66:69], v[178:181], v[210:213], v[66:69]
	v_mfma_f32_16x16x32_bf16 v[118:121], v[166:169], v[190:193], v[118:121]
	v_mfma_f32_16x16x32_bf16 v[114:117], v[182:185], v[190:193], v[114:117]
	v_mfma_f32_16x16x32_bf16 v[102:105], v[166:169], v[198:201], v[102:105]
	v_mfma_f32_16x16x32_bf16 v[98:101], v[182:185], v[198:201], v[98:101]
	v_mfma_f32_16x16x32_bf16 v[86:89], v[166:169], v[206:209], v[86:89]
	v_mfma_f32_16x16x32_bf16 v[82:85], v[182:185], v[206:209], v[82:85]
	v_mfma_f32_16x16x32_bf16 v[70:73], v[166:169], v[214:217], v[70:73]
	v_mfma_f32_16x16x32_bf16 v[66:69], v[182:185], v[214:217], v[66:69]
	s_setprio 0
	s_barrier
	s_mov_b32 m0, s31
	s_add_u32 s98, s36, 0x80
	s_addc_u32 s99, s37, 0
	s_add_u32 s70, s36, 0x80000
	ds_read_b128 v[186:189], v175 offset:16384
	ds_read_b128 v[190:193], v175 offset:17408
	ds_read_b128 v[194:197], v175 offset:18432
	ds_read_b128 v[198:201], v175 offset:19456
	ds_read_b128 v[202:205], v175 offset:20480
	ds_read_b128 v[206:209], v175 offset:21504
	ds_read_b128 v[210:213], v175 offset:22528
	ds_read_b128 v[214:217], v175 offset:23552
	global_load_lds_dwordx4 v148, s[36:37]
	s_mov_b32 m0, s46
	s_addc_u32 s71, s37, 0
	global_load_lds_dwordx4 v152, s[36:37]
	s_mov_b32 m0, s47
	s_nop 0
	global_load_lds_dwordx4 v148, s[70:71]
	s_mov_b32 m0, s48
	s_nop 0
	global_load_lds_dwordx4 v152, s[70:71]
	s_add_u32 s100, s38, 0x80
	s_addc_u32 s101, s39, 0
	s_mov_b32 m0, s49
	s_nop 0
	global_load_lds_dwordx4 v146, s[38:39]
	s_mov_b32 m0, s50
	s_nop 0
	global_load_lds_dwordx4 v150, s[38:39]
	s_waitcnt vmcnt(8)
	s_waitcnt lgkmcnt(0)
	s_barrier
	s_setprio 1
	s_waitcnt lgkmcnt(0)
	v_mfma_f32_16x16x32_bf16 v[62:65], v[130:133], v[186:189], v[62:65]
	v_mfma_f32_16x16x32_bf16 v[58:61], v[138:141], v[186:189], v[58:61]
	v_mfma_f32_16x16x32_bf16 v[46:49], v[130:133], v[194:197], v[46:49]
	v_mfma_f32_16x16x32_bf16 v[42:45], v[138:141], v[194:197], v[42:45]
	v_mfma_f32_16x16x32_bf16 v[30:33], v[130:133], v[202:205], v[30:33]
	v_mfma_f32_16x16x32_bf16 v[26:29], v[138:141], v[202:205], v[26:29]
	v_mfma_f32_16x16x32_bf16 v[14:17], v[130:133], v[210:213], v[14:17]
	v_mfma_f32_16x16x32_bf16 v[10:13], v[138:141], v[210:213], v[10:13]
	v_mfma_f32_16x16x32_bf16 v[62:65], v[134:137], v[190:193], v[62:65]
	v_mfma_f32_16x16x32_bf16 v[58:61], v[142:145], v[190:193], v[58:61]
	v_mfma_f32_16x16x32_bf16 v[46:49], v[134:137], v[198:201], v[46:49]
	v_mfma_f32_16x16x32_bf16 v[42:45], v[142:145], v[198:201], v[42:45]
	v_mfma_f32_16x16x32_bf16 v[30:33], v[134:137], v[206:209], v[30:33]
	v_mfma_f32_16x16x32_bf16 v[26:29], v[142:145], v[206:209], v[26:29]
	v_mfma_f32_16x16x32_bf16 v[14:17], v[134:137], v[214:217], v[14:17]
	v_mfma_f32_16x16x32_bf16 v[10:13], v[142:145], v[214:217], v[10:13]
	v_mfma_f32_16x16x32_bf16 v[54:57], v[162:165], v[186:189], v[54:57]
	v_mfma_f32_16x16x32_bf16 v[50:53], v[178:181], v[186:189], v[50:53]
	v_mfma_f32_16x16x32_bf16 v[38:41], v[162:165], v[194:197], v[38:41]
	v_mfma_f32_16x16x32_bf16 v[34:37], v[178:181], v[194:197], v[34:37]
	v_mfma_f32_16x16x32_bf16 v[22:25], v[162:165], v[202:205], v[22:25]
	v_mfma_f32_16x16x32_bf16 v[18:21], v[178:181], v[202:205], v[18:21]
	v_mfma_f32_16x16x32_bf16 v[6:9], v[162:165], v[210:213], v[6:9]
	v_mfma_f32_16x16x32_bf16 v[2:5], v[178:181], v[210:213], v[2:5]
	v_mfma_f32_16x16x32_bf16 v[54:57], v[166:169], v[190:193], v[54:57]
	v_mfma_f32_16x16x32_bf16 v[50:53], v[182:185], v[190:193], v[50:53]
	v_mfma_f32_16x16x32_bf16 v[38:41], v[166:169], v[198:201], v[38:41]
	v_mfma_f32_16x16x32_bf16 v[34:37], v[182:185], v[198:201], v[34:37]
	v_mfma_f32_16x16x32_bf16 v[22:25], v[166:169], v[206:209], v[22:25]
	v_mfma_f32_16x16x32_bf16 v[18:21], v[182:185], v[206:209], v[18:21]
	v_mfma_f32_16x16x32_bf16 v[6:9], v[166:169], v[214:217], v[6:9]
	v_mfma_f32_16x16x32_bf16 v[2:5], v[182:185], v[214:217], v[2:5]
	s_setprio 0
	s_barrier
; #define PG8_STAGE(bufoff, gbase, voff) do { _Pragma("unroll") for (int _i = 0; _i < 2; ++_i) \
;         __builtin_amdgcn_global_load_lds((const unsigned*)((const char*)(gbase) + (voff)[_i]), (PG8_LAS unsigned*)(lds + (bufoff) + ldsw + _i * 8192), 16, 0, 0); } while (0)
; #define PG8_LDA(dst, b, h) do { if constexpr (DT != 1) { _Pragma("unroll") for (int m = 0; m < 4; ++m) _Pragma("unroll") for (int k = 0; k < 2; ++k) dst[m][k] = *(const PG8_LAS bf16x8*)(lds + PG8_SA(b, h) + aoff + m * 2048 + k * 1024); } \
;         else { _Pragma("unroll") for (int m = 0; m < 4; ++m) dst##8[m] = ld32(lds + PG8_SA(b, h) + aoff + m * 2048); } } while (0)
; #define PG8_LDB(dst, b, h) do { if constexpr (DT != 1) { _Pragma("unroll") for (int n = 0; n < 2; ++n) _Pragma("unroll") for (int k = 0; k < 2; ++k) dst[n][k] = *(const PG8_LAS bf16x8*)(lds + PG8_SB(b, h) + boff + n * 2048 + k * 1024); } \
;         else { _Pragma("unroll") for (int n = 0; n < 2; ++n) dst##8[n] = ld32(lds + PG8_SB(b, h) + boff + n * 2048); } } while (0)
; #define PG8_WAIT_V(n) asm volatile("s_waitcnt vmcnt(" #n ")" ::: "memory")
; #define PG8_WAIT_L(n) asm volatile("s_waitcnt lgkmcnt(" #n ")" ::: "memory")
; #define PG8_BAR __builtin_amdgcn_s_barrier()
; #define PG8_SCHED __builtin_amdgcn_sched_barrier(0)
;     ...
;         for (int t = 0; t < nt; t += 2) {
;             const bool last = (t == nt - 2);
;             const char* a1 = cA + (size_t)(t + 1) * kstep;
;             const char* a2 = last ? nA : cA + (size_t)(t + 2) * kstep; const char* b2 = last ? nB : cB + (size_t)(t + 2) * kstep;
;     ...
;             PG8_LDB(B0, 1, 0); PG8_LDB(B1, 1, 1); PG8_SCHED; PG8_LDA(At, 1, 0); PG8_STAGE(PG8_SA(0, 1), a2 + hstepA, voffA);
;             PG8_WAIT_V(8); PG8_WAIT_L(0); PG8_BAR; PG8_MMA(0, 0, At, B0); PG8_MMA(0, 1, At, B1); PG8_BAR; PG8_SCHED;
;             PG8_LDA(At, 1, 1); PG8_STAGE(PG8_SB(1, 0), b3, voffB); PG8_STAGE(PG8_SB(1, 1), b3 + hstepB, voffB); PG8_STAGE(PG8_SA(1, 0), a3, voffA);
;             PG8_WAIT_V(8); PG8_WAIT_L(0); PG8_BAR; PG8_MMA(1, 0, At, B0); PG8_MMA(1, 1, At, B1); PG8_BAR; PG8_SCHED;
	ds_read_b128 v[130:133], v176
	ds_read_b128 v[134:137], v176 offset:1024
	ds_read_b128 v[138:141], v176 offset:2048
	ds_read_b128 v[142:145], v176 offset:3072
	ds_read_b128 v[162:165], v177
	ds_read_b128 v[166:169], v177 offset:1024
	ds_read_b128 v[178:181], v177 offset:2048
	ds_read_b128 v[182:185], v177 offset:3072
	s_add_u32 s38, s38, 0x80000
	s_addc_u32 s39, s39, 0
	s_mov_b32 m0, s51
	ds_read_b128 v[186:189], v175 offset:32768
	ds_read_b128 v[190:193], v175 offset:33792
	ds_read_b128 v[194:197], v175 offset:34816
	ds_read_b128 v[198:201], v175 offset:35840
	ds_read_b128 v[202:205], v175 offset:36864
	ds_read_b128 v[206:209], v175 offset:37888
	ds_read_b128 v[210:213], v175 offset:38912
	ds_read_b128 v[214:217], v175 offset:39936
	global_load_lds_dwordx4 v146, s[38:39]
	s_mov_b32 m0, s52
	s_nop 0
	global_load_lds_dwordx4 v150, s[38:39]
	s_waitcnt vmcnt(8)
	s_waitcnt lgkmcnt(0)
	s_barrier
	s_setprio 1
	s_waitcnt lgkmcnt(0)
	v_mfma_f32_16x16x32_bf16 v[122:125], v[130:133], v[186:189], v[122:125]
	v_mfma_f32_16x16x32_bf16 v[126:129], v[138:141], v[186:189], v[126:129]
	v_mfma_f32_16x16x32_bf16 v[110:113], v[130:133], v[194:197], v[110:113]
	v_mfma_f32_16x16x32_bf16 v[106:109], v[138:141], v[194:197], v[106:109]
	v_mfma_f32_16x16x32_bf16 v[94:97], v[130:133], v[202:205], v[94:97]
	v_mfma_f32_16x16x32_bf16 v[90:93], v[138:141], v[202:205], v[90:93]
	v_mfma_f32_16x16x32_bf16 v[78:81], v[130:133], v[210:213], v[78:81]
	v_mfma_f32_16x16x32_bf16 v[74:77], v[138:141], v[210:213], v[74:77]
	v_mfma_f32_16x16x32_bf16 v[122:125], v[134:137], v[190:193], v[122:125]
	v_mfma_f32_16x16x32_bf16 v[126:129], v[142:145], v[190:193], v[126:129]
	v_mfma_f32_16x16x32_bf16 v[110:113], v[134:137], v[198:201], v[110:113]
	v_mfma_f32_16x16x32_bf16 v[106:109], v[142:145], v[198:201], v[106:109]
	v_mfma_f32_16x16x32_bf16 v[94:97], v[134:137], v[206:209], v[94:97]
	v_mfma_f32_16x16x32_bf16 v[90:93], v[142:145], v[206:209], v[90:93]
	v_mfma_f32_16x16x32_bf16 v[78:81], v[134:137], v[214:217], v[78:81]
	v_mfma_f32_16x16x32_bf16 v[74:77], v[142:145], v[214:217], v[74:77]
	v_mfma_f32_16x16x32_bf16 v[118:121], v[162:165], v[186:189], v[118:121]
	v_mfma_f32_16x16x32_bf16 v[114:117], v[178:181], v[186:189], v[114:117]
	v_mfma_f32_16x16x32_bf16 v[102:105], v[162:165], v[194:197], v[102:105]
	v_mfma_f32_16x16x32_bf16 v[98:101], v[178:181], v[194:197], v[98:101]
	v_mfma_f32_16x16x32_bf16 v[86:89], v[162:165], v[202:205], v[86:89]
	v_mfma_f32_16x16x32_bf16 v[82:85], v[178:181], v[202:205], v[82:85]
	v_mfma_f32_16x16x32_bf16 v[70:73], v[162:165], v[210:213], v[70:73]
	v_mfma_f32_16x16x32_bf16 v[66:69], v[178:181], v[210:213], v[66:69]
	v_mfma_f32_16x16x32_bf16 v[118:121], v[166:169], v[190:193], v[118:121]
	v_mfma_f32_16x16x32_bf16 v[114:117], v[182:185], v[190:193], v[114:117]
	v_mfma_f32_16x16x32_bf16 v[102:105], v[166:169], v[198:201], v[102:105]
	v_mfma_f32_16x16x32_bf16 v[98:101], v[182:185], v[198:201], v[98:101]
	v_mfma_f32_16x16x32_bf16 v[86:89], v[166:169], v[206:209], v[86:89]
	v_mfma_f32_16x16x32_bf16 v[82:85], v[182:185], v[206:209], v[82:85]
	v_mfma_f32_16x16x32_bf16 v[70:73], v[166:169], v[214:217], v[70:73]
	v_mfma_f32_16x16x32_bf16 v[66:69], v[182:185], v[214:217], v[66:69]
	s_setprio 0
	s_barrier
	s_mov_b32 m0, s55
	s_add_u32 s36, s36, 0x80080
	ds_read_b128 v[186:189], v175 offset:49152
	ds_read_b128 v[190:193], v175 offset:50176
	ds_read_b128 v[194:197], v175 offset:51200
	ds_read_b128 v[198:201], v175 offset:52224
	ds_read_b128 v[202:205], v175 offset:53248
	ds_read_b128 v[206:209], v175 offset:54272
	ds_read_b128 v[210:213], v175 offset:55296
	ds_read_b128 v[214:217], v175 offset:56320
	global_load_lds_dwordx4 v148, s[98:99]
	s_mov_b32 m0, s56
	s_addc_u32 s37, s37, 0
	global_load_lds_dwordx4 v152, s[98:99]
	s_mov_b32 m0, s59
	s_nop 0
	global_load_lds_dwordx4 v148, s[36:37]
	s_mov_b32 m0, s60
	s_nop 0
	global_load_lds_dwordx4 v152, s[36:37]
	s_mov_b32 m0, s57
	s_nop 0
	global_load_lds_dwordx4 v146, s[100:101]
	s_mov_b32 m0, s58
	s_nop 0
	global_load_lds_dwordx4 v150, s[100:101]
	s_waitcnt vmcnt(8)
	s_waitcnt lgkmcnt(0)
	s_barrier
	s_setprio 1
	s_waitcnt lgkmcnt(0)
	v_mfma_f32_16x16x32_bf16 v[62:65], v[130:133], v[186:189], v[62:65]
	v_mfma_f32_16x16x32_bf16 v[58:61], v[138:141], v[186:189], v[58:61]
	v_mfma_f32_16x16x32_bf16 v[46:49], v[130:133], v[194:197], v[46:49]
	v_mfma_f32_16x16x32_bf16 v[42:45], v[138:141], v[194:197], v[42:45]
	v_mfma_f32_16x16x32_bf16 v[30:33], v[130:133], v[202:205], v[30:33]
	v_mfma_f32_16x16x32_bf16 v[26:29], v[138:141], v[202:205], v[26:29]
	v_mfma_f32_16x16x32_bf16 v[14:17], v[130:133], v[210:213], v[14:17]
	v_mfma_f32_16x16x32_bf16 v[10:13], v[138:141], v[210:213], v[10:13]
	v_mfma_f32_16x16x32_bf16 v[62:65], v[134:137], v[190:193], v[62:65]
	v_mfma_f32_16x16x32_bf16 v[58:61], v[142:145], v[190:193], v[58:61]
	v_mfma_f32_16x16x32_bf16 v[46:49], v[134:137], v[198:201], v[46:49]
	v_mfma_f32_16x16x32_bf16 v[42:45], v[142:145], v[198:201], v[42:45]
	v_mfma_f32_16x16x32_bf16 v[30:33], v[134:137], v[206:209], v[30:33]
	v_mfma_f32_16x16x32_bf16 v[26:29], v[142:145], v[206:209], v[26:29]
	v_mfma_f32_16x16x32_bf16 v[14:17], v[134:137], v[214:217], v[14:17]
	v_mfma_f32_16x16x32_bf16 v[10:13], v[142:145], v[214:217], v[10:13]
	v_mfma_f32_16x16x32_bf16 v[54:57], v[162:165], v[186:189], v[54:57]
	v_mfma_f32_16x16x32_bf16 v[50:53], v[178:181], v[186:189], v[50:53]
	v_mfma_f32_16x16x32_bf16 v[38:41], v[162:165], v[194:197], v[38:41]
	v_mfma_f32_16x16x32_bf16 v[34:37], v[178:181], v[194:197], v[34:37]
	v_mfma_f32_16x16x32_bf16 v[22:25], v[162:165], v[202:205], v[22:25]
	v_mfma_f32_16x16x32_bf16 v[18:21], v[178:181], v[202:205], v[18:21]
	v_mfma_f32_16x16x32_bf16 v[6:9], v[162:165], v[210:213], v[6:9]
	v_mfma_f32_16x16x32_bf16 v[2:5], v[178:181], v[210:213], v[2:5]
	v_mfma_f32_16x16x32_bf16 v[54:57], v[166:169], v[190:193], v[54:57]
	v_mfma_f32_16x16x32_bf16 v[50:53], v[182:185], v[190:193], v[50:53]
	v_mfma_f32_16x16x32_bf16 v[38:41], v[166:169], v[198:201], v[38:41]
	v_mfma_f32_16x16x32_bf16 v[34:37], v[182:185], v[198:201], v[34:37]
	v_mfma_f32_16x16x32_bf16 v[22:25], v[166:169], v[206:209], v[22:25]
	v_mfma_f32_16x16x32_bf16 v[18:21], v[182:185], v[206:209], v[18:21]
	v_mfma_f32_16x16x32_bf16 v[6:9], v[166:169], v[214:217], v[6:9]
	v_mfma_f32_16x16x32_bf16 v[2:5], v[182:185], v[214:217], v[2:5]
	s_setprio 0
	s_barrier
	s_add_u32 s67, s67, 0x100
	s_addc_u32 s68, s68, 0
	s_add_u32 s34, s34, 0x100
	s_addc_u32 s35, s35, 0
	s_cmp_ge_i32 s69, s54
	s_mov_b32 s36, s69
	s_cbranch_scc0 .LBB0_713

; #define PG8_STAGE(bufoff, gbase, voff) do { _Pragma("unroll") for (int _i = 0; _i < 2; ++_i) \
;         __builtin_amdgcn_global_load_lds((const unsigned*)((const char*)(gbase) + (voff)[_i]), (PG8_LAS unsigned*)(lds + (bufoff) + ldsw + _i * 8192), 16, 0, 0); } while (0)
; #define PG8_LDA(dst, b, h) do { if constexpr (DT != 1) { _Pragma("unroll") for (int m = 0; m < 4; ++m) _Pragma("unroll") for (int k = 0; k < 2; ++k) dst[m][k] = *(const PG8_LAS bf16x8*)(lds + PG8_SA(b, h) + aoff + m * 2048 + k * 1024); } \
;         else { _Pragma("unroll") for (int m = 0; m < 4; ++m) dst##8[m] = ld32(lds + PG8_SA(b, h) + aoff + m * 2048); } } while (0)
; #define PG8_LDB(dst, b, h) do { if constexpr (DT != 1) { _Pragma("unroll") for (int n = 0; n < 2; ++n) _Pragma("unroll") for (int k = 0; k < 2; ++k) dst[n][k] = *(const PG8_LAS bf16x8*)(lds + PG8_SB(b, h) + boff + n * 2048 + k * 1024); } \
;         else { _Pragma("unroll") for (int n = 0; n < 2; ++n) dst##8[n] = ld32(lds + PG8_SB(b, h) + boff + n * 2048); } } while (0)
; #define PG8_WAIT_V(n) asm volatile("s_waitcnt vmcnt(" #n ")" ::: "memory")
; #define PG8_WAIT_L(n) asm volatile("s_waitcnt lgkmcnt(" #n ")" ::: "memory")
; #define PG8_BAR __builtin_amdgcn_s_barrier()
; #define PG8_SCHED __builtin_amdgcn_sched_barrier(0)
;     ...
;             PG8_LDB(B0, 0, 0); PG8_LDB(B1, 0, 1); PG8_SCHED; PG8_LDA(At, 0, 0); PG8_STAGE(PG8_SA(1, 1), a1 + hstepA, voffA);
;             PG8_WAIT_V(8); PG8_WAIT_L(0); PG8_BAR; PG8_MMA(0, 0, At, B0); PG8_MMA(0, 1, At, B1); PG8_BAR; PG8_SCHED;
;             PG8_LDA(At, 0, 1); PG8_STAGE(PG8_SB(0, 0), b2, voffB); PG8_STAGE(PG8_SB(0, 1), b2 + hstepB, voffB); PG8_STAGE(PG8_SA(0, 0), a2, voffA);
;             PG8_WAIT_V(8); PG8_WAIT_L(0); PG8_BAR; PG8_MMA(1, 0, At, B0); PG8_MMA(1, 1, At, B1); PG8_BAR; PG8_SCHED;
.LBB0_922:
	ds_read_b128 v[146:149], v173
	ds_read_b128 v[150:153], v173 offset:1024
	ds_read_b128 v[154:157], v173 offset:2048
	ds_read_b128 v[158:161], v173 offset:3072
	ds_read_b128 v[162:165], v174
	ds_read_b128 v[166:169], v174 offset:1024
	ds_read_b128 v[178:181], v174 offset:2048
	ds_read_b128 v[182:185], v174 offset:3072
	s_add_i32 s67, s30, 2
	s_add_u32 s28, s26, 0x100
	s_addc_u32 s29, s27, 0
	s_cmp_eq_u32 s58, s30
	s_cselect_b32 s30, s24, s65
	s_cselect_b32 s35, s3, s29
	s_cselect_b32 s34, s2, s28
	s_cselect_b32 s31, s25, s66
	v_lshl_add_u64 v[170:171], s[26:27], 0, v[140:141]
	s_add_i32 m0, s46, 0xc000
	ds_read_b128 v[186:189], v175
	ds_read_b128 v[190:193], v175 offset:1024
	ds_read_b128 v[194:197], v175 offset:2048
	ds_read_b128 v[198:201], v175 offset:3072
	ds_read_b128 v[202:205], v175 offset:4096
	ds_read_b128 v[206:209], v175 offset:5120
	ds_read_b128 v[210:213], v175 offset:6144
	ds_read_b128 v[214:217], v175 offset:7168
	global_load_lds_dwordx4 v[170:171], off
	v_lshl_add_u64 v[170:171], s[26:27], 0, v[138:139]
	s_add_i32 m0, s46, 0xe000
	s_nop 0
	global_load_lds_dwordx4 v[170:171], off
	s_waitcnt vmcnt(8)
	s_waitcnt lgkmcnt(0)
	s_barrier
	s_setprio 1
	s_waitcnt lgkmcnt(0)
	v_mfma_f32_16x16x32_bf16 v[126:129], v[146:149], v[186:189], v[126:129]
	v_mfma_f32_16x16x32_bf16 v[122:125], v[154:157], v[186:189], v[122:125]
	v_mfma_f32_16x16x32_bf16 v[118:121], v[146:149], v[194:197], v[118:121]
	v_mfma_f32_16x16x32_bf16 v[114:117], v[154:157], v[194:197], v[114:117]
	v_mfma_f32_16x16x32_bf16 v[106:109], v[146:149], v[202:205], v[106:109]
	v_mfma_f32_16x16x32_bf16 v[98:101], v[154:157], v[202:205], v[98:101]
	v_mfma_f32_16x16x32_bf16 v[90:93], v[146:149], v[210:213], v[90:93]
	v_mfma_f32_16x16x32_bf16 v[82:85], v[154:157], v[210:213], v[82:85]
	v_mfma_f32_16x16x32_bf16 v[126:129], v[150:153], v[190:193], v[126:129]
	v_mfma_f32_16x16x32_bf16 v[122:125], v[158:161], v[190:193], v[122:125]
	v_mfma_f32_16x16x32_bf16 v[118:121], v[150:153], v[198:201], v[118:121]
	v_mfma_f32_16x16x32_bf16 v[114:117], v[158:161], v[198:201], v[114:117]
	v_mfma_f32_16x16x32_bf16 v[106:109], v[150:153], v[206:209], v[106:109]
	v_mfma_f32_16x16x32_bf16 v[98:101], v[158:161], v[206:209], v[98:101]
	v_mfma_f32_16x16x32_bf16 v[90:93], v[150:153], v[214:217], v[90:93]
	v_mfma_f32_16x16x32_bf16 v[82:85], v[158:161], v[214:217], v[82:85]
	v_mfma_f32_16x16x32_bf16 v[110:113], v[162:165], v[186:189], v[110:113]
	v_mfma_f32_16x16x32_bf16 v[102:105], v[178:181], v[186:189], v[102:105]
	v_mfma_f32_16x16x32_bf16 v[94:97], v[162:165], v[194:197], v[94:97]
	v_mfma_f32_16x16x32_bf16 v[86:89], v[178:181], v[194:197], v[86:89]
	v_mfma_f32_16x16x32_bf16 v[78:81], v[162:165], v[202:205], v[78:81]
	v_mfma_f32_16x16x32_bf16 v[74:77], v[178:181], v[202:205], v[74:77]
	v_mfma_f32_16x16x32_bf16 v[70:73], v[162:165], v[210:213], v[70:73]
	v_mfma_f32_16x16x32_bf16 v[66:69], v[178:181], v[210:213], v[66:69]
	v_mfma_f32_16x16x32_bf16 v[110:113], v[166:169], v[190:193], v[110:113]
	v_mfma_f32_16x16x32_bf16 v[102:105], v[182:185], v[190:193], v[102:105]
	v_mfma_f32_16x16x32_bf16 v[94:97], v[166:169], v[198:201], v[94:97]
	v_mfma_f32_16x16x32_bf16 v[86:89], v[182:185], v[198:201], v[86:89]
	v_mfma_f32_16x16x32_bf16 v[78:81], v[166:169], v[206:209], v[78:81]
	v_mfma_f32_16x16x32_bf16 v[74:77], v[182:185], v[206:209], v[74:77]
	v_mfma_f32_16x16x32_bf16 v[70:73], v[166:169], v[214:217], v[70:73]
	v_mfma_f32_16x16x32_bf16 v[66:69], v[182:185], v[214:217], v[66:69]
	s_setprio 0
	s_barrier
	s_mov_b32 m0, s42
	s_add_u32 s98, s30, 0x80
	s_addc_u32 s99, s31, 0
	s_add_u32 s26, s30, 0x160000
	ds_read_b128 v[186:189], v175 offset:16384
	ds_read_b128 v[190:193], v175 offset:17408
	ds_read_b128 v[194:197], v175 offset:18432
	ds_read_b128 v[198:201], v175 offset:19456
	ds_read_b128 v[202:205], v175 offset:20480
	ds_read_b128 v[206:209], v175 offset:21504
	ds_read_b128 v[210:213], v175 offset:22528
	ds_read_b128 v[214:217], v175 offset:23552
	global_load_lds_dwordx4 v132, s[30:31]
	s_mov_b32 m0, s43
	s_addc_u32 s27, s31, 0
	global_load_lds_dwordx4 v136, s[30:31]
	s_mov_b32 m0, s44
	s_nop 0
	global_load_lds_dwordx4 v132, s[26:27]
	s_mov_b32 m0, s45
	s_nop 0
	global_load_lds_dwordx4 v136, s[26:27]
	s_add_u32 s100, s34, 0x80
	s_addc_u32 s101, s35, 0
	s_mov_b32 m0, s46
	s_nop 0
	global_load_lds_dwordx4 v130, s[34:35]
	s_mov_b32 m0, s47
	s_nop 0
	global_load_lds_dwordx4 v134, s[34:35]
	s_waitcnt vmcnt(8)
	s_waitcnt lgkmcnt(0)
	s_barrier
	s_setprio 1
	s_waitcnt lgkmcnt(0)
	v_mfma_f32_16x16x32_bf16 v[62:65], v[146:149], v[186:189], v[62:65]
	v_mfma_f32_16x16x32_bf16 v[58:61], v[154:157], v[186:189], v[58:61]
	v_mfma_f32_16x16x32_bf16 v[54:57], v[146:149], v[194:197], v[54:57]
	v_mfma_f32_16x16x32_bf16 v[50:53], v[154:157], v[194:197], v[50:53]
	v_mfma_f32_16x16x32_bf16 v[42:45], v[146:149], v[202:205], v[42:45]
	v_mfma_f32_16x16x32_bf16 v[34:37], v[154:157], v[202:205], v[34:37]
	v_mfma_f32_16x16x32_bf16 v[26:29], v[146:149], v[210:213], v[26:29]
	v_mfma_f32_16x16x32_bf16 v[18:21], v[154:157], v[210:213], v[18:21]
	v_mfma_f32_16x16x32_bf16 v[62:65], v[150:153], v[190:193], v[62:65]
	v_mfma_f32_16x16x32_bf16 v[58:61], v[158:161], v[190:193], v[58:61]
	v_mfma_f32_16x16x32_bf16 v[54:57], v[150:153], v[198:201], v[54:57]
	v_mfma_f32_16x16x32_bf16 v[50:53], v[158:161], v[198:201], v[50:53]
	v_mfma_f32_16x16x32_bf16 v[42:45], v[150:153], v[206:209], v[42:45]
	v_mfma_f32_16x16x32_bf16 v[34:37], v[158:161], v[206:209], v[34:37]
	v_mfma_f32_16x16x32_bf16 v[26:29], v[150:153], v[214:217], v[26:29]
	v_mfma_f32_16x16x32_bf16 v[18:21], v[158:161], v[214:217], v[18:21]
	v_mfma_f32_16x16x32_bf16 v[46:49], v[162:165], v[186:189], v[46:49]
	v_mfma_f32_16x16x32_bf16 v[38:41], v[178:181], v[186:189], v[38:41]
	v_mfma_f32_16x16x32_bf16 v[30:33], v[162:165], v[194:197], v[30:33]
	v_mfma_f32_16x16x32_bf16 v[22:25], v[178:181], v[194:197], v[22:25]
	v_mfma_f32_16x16x32_bf16 v[14:17], v[162:165], v[202:205], v[14:17]
	v_mfma_f32_16x16x32_bf16 v[10:13], v[178:181], v[202:205], v[10:13]
	v_mfma_f32_16x16x32_bf16 v[6:9], v[162:165], v[210:213], v[6:9]
	v_mfma_f32_16x16x32_bf16 v[2:5], v[178:181], v[210:213], v[2:5]
	v_mfma_f32_16x16x32_bf16 v[46:49], v[166:169], v[190:193], v[46:49]
	v_mfma_f32_16x16x32_bf16 v[38:41], v[182:185], v[190:193], v[38:41]
	v_mfma_f32_16x16x32_bf16 v[30:33], v[166:169], v[198:201], v[30:33]
	v_mfma_f32_16x16x32_bf16 v[22:25], v[182:185], v[198:201], v[22:25]
	v_mfma_f32_16x16x32_bf16 v[14:17], v[166:169], v[206:209], v[14:17]
	v_mfma_f32_16x16x32_bf16 v[10:13], v[182:185], v[206:209], v[10:13]
	v_mfma_f32_16x16x32_bf16 v[6:9], v[166:169], v[214:217], v[6:9]
	v_mfma_f32_16x16x32_bf16 v[2:5], v[182:185], v[214:217], v[2:5]
	s_setprio 0
	s_barrier
; #define PG8_STAGE(bufoff, gbase, voff) do { _Pragma("unroll") for (int _i = 0; _i < 2; ++_i) \
;         __builtin_amdgcn_global_load_lds((const unsigned*)((const char*)(gbase) + (voff)[_i]), (PG8_LAS unsigned*)(lds + (bufoff) + ldsw + _i * 8192), 16, 0, 0); } while (0)
; #define PG8_LDA(dst, b, h) do { if constexpr (DT != 1) { _Pragma("unroll") for (int m = 0; m < 4; ++m) _Pragma("unroll") for (int k = 0; k < 2; ++k) dst[m][k] = *(const PG8_LAS bf16x8*)(lds + PG8_SA(b, h) + aoff + m * 2048 + k * 1024); } \
;         else { _Pragma("unroll") for (int m = 0; m < 4; ++m) dst##8[m] = ld32(lds + PG8_SA(b, h) + aoff + m * 2048); } } while (0)
; #define PG8_LDB(dst, b, h) do { if constexpr (DT != 1) { _Pragma("unroll") for (int n = 0; n < 2; ++n) _Pragma("unroll") for (int k = 0; k < 2; ++k) dst[n][k] = *(const PG8_LAS bf16x8*)(lds + PG8_SB(b, h) + boff + n * 2048 + k * 1024); } \
;         else { _Pragma("unroll") for (int n = 0; n < 2; ++n) dst##8[n] = ld32(lds + PG8_SB(b, h) + boff + n * 2048); } } while (0)
; #define PG8_WAIT_V(n) asm volatile("s_waitcnt vmcnt(" #n ")" ::: "memory")
; #define PG8_WAIT_L(n) asm volatile("s_waitcnt lgkmcnt(" #n ")" ::: "memory")
; #define PG8_BAR __builtin_amdgcn_s_barrier()
; #define PG8_SCHED __builtin_amdgcn_sched_barrier(0)
;     ...
;             PG8_LDB(B0, 1, 0); PG8_LDB(B1, 1, 1); PG8_SCHED; PG8_LDA(At, 1, 0); PG8_STAGE(PG8_SA(0, 1), a2 + hstepA, voffA);
;             PG8_WAIT_V(8); PG8_WAIT_L(0); PG8_BAR; PG8_MMA(0, 0, At, B0); PG8_MMA(0, 1, At, B1); PG8_BAR; PG8_SCHED;
;             PG8_LDA(At, 1, 1); PG8_STAGE(PG8_SB(1, 0), b3, voffB); PG8_STAGE(PG8_SB(1, 1), b3 + hstepB, voffB); PG8_STAGE(PG8_SA(1, 0), a3, voffA);
	ds_read_b128 v[146:149], v176
	ds_read_b128 v[150:153], v176 offset:1024
	ds_read_b128 v[154:157], v176 offset:2048
	ds_read_b128 v[158:161], v176 offset:3072
	ds_read_b128 v[162:165], v177
	ds_read_b128 v[166:169], v177 offset:1024
	ds_read_b128 v[178:181], v177 offset:2048
	ds_read_b128 v[182:185], v177 offset:3072
	s_add_u32 s26, s34, 0x160000
	s_addc_u32 s27, s35, 0
	s_mov_b32 m0, s48
	ds_read_b128 v[186:189], v175 offset:32768
	ds_read_b128 v[190:193], v175 offset:33792
	ds_read_b128 v[194:197], v175 offset:34816
	ds_read_b128 v[198:201], v175 offset:35840
	ds_read_b128 v[202:205], v175 offset:36864
	ds_read_b128 v[206:209], v175 offset:37888
	ds_read_b128 v[210:213], v175 offset:38912
	ds_read_b128 v[214:217], v175 offset:39936
	global_load_lds_dwordx4 v130, s[26:27]
	s_mov_b32 m0, s49
	s_nop 0
	global_load_lds_dwordx4 v134, s[26:27]
	s_waitcnt vmcnt(8)
	s_waitcnt lgkmcnt(0)
	s_barrier
	s_setprio 1
	s_waitcnt lgkmcnt(0)
	v_mfma_f32_16x16x32_bf16 v[126:129], v[146:149], v[186:189], v[126:129]
	v_mfma_f32_16x16x32_bf16 v[122:125], v[154:157], v[186:189], v[122:125]
	v_mfma_f32_16x16x32_bf16 v[118:121], v[146:149], v[194:197], v[118:121]
	v_mfma_f32_16x16x32_bf16 v[114:117], v[154:157], v[194:197], v[114:117]
	v_mfma_f32_16x16x32_bf16 v[106:109], v[146:149], v[202:205], v[106:109]
	v_mfma_f32_16x16x32_bf16 v[98:101], v[154:157], v[202:205], v[98:101]
	v_mfma_f32_16x16x32_bf16 v[90:93], v[146:149], v[210:213], v[90:93]
	v_mfma_f32_16x16x32_bf16 v[82:85], v[154:157], v[210:213], v[82:85]
	v_mfma_f32_16x16x32_bf16 v[126:129], v[150:153], v[190:193], v[126:129]
	v_mfma_f32_16x16x32_bf16 v[122:125], v[158:161], v[190:193], v[122:125]
	v_mfma_f32_16x16x32_bf16 v[118:121], v[150:153], v[198:201], v[118:121]
	v_mfma_f32_16x16x32_bf16 v[114:117], v[158:161], v[198:201], v[114:117]
	v_mfma_f32_16x16x32_bf16 v[106:109], v[150:153], v[206:209], v[106:109]
	v_mfma_f32_16x16x32_bf16 v[98:101], v[158:161], v[206:209], v[98:101]
	v_mfma_f32_16x16x32_bf16 v[90:93], v[150:153], v[214:217], v[90:93]
	v_mfma_f32_16x16x32_bf16 v[82:85], v[158:161], v[214:217], v[82:85]
	v_mfma_f32_16x16x32_bf16 v[110:113], v[162:165], v[186:189], v[110:113]
	v_mfma_f32_16x16x32_bf16 v[102:105], v[178:181], v[186:189], v[102:105]
	v_mfma_f32_16x16x32_bf16 v[94:97], v[162:165], v[194:197], v[94:97]
	v_mfma_f32_16x16x32_bf16 v[86:89], v[178:181], v[194:197], v[86:89]
	v_mfma_f32_16x16x32_bf16 v[78:81], v[162:165], v[202:205], v[78:81]
	v_mfma_f32_16x16x32_bf16 v[74:77], v[178:181], v[202:205], v[74:77]
	v_mfma_f32_16x16x32_bf16 v[70:73], v[162:165], v[210:213], v[70:73]
	v_mfma_f32_16x16x32_bf16 v[66:69], v[178:181], v[210:213], v[66:69]
	v_mfma_f32_16x16x32_bf16 v[110:113], v[166:169], v[190:193], v[110:113]
	v_mfma_f32_16x16x32_bf16 v[102:105], v[182:185], v[190:193], v[102:105]
	v_mfma_f32_16x16x32_bf16 v[94:97], v[166:169], v[198:201], v[94:97]
	v_mfma_f32_16x16x32_bf16 v[86:89], v[182:185], v[198:201], v[86:89]
	v_mfma_f32_16x16x32_bf16 v[78:81], v[166:169], v[206:209], v[78:81]
	v_mfma_f32_16x16x32_bf16 v[74:77], v[182:185], v[206:209], v[74:77]
	v_mfma_f32_16x16x32_bf16 v[70:73], v[166:169], v[214:217], v[70:73]
	v_mfma_f32_16x16x32_bf16 v[66:69], v[182:185], v[214:217], v[66:69]
	s_setprio 0
	s_barrier
	s_mov_b32 m0, s52
	s_add_u32 s26, s30, 0x160080
	ds_read_b128 v[186:189], v175 offset:49152
	ds_read_b128 v[190:193], v175 offset:50176
	ds_read_b128 v[194:197], v175 offset:51200
	ds_read_b128 v[198:201], v175 offset:52224
	ds_read_b128 v[202:205], v175 offset:53248
	ds_read_b128 v[206:209], v175 offset:54272
	ds_read_b128 v[210:213], v175 offset:55296
	ds_read_b128 v[214:217], v175 offset:56320
	global_load_lds_dwordx4 v132, s[98:99]
	s_mov_b32 m0, s53
	s_addc_u32 s27, s31, 0
	global_load_lds_dwordx4 v136, s[98:99]
	s_mov_b32 m0, s56
	s_nop 0
	global_load_lds_dwordx4 v132, s[26:27]
	s_mov_b32 m0, s57
	s_nop 0
	global_load_lds_dwordx4 v136, s[26:27]
	s_mov_b32 m0, s54
	s_nop 0
	global_load_lds_dwordx4 v130, s[100:101]
	s_mov_b32 m0, s55
	s_nop 0
	global_load_lds_dwordx4 v134, s[100:101]
	s_waitcnt vmcnt(8)
	s_waitcnt lgkmcnt(0)
	s_barrier
; #define PG8_STAGE(bufoff, gbase, voff) do { _Pragma("unroll") for (int _i = 0; _i < 2; ++_i) \
;         __builtin_amdgcn_global_load_lds((const unsigned*)((const char*)(gbase) + (voff)[_i]), (PG8_LAS unsigned*)(lds + (bufoff) + ldsw + _i * 8192), 16, 0, 0); } while (0)
; #define PG8_LDA(dst, b, h) do { if constexpr (DT != 1) { _Pragma("unroll") for (int m = 0; m < 4; ++m) _Pragma("unroll") for (int k = 0; k < 2; ++k) dst[m][k] = *(const PG8_LAS bf16x8*)(lds + PG8_SA(b, h) + aoff + m * 2048 + k * 1024); } \
;         else { _Pragma("unroll") for (int m = 0; m < 4; ++m) dst##8[m] = ld32(lds + PG8_SA(b, h) + aoff + m * 2048); } } while (0)
; #define PG8_WAIT_V(n) asm volatile("s_waitcnt vmcnt(" #n ")" ::: "memory")
; #define PG8_WAIT_L(n) asm volatile("s_waitcnt lgkmcnt(" #n ")" ::: "memory")
; #define PG8_BAR __builtin_amdgcn_s_barrier()
; #define PG8_SCHED __builtin_amdgcn_sched_barrier(0)
;     __device__ __forceinline__ void operator()(const f32x4 (&acc)[2][2][4][2], const Unit& u, int wr, int wc, int fr, int fq) const {
;     ...
;                         const f32x4 o0 = b0 + acc[ai][bj][m][0] * s, o1 = b1 + acc[ai][bj][m][1] * s;
;     ...
;             PG8_WAIT_V(8); PG8_WAIT_L(0); PG8_BAR; PG8_MMA(0, 0, At, B0); PG8_MMA(0, 1, At, B1); PG8_BAR; PG8_SCHED;
;             PG8_LDA(At, 1, 1); PG8_STAGE(PG8_SB(1, 0), b3, voffB); PG8_STAGE(PG8_SB(1, 1), b3 + hstepB, voffB); PG8_STAGE(PG8_SA(1, 0), a3, voffA);
;             PG8_WAIT_V(8); PG8_WAIT_L(0); PG8_BAR; PG8_MMA(1, 0, At, B0); PG8_MMA(1, 1, At, B1); PG8_BAR; PG8_SCHED;
	s_setprio 1
	s_waitcnt lgkmcnt(0)
	v_mfma_f32_16x16x32_bf16 v[62:65], v[146:149], v[186:189], v[62:65]
	v_mfma_f32_16x16x32_bf16 v[58:61], v[154:157], v[186:189], v[58:61]
	v_mfma_f32_16x16x32_bf16 v[54:57], v[146:149], v[194:197], v[54:57]
	v_mfma_f32_16x16x32_bf16 v[50:53], v[154:157], v[194:197], v[50:53]
	v_mfma_f32_16x16x32_bf16 v[42:45], v[146:149], v[202:205], v[42:45]
	v_mfma_f32_16x16x32_bf16 v[34:37], v[154:157], v[202:205], v[34:37]
	v_mfma_f32_16x16x32_bf16 v[26:29], v[146:149], v[210:213], v[26:29]
	v_mfma_f32_16x16x32_bf16 v[18:21], v[154:157], v[210:213], v[18:21]
	v_mfma_f32_16x16x32_bf16 v[62:65], v[150:153], v[190:193], v[62:65]
	v_mfma_f32_16x16x32_bf16 v[58:61], v[158:161], v[190:193], v[58:61]
	v_mfma_f32_16x16x32_bf16 v[54:57], v[150:153], v[198:201], v[54:57]
	v_mfma_f32_16x16x32_bf16 v[50:53], v[158:161], v[198:201], v[50:53]
	v_mfma_f32_16x16x32_bf16 v[42:45], v[150:153], v[206:209], v[42:45]
	v_mfma_f32_16x16x32_bf16 v[34:37], v[158:161], v[206:209], v[34:37]
	v_mfma_f32_16x16x32_bf16 v[26:29], v[150:153], v[214:217], v[26:29]
	v_mfma_f32_16x16x32_bf16 v[18:21], v[158:161], v[214:217], v[18:21]
	v_mfma_f32_16x16x32_bf16 v[46:49], v[162:165], v[186:189], v[46:49]
	v_mfma_f32_16x16x32_bf16 v[38:41], v[178:181], v[186:189], v[38:41]
	v_mfma_f32_16x16x32_bf16 v[30:33], v[162:165], v[194:197], v[30:33]
	v_mfma_f32_16x16x32_bf16 v[22:25], v[178:181], v[194:197], v[22:25]
	v_mfma_f32_16x16x32_bf16 v[14:17], v[162:165], v[202:205], v[14:17]
	v_mfma_f32_16x16x32_bf16 v[10:13], v[178:181], v[202:205], v[10:13]
	v_mfma_f32_16x16x32_bf16 v[6:9], v[162:165], v[210:213], v[6:9]
	v_mfma_f32_16x16x32_bf16 v[2:5], v[178:181], v[210:213], v[2:5]
	v_mfma_f32_16x16x32_bf16 v[46:49], v[166:169], v[190:193], v[46:49]
	v_mfma_f32_16x16x32_bf16 v[38:41], v[182:185], v[190:193], v[38:41]
	v_mfma_f32_16x16x32_bf16 v[30:33], v[166:169], v[198:201], v[30:33]
	v_mfma_f32_16x16x32_bf16 v[22:25], v[182:185], v[198:201], v[22:25]
	v_mfma_f32_16x16x32_bf16 v[14:17], v[166:169], v[206:209], v[14:17]
	v_mfma_f32_16x16x32_bf16 v[10:13], v[182:185], v[206:209], v[10:13]
	v_mfma_f32_16x16x32_bf16 v[6:9], v[166:169], v[214:217], v[6:9]
	v_mfma_f32_16x16x32_bf16 v[2:5], v[182:185], v[214:217], v[2:5]
	s_setprio 0
	s_barrier
	s_add_u32 s65, s65, 0x100
	s_addc_u32 s66, s66, 0
	s_cmp_ge_i32 s67, s51
	s_mov_b64 s[26:27], s[28:29]
	s_mov_b32 s30, s67
	s_cbranch_scc0 .LBB0_922
	v_pk_mul_f32 v[128:129], v[128:129], 0.5 op_sel_hi:[1,0]
	v_pk_mul_f32 v[126:127], v[126:127], 0.5 op_sel_hi:[1,0]
	v_pk_mul_f32 v[124:125], v[124:125], 0.5 op_sel_hi:[1,0]
	v_pk_mul_f32 v[122:123], v[122:123], 0.5 op_sel_hi:[1,0]
	v_pk_mul_f32 v[152:153], v[112:113], 0.5 op_sel_hi:[1,0]
	v_pk_mul_f32 v[154:155], v[110:111], 0.5 op_sel_hi:[1,0]
	v_pk_mul_f32 v[156:157], v[104:105], 0.5 op_sel_hi:[1,0]
	v_pk_mul_f32 v[158:159], v[102:103], 0.5 op_sel_hi:[1,0]
	v_pk_mul_f32 v[120:121], v[120:121], 0.5 op_sel_hi:[1,0]
	v_pk_mul_f32 v[118:119], v[118:119], 0.5 op_sel_hi:[1,0]
	v_pk_mul_f32 v[116:117], v[116:117], 0.5 op_sel_hi:[1,0]
	v_pk_mul_f32 v[114:115], v[114:115], 0.5 op_sel_hi:[1,0]
	v_pk_mul_f32 v[160:161], v[96:97], 0.5 op_sel_hi:[1,0]
	v_pk_mul_f32 v[146:147], v[94:95], 0.5 op_sel_hi:[1,0]
	v_pk_mul_f32 v[150:151], v[88:89], 0.5 op_sel_hi:[1,0]
	v_pk_mul_f32 v[148:149], v[86:87], 0.5 op_sel_hi:[1,0]
	v_pk_mul_f32 v[94:95], v[108:109], 0.5 op_sel_hi:[1,0]
	v_pk_mul_f32 v[96:97], v[106:107], 0.5 op_sel_hi:[1,0]
	v_pk_mul_f32 v[100:101], v[100:101], 0.5 op_sel_hi:[1,0]
	v_pk_mul_f32 v[98:99], v[98:99], 0.5 op_sel_hi:[1,0]
	v_pk_mul_f32 v[106:107], v[80:81], 0.5 op_sel_hi:[1,0]
	v_pk_mul_f32 v[108:109], v[78:79], 0.5 op_sel_hi:[1,0]
	v_pk_mul_f32 v[110:111], v[76:77], 0.5 op_sel_hi:[1,0]
	v_pk_mul_f32 v[112:113], v[74:75], 0.5 op_sel_hi:[1,0]
	v_pk_mul_f32 v[74:75], v[92:93], 0.5 op_sel_hi:[1,0]
	v_pk_mul_f32 v[86:87], v[90:91], 0.5 op_sel_hi:[1,0]
	v_pk_mul_f32 v[84:85], v[84:85], 0.5 op_sel_hi:[1,0]
	v_pk_mul_f32 v[88:89], v[82:83], 0.5 op_sel_hi:[1,0]
	v_pk_mul_f32 v[90:91], v[72:73], 0.5 op_sel_hi:[1,0]
	v_pk_mul_f32 v[92:93], v[70:71], 0.5 op_sel_hi:[1,0]
	v_pk_mul_f32 v[102:103], v[68:69], 0.5 op_sel_hi:[1,0]
	v_pk_mul_f32 v[104:105], v[66:67], 0.5 op_sel_hi:[1,0]
	v_pk_mul_f32 v[72:73], v[64:65], 0.5 op_sel_hi:[1,0]
	v_pk_mul_f32 v[70:71], v[62:63], 0.5 op_sel_hi:[1,0]
	v_pk_mul_f32 v[82:83], v[60:61], 0.5 op_sel_hi:[1,0]
	v_pk_mul_f32 v[80:81], v[58:59], 0.5 op_sel_hi:[1,0]
	v_pk_mul_f32 v[68:69], v[48:49], 0.5 op_sel_hi:[1,0]
	v_pk_mul_f32 v[66:67], v[46:47], 0.5 op_sel_hi:[1,0]
	v_pk_mul_f32 v[78:79], v[40:41], 0.5 op_sel_hi:[1,0]
	v_pk_mul_f32 v[76:77], v[38:39], 0.5 op_sel_hi:[1,0]
	v_pk_mul_f32 v[56:57], v[56:57], 0.5 op_sel_hi:[1,0]
	v_pk_mul_f32 v[54:55], v[54:55], 0.5 op_sel_hi:[1,0]
	v_pk_mul_f32 v[64:65], v[52:53], 0.5 op_sel_hi:[1,0]
	v_pk_mul_f32 v[62:63], v[50:51], 0.5 op_sel_hi:[1,0]
	v_pk_mul_f32 v[52:53], v[32:33], 0.5 op_sel_hi:[1,0]
	v_pk_mul_f32 v[50:51], v[30:31], 0.5 op_sel_hi:[1,0]
	v_pk_mul_f32 v[60:61], v[24:25], 0.5 op_sel_hi:[1,0]
	v_pk_mul_f32 v[58:59], v[22:23], 0.5 op_sel_hi:[1,0]
	v_pk_mul_f32 v[40:41], v[44:45], 0.5 op_sel_hi:[1,0]
	v_pk_mul_f32 v[38:39], v[42:43], 0.5 op_sel_hi:[1,0]
	v_pk_mul_f32 v[48:49], v[36:37], 0.5 op_sel_hi:[1,0]
	v_pk_mul_f32 v[46:47], v[34:35], 0.5 op_sel_hi:[1,0]
	v_pk_mul_f32 v[36:37], v[16:17], 0.5 op_sel_hi:[1,0]
	v_pk_mul_f32 v[34:35], v[14:15], 0.5 op_sel_hi:[1,0]
	v_pk_mul_f32 v[44:45], v[12:13], 0.5 op_sel_hi:[1,0]
	v_pk_mul_f32 v[42:43], v[10:11], 0.5 op_sel_hi:[1,0]
	v_pk_mul_f32 v[24:25], v[28:29], 0.5 op_sel_hi:[1,0]
	v_pk_mul_f32 v[22:23], v[26:27], 0.5 op_sel_hi:[1,0]
	v_pk_mul_f32 v[32:33], v[20:21], 0.5 op_sel_hi:[1,0]
	v_pk_mul_f32 v[30:31], v[18:19], 0.5 op_sel_hi:[1,0]
	v_pk_mul_f32 v[20:21], v[8:9], 0.5 op_sel_hi:[1,0]
	v_pk_mul_f32 v[18:19], v[6:7], 0.5 op_sel_hi:[1,0]
	v_pk_mul_f32 v[28:29], v[4:5], 0.5 op_sel_hi:[1,0]
	v_pk_mul_f32 v[26:27], v[2:3], 0.5 op_sel_hi:[1,0]

; #define PG8_STAGE(bufoff, gbase, voff) do { _Pragma("unroll") for (int _i = 0; _i < 2; ++_i) \
;         __builtin_amdgcn_global_load_lds((const unsigned*)((const char*)(gbase) + (voff)[_i]), (PG8_LAS unsigned*)(lds + (bufoff) + ldsw + _i * 8192), 16, 0, 0); } while (0)
; #define PG8_LDA(dst, b, h) do { if constexpr (DT != 1) { _Pragma("unroll") for (int m = 0; m < 4; ++m) _Pragma("unroll") for (int k = 0; k < 2; ++k) dst[m][k] = *(const PG8_LAS bf16x8*)(lds + PG8_SA(b, h) + aoff + m * 2048 + k * 1024); } \
;         else { _Pragma("unroll") for (int m = 0; m < 4; ++m) dst##8[m] = ld32(lds + PG8_SA(b, h) + aoff + m * 2048); } } while (0)
; #define PG8_LDB(dst, b, h) do { if constexpr (DT != 1) { _Pragma("unroll") for (int n = 0; n < 2; ++n) _Pragma("unroll") for (int k = 0; k < 2; ++k) dst[n][k] = *(const PG8_LAS bf16x8*)(lds + PG8_SB(b, h) + boff + n * 2048 + k * 1024); } \
;         else { _Pragma("unroll") for (int n = 0; n < 2; ++n) dst##8[n] = ld32(lds + PG8_SB(b, h) + boff + n * 2048); } } while (0)
; #define PG8_WAIT_V(n) asm volatile("s_waitcnt vmcnt(" #n ")" ::: "memory")
; #define PG8_WAIT_L(n) asm volatile("s_waitcnt lgkmcnt(" #n ")" ::: "memory")
; #define PG8_BAR __builtin_amdgcn_s_barrier()
; #define PG8_SCHED __builtin_amdgcn_sched_barrier(0)
;     ...
;             PG8_LDB(B0, 0, 0); PG8_LDB(B1, 0, 1); PG8_SCHED; PG8_LDA(At, 0, 0); PG8_STAGE(PG8_SA(1, 1), a1 + hstepA, voffA);
;             PG8_WAIT_V(8); PG8_WAIT_L(0); PG8_BAR; PG8_MMA(0, 0, At, B0); PG8_MMA(0, 1, At, B1); PG8_BAR; PG8_SCHED;
;             PG8_LDA(At, 0, 1); PG8_STAGE(PG8_SB(0, 0), b2, voffB); PG8_STAGE(PG8_SB(0, 1), b2 + hstepB, voffB); PG8_STAGE(PG8_SA(0, 0), a2, voffA);
;             PG8_WAIT_V(8); PG8_WAIT_L(0); PG8_BAR; PG8_MMA(1, 0, At, B0); PG8_MMA(1, 1, At, B1); PG8_BAR; PG8_SCHED;
.LBB0_1412:
	v_add_u32_e32 v162, s35, v168
	v_add_u32_e32 v166, s36, v168
	ds_read_b128 v[150:153], v162
	ds_read_b128 v[154:157], v162 offset:1024
	ds_read_b128 v[158:161], v162 offset:2048
	ds_read_b128 v[162:165], v162 offset:3072
	ds_read_b128 v[178:181], v166
	ds_read_b128 v[182:185], v166 offset:1024
	ds_read_b128 v[186:189], v166 offset:2048
	ds_read_b128 v[190:193], v166 offset:3072
	s_add_i32 s68, s26, 2
	s_add_u32 s27, s24, 0xfffc0080
	s_addc_u32 s28, s25, -1
	s_cmp_eq_u32 s61, s26
	s_cselect_b32 s26, s65, s66
	s_cselect_b32 s29, s15, s28
	s_cselect_b32 s28, s17, s27
	s_cselect_b32 s27, s64, s67
	s_add_i32 m0, s46, 0xc000
	ds_read_b128 v[194:197], v177
	ds_read_b128 v[198:201], v177 offset:1024
	ds_read_b128 v[202:205], v177 offset:2048
	ds_read_b128 v[206:209], v177 offset:3072
	ds_read_b128 v[210:213], v177 offset:4096
	ds_read_b128 v[214:217], v177 offset:5120
	ds_read_b128 v[218:221], v177 offset:6144
	ds_read_b128 v[222:225], v177 offset:7168
	global_load_lds_dwordx4 v144, s[24:25]
	s_add_i32 m0, s46, 0xe000
	s_nop 0
	global_load_lds_dwordx4 v142, s[24:25]
	s_waitcnt vmcnt(8)
	s_waitcnt lgkmcnt(0)
	s_barrier
	s_setprio 1
	s_waitcnt lgkmcnt(0)
	v_mfma_i32_16x16x64_i8 v[126:129], v[150:153], v[194:197], v[126:129]
	v_mfma_i32_16x16x64_i8 v[122:125], v[158:161], v[194:197], v[122:125]
	v_mfma_i32_16x16x64_i8 v[118:121], v[150:153], v[202:205], v[118:121]
	v_mfma_i32_16x16x64_i8 v[114:117], v[158:161], v[202:205], v[114:117]
	v_mfma_i32_16x16x64_i8 v[106:109], v[150:153], v[210:213], v[106:109]
	v_mfma_i32_16x16x64_i8 v[98:101], v[158:161], v[210:213], v[98:101]
	v_mfma_i32_16x16x64_i8 v[90:93], v[150:153], v[218:221], v[90:93]
	v_mfma_i32_16x16x64_i8 v[82:85], v[158:161], v[218:221], v[82:85]
	v_mfma_i32_16x16x64_i8 v[126:129], v[154:157], v[198:201], v[126:129]
	v_mfma_i32_16x16x64_i8 v[122:125], v[162:165], v[198:201], v[122:125]
	v_mfma_i32_16x16x64_i8 v[118:121], v[154:157], v[206:209], v[118:121]
	v_mfma_i32_16x16x64_i8 v[114:117], v[162:165], v[206:209], v[114:117]
	v_mfma_i32_16x16x64_i8 v[106:109], v[154:157], v[214:217], v[106:109]
	v_mfma_i32_16x16x64_i8 v[98:101], v[162:165], v[214:217], v[98:101]
	v_mfma_i32_16x16x64_i8 v[90:93], v[154:157], v[222:225], v[90:93]
	v_mfma_i32_16x16x64_i8 v[82:85], v[162:165], v[222:225], v[82:85]
	v_mfma_i32_16x16x64_i8 v[110:113], v[178:181], v[194:197], v[110:113]
	v_mfma_i32_16x16x64_i8 v[102:105], v[186:189], v[194:197], v[102:105]
	v_mfma_i32_16x16x64_i8 v[94:97], v[178:181], v[202:205], v[94:97]
	v_mfma_i32_16x16x64_i8 v[86:89], v[186:189], v[202:205], v[86:89]
	v_mfma_i32_16x16x64_i8 v[78:81], v[178:181], v[210:213], v[78:81]
	v_mfma_i32_16x16x64_i8 v[74:77], v[186:189], v[210:213], v[74:77]
	v_mfma_i32_16x16x64_i8 v[70:73], v[178:181], v[218:221], v[70:73]
	v_mfma_i32_16x16x64_i8 v[66:69], v[186:189], v[218:221], v[66:69]
	v_mfma_i32_16x16x64_i8 v[110:113], v[182:185], v[198:201], v[110:113]
	v_mfma_i32_16x16x64_i8 v[102:105], v[190:193], v[198:201], v[102:105]
	v_mfma_i32_16x16x64_i8 v[94:97], v[182:185], v[206:209], v[94:97]
	v_mfma_i32_16x16x64_i8 v[86:89], v[190:193], v[206:209], v[86:89]
	v_mfma_i32_16x16x64_i8 v[78:81], v[182:185], v[214:217], v[78:81]
	v_mfma_i32_16x16x64_i8 v[74:77], v[190:193], v[214:217], v[74:77]
	v_mfma_i32_16x16x64_i8 v[70:73], v[182:185], v[222:225], v[70:73]
	v_mfma_i32_16x16x64_i8 v[66:69], v[190:193], v[222:225], v[66:69]
	s_setprio 0
	s_barrier
	s_mov_b32 m0, s23
	s_add_u32 s98, s26, 0x80
	s_addc_u32 s99, s27, 0
	s_add_u32 s70, s26, 0x40000
	ds_read_b128 v[194:197], v177 offset:16384
	ds_read_b128 v[198:201], v177 offset:17408
	ds_read_b128 v[202:205], v177 offset:18432
	ds_read_b128 v[206:209], v177 offset:19456
	ds_read_b128 v[210:213], v177 offset:20480
	ds_read_b128 v[214:217], v177 offset:21504
	ds_read_b128 v[218:221], v177 offset:22528
	ds_read_b128 v[222:225], v177 offset:23552
	global_load_lds_dwordx4 v132, s[26:27]
	s_mov_b32 m0, s43
	s_addc_u32 s71, s27, 0
	global_load_lds_dwordx4 v136, s[26:27]
	s_mov_b32 m0, s44
	s_nop 0
	global_load_lds_dwordx4 v132, s[70:71]
	s_mov_b32 m0, s45
	s_nop 0
	global_load_lds_dwordx4 v136, s[70:71]
	s_add_u32 s100, s28, 0x80
	s_addc_u32 s101, s29, 0
	s_mov_b32 m0, s46
	s_nop 0
	global_load_lds_dwordx4 v130, s[28:29]
	s_mov_b32 m0, s47
	s_nop 0
	global_load_lds_dwordx4 v134, s[28:29]
	s_waitcnt vmcnt(8)
	s_waitcnt lgkmcnt(0)
	s_barrier
	s_setprio 1
	s_waitcnt lgkmcnt(0)
	v_mfma_i32_16x16x64_i8 v[62:65], v[150:153], v[194:197], v[62:65]
	v_mfma_i32_16x16x64_i8 v[58:61], v[158:161], v[194:197], v[58:61]
	v_mfma_i32_16x16x64_i8 v[54:57], v[150:153], v[202:205], v[54:57]
	v_mfma_i32_16x16x64_i8 v[50:53], v[158:161], v[202:205], v[50:53]
	v_mfma_i32_16x16x64_i8 v[42:45], v[150:153], v[210:213], v[42:45]
	v_mfma_i32_16x16x64_i8 v[34:37], v[158:161], v[210:213], v[34:37]
	v_mfma_i32_16x16x64_i8 v[26:29], v[150:153], v[218:221], v[26:29]
	v_mfma_i32_16x16x64_i8 v[18:21], v[158:161], v[218:221], v[18:21]
	v_mfma_i32_16x16x64_i8 v[62:65], v[154:157], v[198:201], v[62:65]
	v_mfma_i32_16x16x64_i8 v[58:61], v[162:165], v[198:201], v[58:61]
	v_mfma_i32_16x16x64_i8 v[54:57], v[154:157], v[206:209], v[54:57]
	v_mfma_i32_16x16x64_i8 v[50:53], v[162:165], v[206:209], v[50:53]
	v_mfma_i32_16x16x64_i8 v[42:45], v[154:157], v[214:217], v[42:45]
	v_mfma_i32_16x16x64_i8 v[34:37], v[162:165], v[214:217], v[34:37]
	v_mfma_i32_16x16x64_i8 v[26:29], v[154:157], v[222:225], v[26:29]
	v_mfma_i32_16x16x64_i8 v[18:21], v[162:165], v[222:225], v[18:21]
	v_mfma_i32_16x16x64_i8 v[46:49], v[178:181], v[194:197], v[46:49]
	v_mfma_i32_16x16x64_i8 v[38:41], v[186:189], v[194:197], v[38:41]
	v_mfma_i32_16x16x64_i8 v[30:33], v[178:181], v[202:205], v[30:33]
	v_mfma_i32_16x16x64_i8 v[22:25], v[186:189], v[202:205], v[22:25]
	v_mfma_i32_16x16x64_i8 v[14:17], v[178:181], v[210:213], v[14:17]
	v_mfma_i32_16x16x64_i8 v[10:13], v[186:189], v[210:213], v[10:13]
	v_mfma_i32_16x16x64_i8 v[6:9], v[178:181], v[218:221], v[6:9]
	v_mfma_i32_16x16x64_i8 v[2:5], v[186:189], v[218:221], v[2:5]
	v_mfma_i32_16x16x64_i8 v[46:49], v[182:185], v[198:201], v[46:49]
	v_mfma_i32_16x16x64_i8 v[38:41], v[190:193], v[198:201], v[38:41]
	v_mfma_i32_16x16x64_i8 v[30:33], v[182:185], v[206:209], v[30:33]
	v_mfma_i32_16x16x64_i8 v[22:25], v[190:193], v[206:209], v[22:25]
	v_mfma_i32_16x16x64_i8 v[14:17], v[182:185], v[214:217], v[14:17]
	v_mfma_i32_16x16x64_i8 v[10:13], v[190:193], v[214:217], v[10:13]
	v_mfma_i32_16x16x64_i8 v[6:9], v[182:185], v[222:225], v[6:9]
	v_mfma_i32_16x16x64_i8 v[2:5], v[190:193], v[222:225], v[2:5]
	s_setprio 0
	s_barrier
; #define PG8_STAGE(bufoff, gbase, voff) do { _Pragma("unroll") for (int _i = 0; _i < 2; ++_i) \
;         __builtin_amdgcn_global_load_lds((const unsigned*)((const char*)(gbase) + (voff)[_i]), (PG8_LAS unsigned*)(lds + (bufoff) + ldsw + _i * 8192), 16, 0, 0); } while (0)
; #define PG8_LDA(dst, b, h) do { if constexpr (DT != 1) { _Pragma("unroll") for (int m = 0; m < 4; ++m) _Pragma("unroll") for (int k = 0; k < 2; ++k) dst[m][k] = *(const PG8_LAS bf16x8*)(lds + PG8_SA(b, h) + aoff + m * 2048 + k * 1024); } \
;         else { _Pragma("unroll") for (int m = 0; m < 4; ++m) dst##8[m] = ld32(lds + PG8_SA(b, h) + aoff + m * 2048); } } while (0)
; #define PG8_LDB(dst, b, h) do { if constexpr (DT != 1) { _Pragma("unroll") for (int n = 0; n < 2; ++n) _Pragma("unroll") for (int k = 0; k < 2; ++k) dst[n][k] = *(const PG8_LAS bf16x8*)(lds + PG8_SB(b, h) + boff + n * 2048 + k * 1024); } \
;         else { _Pragma("unroll") for (int n = 0; n < 2; ++n) dst##8[n] = ld32(lds + PG8_SB(b, h) + boff + n * 2048); } } while (0)
; #define PG8_WAIT_V(n) asm volatile("s_waitcnt vmcnt(" #n ")" ::: "memory")
; #define PG8_WAIT_L(n) asm volatile("s_waitcnt lgkmcnt(" #n ")" ::: "memory")
; #define PG8_BAR __builtin_amdgcn_s_barrier()
; #define PG8_SCHED __builtin_amdgcn_sched_barrier(0)
;     ...
;             PG8_LDB(B0, 1, 0); PG8_LDB(B1, 1, 1); PG8_SCHED; PG8_LDA(At, 1, 0); PG8_STAGE(PG8_SA(0, 1), a2 + hstepA, voffA);
;             PG8_WAIT_V(8); PG8_WAIT_L(0); PG8_BAR; PG8_MMA(0, 0, At, B0); PG8_MMA(0, 1, At, B1); PG8_BAR; PG8_SCHED;
;             PG8_LDA(At, 1, 1); PG8_STAGE(PG8_SB(1, 0), b3, voffB); PG8_STAGE(PG8_SB(1, 1), b3 + hstepB, voffB); PG8_STAGE(PG8_SA(1, 0), a3, voffA);
	v_add_u32_e32 v162, s51, v168
	v_add_u32_e32 v190, s52, v168
	ds_read_b128 v[150:153], v162
	ds_read_b128 v[154:157], v162 offset:1024
	ds_read_b128 v[158:161], v162 offset:2048
	ds_read_b128 v[162:165], v162 offset:3072
	ds_read_b128 v[178:181], v190
	ds_read_b128 v[182:185], v190 offset:1024
	ds_read_b128 v[186:189], v190 offset:2048
	ds_read_b128 v[190:193], v190 offset:3072
	s_add_u32 s28, s28, 0x40000
	s_addc_u32 s29, s29, 0
	s_mov_b32 m0, s48
	ds_read_b128 v[194:197], v177 offset:32768
	ds_read_b128 v[198:201], v177 offset:33792
	ds_read_b128 v[202:205], v177 offset:34816
	ds_read_b128 v[206:209], v177 offset:35840
	ds_read_b128 v[210:213], v177 offset:36864
	ds_read_b128 v[214:217], v177 offset:37888
	ds_read_b128 v[218:221], v177 offset:38912
	ds_read_b128 v[222:225], v177 offset:39936
	global_load_lds_dwordx4 v130, s[28:29]
	s_mov_b32 m0, s49
	s_nop 0
	global_load_lds_dwordx4 v134, s[28:29]
	s_waitcnt vmcnt(8)
	s_waitcnt lgkmcnt(0)
	s_barrier
	s_setprio 1
	s_waitcnt lgkmcnt(0)
	v_mfma_i32_16x16x64_i8 v[126:129], v[150:153], v[194:197], v[126:129]
	v_mfma_i32_16x16x64_i8 v[122:125], v[158:161], v[194:197], v[122:125]
	v_mfma_i32_16x16x64_i8 v[118:121], v[150:153], v[202:205], v[118:121]
	v_mfma_i32_16x16x64_i8 v[114:117], v[158:161], v[202:205], v[114:117]
	v_mfma_i32_16x16x64_i8 v[106:109], v[150:153], v[210:213], v[106:109]
	v_mfma_i32_16x16x64_i8 v[98:101], v[158:161], v[210:213], v[98:101]
	v_mfma_i32_16x16x64_i8 v[90:93], v[150:153], v[218:221], v[90:93]
	v_mfma_i32_16x16x64_i8 v[82:85], v[158:161], v[218:221], v[82:85]
	v_mfma_i32_16x16x64_i8 v[126:129], v[154:157], v[198:201], v[126:129]
	v_mfma_i32_16x16x64_i8 v[122:125], v[162:165], v[198:201], v[122:125]
	v_mfma_i32_16x16x64_i8 v[118:121], v[154:157], v[206:209], v[118:121]
	v_mfma_i32_16x16x64_i8 v[114:117], v[162:165], v[206:209], v[114:117]
	v_mfma_i32_16x16x64_i8 v[106:109], v[154:157], v[214:217], v[106:109]
	v_mfma_i32_16x16x64_i8 v[98:101], v[162:165], v[214:217], v[98:101]
	v_mfma_i32_16x16x64_i8 v[90:93], v[154:157], v[222:225], v[90:93]
	v_mfma_i32_16x16x64_i8 v[82:85], v[162:165], v[222:225], v[82:85]
	v_mfma_i32_16x16x64_i8 v[110:113], v[178:181], v[194:197], v[110:113]
	v_mfma_i32_16x16x64_i8 v[102:105], v[186:189], v[194:197], v[102:105]
	v_mfma_i32_16x16x64_i8 v[94:97], v[178:181], v[202:205], v[94:97]
	v_mfma_i32_16x16x64_i8 v[86:89], v[186:189], v[202:205], v[86:89]
	v_mfma_i32_16x16x64_i8 v[78:81], v[178:181], v[210:213], v[78:81]
	v_mfma_i32_16x16x64_i8 v[74:77], v[186:189], v[210:213], v[74:77]
	v_mfma_i32_16x16x64_i8 v[70:73], v[178:181], v[218:221], v[70:73]
	v_mfma_i32_16x16x64_i8 v[66:69], v[186:189], v[218:221], v[66:69]
	v_mfma_i32_16x16x64_i8 v[110:113], v[182:185], v[198:201], v[110:113]
	v_mfma_i32_16x16x64_i8 v[102:105], v[190:193], v[198:201], v[102:105]
	v_mfma_i32_16x16x64_i8 v[94:97], v[182:185], v[206:209], v[94:97]
	v_mfma_i32_16x16x64_i8 v[86:89], v[190:193], v[206:209], v[86:89]
	v_mfma_i32_16x16x64_i8 v[78:81], v[182:185], v[214:217], v[78:81]
	v_mfma_i32_16x16x64_i8 v[74:77], v[190:193], v[214:217], v[74:77]
	v_mfma_i32_16x16x64_i8 v[70:73], v[182:185], v[222:225], v[70:73]
	v_mfma_i32_16x16x64_i8 v[66:69], v[190:193], v[222:225], v[66:69]
	s_setprio 0
	s_barrier
	s_mov_b32 m0, s55
	s_add_u32 s26, s26, 0x40080
	ds_read_b128 v[194:197], v177 offset:49152
	ds_read_b128 v[198:201], v177 offset:50176
	ds_read_b128 v[202:205], v177 offset:51200
	ds_read_b128 v[206:209], v177 offset:52224
	ds_read_b128 v[210:213], v177 offset:53248
	ds_read_b128 v[214:217], v177 offset:54272
	ds_read_b128 v[218:221], v177 offset:55296
	ds_read_b128 v[222:225], v177 offset:56320
	global_load_lds_dwordx4 v132, s[98:99]
	s_mov_b32 m0, s56
	s_addc_u32 s27, s27, 0
	global_load_lds_dwordx4 v136, s[98:99]
	s_mov_b32 m0, s59
	s_nop 0
	global_load_lds_dwordx4 v132, s[26:27]
	s_mov_b32 m0, s60
	s_nop 0
	global_load_lds_dwordx4 v136, s[26:27]
	s_mov_b32 m0, s57
	s_nop 0
	global_load_lds_dwordx4 v130, s[100:101]
	s_mov_b32 m0, s58
	s_nop 0
	global_load_lds_dwordx4 v134, s[100:101]
	s_waitcnt vmcnt(8)
	s_waitcnt lgkmcnt(0)
	s_barrier
; #define PG8_WAIT_V(n) asm volatile("s_waitcnt vmcnt(" #n ")" ::: "memory")
; #define PG8_WAIT_L(n) asm volatile("s_waitcnt lgkmcnt(" #n ")" ::: "memory")
; #define PG8_BAR __builtin_amdgcn_s_barrier()
; #define PG8_SCHED __builtin_amdgcn_sched_barrier(0)
; __device__ __forceinline__ f32x4 i32bits_to_f32(f32x4 v) { return (f32x4){(float)__float_as_int(v.x), (float)__float_as_int(v.y), (float)__float_as_int(v.z), (float)__float_as_int(v.w)}; }
;     ...
;             PG8_WAIT_V(8); PG8_WAIT_L(0); PG8_BAR; PG8_MMA(1, 0, At, B0); PG8_MMA(1, 1, At, B1); PG8_BAR; PG8_SCHED;
	s_setprio 1
	s_waitcnt lgkmcnt(0)
	v_mfma_i32_16x16x64_i8 v[62:65], v[150:153], v[194:197], v[62:65]
	v_mfma_i32_16x16x64_i8 v[58:61], v[158:161], v[194:197], v[58:61]
	v_mfma_i32_16x16x64_i8 v[54:57], v[150:153], v[202:205], v[54:57]
	v_mfma_i32_16x16x64_i8 v[50:53], v[158:161], v[202:205], v[50:53]
	v_mfma_i32_16x16x64_i8 v[42:45], v[150:153], v[210:213], v[42:45]
	v_mfma_i32_16x16x64_i8 v[34:37], v[158:161], v[210:213], v[34:37]
	v_mfma_i32_16x16x64_i8 v[26:29], v[150:153], v[218:221], v[26:29]
	v_mfma_i32_16x16x64_i8 v[18:21], v[158:161], v[218:221], v[18:21]
	v_mfma_i32_16x16x64_i8 v[62:65], v[154:157], v[198:201], v[62:65]
	v_mfma_i32_16x16x64_i8 v[58:61], v[162:165], v[198:201], v[58:61]
	v_mfma_i32_16x16x64_i8 v[54:57], v[154:157], v[206:209], v[54:57]
	v_mfma_i32_16x16x64_i8 v[50:53], v[162:165], v[206:209], v[50:53]
	v_mfma_i32_16x16x64_i8 v[42:45], v[154:157], v[214:217], v[42:45]
	v_mfma_i32_16x16x64_i8 v[34:37], v[162:165], v[214:217], v[34:37]
	v_mfma_i32_16x16x64_i8 v[26:29], v[154:157], v[222:225], v[26:29]
	v_mfma_i32_16x16x64_i8 v[18:21], v[162:165], v[222:225], v[18:21]
	v_mfma_i32_16x16x64_i8 v[46:49], v[178:181], v[194:197], v[46:49]
	v_mfma_i32_16x16x64_i8 v[38:41], v[186:189], v[194:197], v[38:41]
	v_mfma_i32_16x16x64_i8 v[30:33], v[178:181], v[202:205], v[30:33]
	v_mfma_i32_16x16x64_i8 v[22:25], v[186:189], v[202:205], v[22:25]
	v_mfma_i32_16x16x64_i8 v[14:17], v[178:181], v[210:213], v[14:17]
	v_mfma_i32_16x16x64_i8 v[10:13], v[186:189], v[210:213], v[10:13]
	v_mfma_i32_16x16x64_i8 v[6:9], v[178:181], v[218:221], v[6:9]
	v_mfma_i32_16x16x64_i8 v[2:5], v[186:189], v[218:221], v[2:5]
	v_mfma_i32_16x16x64_i8 v[46:49], v[182:185], v[198:201], v[46:49]
	v_mfma_i32_16x16x64_i8 v[38:41], v[190:193], v[198:201], v[38:41]
	v_mfma_i32_16x16x64_i8 v[30:33], v[182:185], v[206:209], v[30:33]
	v_mfma_i32_16x16x64_i8 v[22:25], v[190:193], v[206:209], v[22:25]
	v_mfma_i32_16x16x64_i8 v[14:17], v[182:185], v[214:217], v[14:17]
	v_mfma_i32_16x16x64_i8 v[10:13], v[190:193], v[214:217], v[10:13]
	v_mfma_i32_16x16x64_i8 v[6:9], v[182:185], v[222:225], v[6:9]
	v_mfma_i32_16x16x64_i8 v[2:5], v[190:193], v[222:225], v[2:5]
	s_setprio 0
	s_barrier
	s_add_u32 s66, s66, 0x100
	s_addc_u32 s67, s67, 0
	s_add_u32 s24, s24, 0x100
	s_addc_u32 s25, s25, 0
	s_cmp_ge_i32 s68, s54
	s_mov_b32 s26, s68
	s_cbranch_scc0 .LBB0_1412
	v_cvt_f32_i32_e32 v150, v126
	v_cvt_f32_i32_e32 v151, v127
	v_cvt_f32_i32_e32 v126, v128
	v_cvt_f32_i32_e32 v127, v129
	v_cvt_f32_i32_e32 v122, v122
	v_cvt_f32_i32_e32 v123, v123
	v_cvt_f32_i32_e32 v124, v124
	v_cvt_f32_i32_e32 v125, v125
	v_cvt_f32_i32_e32 v158, v110
	v_cvt_f32_i32_e32 v159, v111
	v_cvt_f32_i32_e32 v160, v112
	v_cvt_f32_i32_e32 v161, v113
	v_cvt_f32_i32_e32 v162, v102
	v_cvt_f32_i32_e32 v163, v103
	v_cvt_f32_i32_e32 v164, v104
	v_cvt_f32_i32_e32 v165, v105
	v_cvt_f32_i32_e32 v152, v118
	v_cvt_f32_i32_e32 v153, v119
	v_cvt_f32_i32_e32 v154, v120
	v_cvt_f32_i32_e32 v155, v121
	v_cvt_f32_i32_e32 v128, v114
	v_cvt_f32_i32_e32 v129, v115
	v_cvt_f32_i32_e32 v156, v116
	v_cvt_f32_i32_e32 v157, v117
	v_cvt_f32_i32_e32 v116, v94
	v_cvt_f32_i32_e32 v117, v95
	v_cvt_f32_i32_e32 v120, v96
	v_cvt_f32_i32_e32 v121, v97
	v_cvt_f32_i32_e32 v114, v86
	v_cvt_f32_i32_e32 v115, v87
	v_cvt_f32_i32_e32 v118, v88
	v_cvt_f32_i32_e32 v119, v89
	v_cvt_f32_i32_e32 v102, v106
	v_cvt_f32_i32_e32 v103, v107
	v_cvt_f32_i32_e32 v104, v108
	v_cvt_f32_i32_e32 v105, v109
	v_cvt_f32_i32_e32 v98, v98
	v_cvt_f32_i32_e32 v99, v99
	v_cvt_f32_i32_e32 v100, v100
	v_cvt_f32_i32_e32 v101, v101
	v_cvt_f32_i32_e32 v108, v78
	v_cvt_f32_i32_e32 v109, v79
	v_cvt_f32_i32_e32 v112, v80
	v_cvt_f32_i32_e32 v113, v81
	v_cvt_f32_i32_e32 v106, v74
	v_cvt_f32_i32_e32 v107, v75
	v_cvt_f32_i32_e32 v110, v76
	v_cvt_f32_i32_e32 v111, v77
	v_cvt_f32_i32_e32 v76, v90
	v_cvt_f32_i32_e32 v77, v91
	v_cvt_f32_i32_e32 v80, v92
	v_cvt_f32_i32_e32 v81, v93
	v_cvt_f32_i32_e32 v74, v82
	v_cvt_f32_i32_e32 v75, v83
	v_cvt_f32_i32_e32 v78, v84
	v_cvt_f32_i32_e32 v79, v85
	v_cvt_f32_i32_e32 v92, v70
	v_cvt_f32_i32_e32 v93, v71
	v_cvt_f32_i32_e32 v96, v72
	v_cvt_f32_i32_e32 v97, v73
	v_cvt_f32_i32_e32 v90, v66
	v_cvt_f32_i32_e32 v91, v67
	v_cvt_f32_i32_e32 v94, v68
	v_cvt_f32_i32_e32 v95, v69
	v_cvt_f32_i32_e32 v68, v62
	v_cvt_f32_i32_e32 v69, v63
	v_cvt_f32_i32_e32 v72, v64
	v_cvt_f32_i32_e32 v73, v65
	v_cvt_f32_i32_e32 v66, v58
	v_cvt_f32_i32_e32 v67, v59
	v_cvt_f32_i32_e32 v70, v60
	v_cvt_f32_i32_e32 v71, v61
	v_cvt_f32_i32_e32 v84, v46
	v_cvt_f32_i32_e32 v85, v47
	v_cvt_f32_i32_e32 v88, v48
	v_cvt_f32_i32_e32 v89, v49
	v_cvt_f32_i32_e32 v82, v38
	v_cvt_f32_i32_e32 v83, v39
	v_cvt_f32_i32_e32 v86, v40
	v_cvt_f32_i32_e32 v87, v41
	v_cvt_f32_i32_e32 v54, v54
	v_cvt_f32_i32_e32 v55, v55
	v_cvt_f32_i32_e32 v56, v56
	v_cvt_f32_i32_e32 v57, v57
	v_cvt_f32_i32_e32 v50, v50
	v_cvt_f32_i32_e32 v51, v51
	v_cvt_f32_i32_e32 v52, v52
	v_cvt_f32_i32_e32 v53, v53
	v_cvt_f32_i32_e32 v60, v30
	v_cvt_f32_i32_e32 v61, v31
	v_cvt_f32_i32_e32 v64, v32
	v_cvt_f32_i32_e32 v65, v33
	v_cvt_f32_i32_e32 v58, v22
	v_cvt_f32_i32_e32 v59, v23
	v_cvt_f32_i32_e32 v62, v24
	v_cvt_f32_i32_e32 v63, v25
	v_cvt_f32_i32_e32 v38, v42
	v_cvt_f32_i32_e32 v39, v43
	v_cvt_f32_i32_e32 v40, v44
	v_cvt_f32_i32_e32 v41, v45
	v_cvt_f32_i32_e32 v34, v34
	v_cvt_f32_i32_e32 v35, v35
	v_cvt_f32_i32_e32 v36, v36
	v_cvt_f32_i32_e32 v37, v37
	v_cvt_f32_i32_e32 v44, v14
	v_cvt_f32_i32_e32 v45, v15
	v_cvt_f32_i32_e32 v48, v16
	v_cvt_f32_i32_e32 v49, v17
	v_cvt_f32_i32_e32 v42, v10
	v_cvt_f32_i32_e32 v43, v11
	v_cvt_f32_i32_e32 v46, v12
	v_cvt_f32_i32_e32 v47, v13
	v_cvt_f32_i32_e32 v22, v26
	v_cvt_f32_i32_e32 v23, v27
	v_cvt_f32_i32_e32 v24, v28
	v_cvt_f32_i32_e32 v25, v29
	v_cvt_f32_i32_e32 v18, v18
	v_cvt_f32_i32_e32 v19, v19
	v_cvt_f32_i32_e32 v20, v20
	v_cvt_f32_i32_e32 v21, v21
	v_cvt_f32_i32_e32 v28, v6
	v_cvt_f32_i32_e32 v29, v7
	v_cvt_f32_i32_e32 v32, v8
	v_cvt_f32_i32_e32 v33, v9
	v_cvt_f32_i32_e32 v26, v2
	v_cvt_f32_i32_e32 v27, v3
	v_cvt_f32_i32_e32 v30, v4
	v_cvt_f32_i32_e32 v31, v5

; #define PG8_STAGE(bufoff, gbase, voff) do { _Pragma("unroll") for (int _i = 0; _i < 2; ++_i) \
;         __builtin_amdgcn_global_load_lds((const unsigned*)((const char*)(gbase) + (voff)[_i]), (PG8_LAS unsigned*)(lds + (bufoff) + ldsw + _i * 8192), 16, 0, 0); } while (0)
; #define PG8_LDA(dst, b, h) do { if constexpr (DT != 1) { _Pragma("unroll") for (int m = 0; m < 4; ++m) _Pragma("unroll") for (int k = 0; k < 2; ++k) dst[m][k] = *(const PG8_LAS bf16x8*)(lds + PG8_SA(b, h) + aoff + m * 2048 + k * 1024); } \
;         else { _Pragma("unroll") for (int m = 0; m < 4; ++m) dst##8[m] = ld32(lds + PG8_SA(b, h) + aoff + m * 2048); } } while (0)
; #define PG8_LDB(dst, b, h) do { if constexpr (DT != 1) { _Pragma("unroll") for (int n = 0; n < 2; ++n) _Pragma("unroll") for (int k = 0; k < 2; ++k) dst[n][k] = *(const PG8_LAS bf16x8*)(lds + PG8_SB(b, h) + boff + n * 2048 + k * 1024); } \
;         else { _Pragma("unroll") for (int n = 0; n < 2; ++n) dst##8[n] = ld32(lds + PG8_SB(b, h) + boff + n * 2048); } } while (0)
; #define PG8_WAIT_V(n) asm volatile("s_waitcnt vmcnt(" #n ")" ::: "memory")
; #define PG8_WAIT_L(n) asm volatile("s_waitcnt lgkmcnt(" #n ")" ::: "memory")
; #define PG8_BAR __builtin_amdgcn_s_barrier()
; #define PG8_SCHED __builtin_amdgcn_sched_barrier(0)
;     ...
;             PG8_LDB(B0, 0, 0); PG8_LDB(B1, 0, 1); PG8_SCHED; PG8_LDA(At, 0, 0); PG8_STAGE(PG8_SA(1, 1), a1 + hstepA, voffA);
;             PG8_WAIT_V(8); PG8_WAIT_L(0); PG8_BAR; PG8_MMA(0, 0, At, B0); PG8_MMA(0, 1, At, B1); PG8_BAR; PG8_SCHED;
;             PG8_LDA(At, 0, 1); PG8_STAGE(PG8_SB(0, 0), b2, voffB); PG8_STAGE(PG8_SB(0, 1), b2 + hstepB, voffB); PG8_STAGE(PG8_SA(0, 0), a2, voffA);
;             PG8_WAIT_V(8); PG8_WAIT_L(0); PG8_BAR; PG8_MMA(1, 0, At, B0); PG8_MMA(1, 1, At, B1); PG8_BAR; PG8_SCHED;
.LBB0_2262:
	ds_read_b128 v[154:157], v148
	ds_read_b128 v[158:161], v148 offset:1024
	ds_read_b128 v[162:165], v148 offset:2048
	ds_read_b128 v[166:169], v148 offset:3072
	ds_read_b128 v[170:173], v149
	ds_read_b128 v[174:177], v149 offset:1024
	ds_read_b128 v[178:181], v149 offset:2048
	ds_read_b128 v[182:185], v149 offset:3072
	s_add_i32 s65, s28, 2
	s_add_u32 s29, s26, 0xfff80080
	s_addc_u32 s30, s27, -1
	s_cmp_eq_u32 s61, s28
	s_cselect_b32 s28, s23, s25
	s_cselect_b32 s31, s2, s30
	s_cselect_b32 s30, s15, s29
	s_cselect_b32 s29, s17, s64
	s_add_i32 m0, s44, 0xc000
	ds_read_b128 v[186:189], v150
	ds_read_b128 v[190:193], v150 offset:1024
	ds_read_b128 v[194:197], v150 offset:2048
	ds_read_b128 v[198:201], v150 offset:3072
	ds_read_b128 v[202:205], v150 offset:4096
	ds_read_b128 v[206:209], v150 offset:5120
	ds_read_b128 v[210:213], v150 offset:6144
	ds_read_b128 v[214:217], v150 offset:7168
	global_load_lds_dwordx4 v142, s[26:27]
	s_add_i32 m0, s44, 0xe000
	s_nop 0
	global_load_lds_dwordx4 v140, s[26:27]
	s_waitcnt vmcnt(8)
	s_waitcnt lgkmcnt(0)
	s_barrier
	s_setprio 1
	s_waitcnt lgkmcnt(0)
	v_mfma_f32_16x16x32_bf16 v[126:129], v[154:157], v[186:189], v[126:129]
	v_mfma_f32_16x16x32_bf16 v[122:125], v[162:165], v[186:189], v[122:125]
	v_mfma_f32_16x16x32_bf16 v[110:113], v[154:157], v[194:197], v[110:113]
	v_mfma_f32_16x16x32_bf16 v[106:109], v[162:165], v[194:197], v[106:109]
	v_mfma_f32_16x16x32_bf16 v[94:97], v[154:157], v[202:205], v[94:97]
	v_mfma_f32_16x16x32_bf16 v[90:93], v[162:165], v[202:205], v[90:93]
	v_mfma_f32_16x16x32_bf16 v[78:81], v[154:157], v[210:213], v[78:81]
	v_mfma_f32_16x16x32_bf16 v[74:77], v[162:165], v[210:213], v[74:77]
	v_mfma_f32_16x16x32_bf16 v[126:129], v[158:161], v[190:193], v[126:129]
	v_mfma_f32_16x16x32_bf16 v[122:125], v[166:169], v[190:193], v[122:125]
	v_mfma_f32_16x16x32_bf16 v[110:113], v[158:161], v[198:201], v[110:113]
	v_mfma_f32_16x16x32_bf16 v[106:109], v[166:169], v[198:201], v[106:109]
	v_mfma_f32_16x16x32_bf16 v[94:97], v[158:161], v[206:209], v[94:97]
	v_mfma_f32_16x16x32_bf16 v[90:93], v[166:169], v[206:209], v[90:93]
	v_mfma_f32_16x16x32_bf16 v[78:81], v[158:161], v[214:217], v[78:81]
	v_mfma_f32_16x16x32_bf16 v[74:77], v[166:169], v[214:217], v[74:77]
	v_mfma_f32_16x16x32_bf16 v[118:121], v[170:173], v[186:189], v[118:121]
	v_mfma_f32_16x16x32_bf16 v[114:117], v[178:181], v[186:189], v[114:117]
	v_mfma_f32_16x16x32_bf16 v[102:105], v[170:173], v[194:197], v[102:105]
	v_mfma_f32_16x16x32_bf16 v[98:101], v[178:181], v[194:197], v[98:101]
	v_mfma_f32_16x16x32_bf16 v[86:89], v[170:173], v[202:205], v[86:89]
	v_mfma_f32_16x16x32_bf16 v[82:85], v[178:181], v[202:205], v[82:85]
	v_mfma_f32_16x16x32_bf16 v[70:73], v[170:173], v[210:213], v[70:73]
	v_mfma_f32_16x16x32_bf16 v[66:69], v[178:181], v[210:213], v[66:69]
	v_mfma_f32_16x16x32_bf16 v[118:121], v[174:177], v[190:193], v[118:121]
	v_mfma_f32_16x16x32_bf16 v[114:117], v[182:185], v[190:193], v[114:117]
	v_mfma_f32_16x16x32_bf16 v[102:105], v[174:177], v[198:201], v[102:105]
	v_mfma_f32_16x16x32_bf16 v[98:101], v[182:185], v[198:201], v[98:101]
	v_mfma_f32_16x16x32_bf16 v[86:89], v[174:177], v[206:209], v[86:89]
	v_mfma_f32_16x16x32_bf16 v[82:85], v[182:185], v[206:209], v[82:85]
	v_mfma_f32_16x16x32_bf16 v[70:73], v[174:177], v[214:217], v[70:73]
	v_mfma_f32_16x16x32_bf16 v[66:69], v[182:185], v[214:217], v[66:69]
	s_setprio 0
	s_barrier
	s_mov_b32 m0, s40
	s_add_u32 s98, s28, 0x80
	s_addc_u32 s99, s29, 0
	s_add_u32 s66, s28, 0x80000
	ds_read_b128 v[186:189], v150 offset:16384
	ds_read_b128 v[190:193], v150 offset:17408
	ds_read_b128 v[194:197], v150 offset:18432
	ds_read_b128 v[198:201], v150 offset:19456
	ds_read_b128 v[202:205], v150 offset:20480
	ds_read_b128 v[206:209], v150 offset:21504
	ds_read_b128 v[210:213], v150 offset:22528
	ds_read_b128 v[214:217], v150 offset:23552
	global_load_lds_dwordx4 v132, s[28:29]
	s_mov_b32 m0, s41
	s_addc_u32 s67, s29, 0
	global_load_lds_dwordx4 v136, s[28:29]
	s_mov_b32 m0, s42
	s_nop 0
	global_load_lds_dwordx4 v132, s[66:67]
	s_mov_b32 m0, s43
	s_nop 0
	global_load_lds_dwordx4 v136, s[66:67]
	s_add_u32 s100, s30, 0x80
	s_addc_u32 s101, s31, 0
	s_mov_b32 m0, s44
	s_nop 0
	global_load_lds_dwordx4 v130, s[30:31]
	s_mov_b32 m0, s45
	s_nop 0
	global_load_lds_dwordx4 v134, s[30:31]
	s_waitcnt vmcnt(8)
	s_waitcnt lgkmcnt(0)
	s_barrier
	s_setprio 1
	s_waitcnt lgkmcnt(0)
	v_mfma_f32_16x16x32_bf16 v[62:65], v[154:157], v[186:189], v[62:65]
	v_mfma_f32_16x16x32_bf16 v[58:61], v[162:165], v[186:189], v[58:61]
	v_mfma_f32_16x16x32_bf16 v[46:49], v[154:157], v[194:197], v[46:49]
	v_mfma_f32_16x16x32_bf16 v[42:45], v[162:165], v[194:197], v[42:45]
	v_mfma_f32_16x16x32_bf16 v[30:33], v[154:157], v[202:205], v[30:33]
	v_mfma_f32_16x16x32_bf16 v[26:29], v[162:165], v[202:205], v[26:29]
	v_mfma_f32_16x16x32_bf16 v[14:17], v[154:157], v[210:213], v[14:17]
	v_mfma_f32_16x16x32_bf16 v[10:13], v[162:165], v[210:213], v[10:13]
	v_mfma_f32_16x16x32_bf16 v[62:65], v[158:161], v[190:193], v[62:65]
	v_mfma_f32_16x16x32_bf16 v[58:61], v[166:169], v[190:193], v[58:61]
	v_mfma_f32_16x16x32_bf16 v[46:49], v[158:161], v[198:201], v[46:49]
	v_mfma_f32_16x16x32_bf16 v[42:45], v[166:169], v[198:201], v[42:45]
	v_mfma_f32_16x16x32_bf16 v[30:33], v[158:161], v[206:209], v[30:33]
	v_mfma_f32_16x16x32_bf16 v[26:29], v[166:169], v[206:209], v[26:29]
	v_mfma_f32_16x16x32_bf16 v[14:17], v[158:161], v[214:217], v[14:17]
	v_mfma_f32_16x16x32_bf16 v[10:13], v[166:169], v[214:217], v[10:13]
	v_mfma_f32_16x16x32_bf16 v[54:57], v[170:173], v[186:189], v[54:57]
	v_mfma_f32_16x16x32_bf16 v[50:53], v[178:181], v[186:189], v[50:53]
	v_mfma_f32_16x16x32_bf16 v[38:41], v[170:173], v[194:197], v[38:41]
	v_mfma_f32_16x16x32_bf16 v[34:37], v[178:181], v[194:197], v[34:37]
	v_mfma_f32_16x16x32_bf16 v[22:25], v[170:173], v[202:205], v[22:25]
	v_mfma_f32_16x16x32_bf16 v[18:21], v[178:181], v[202:205], v[18:21]
	v_mfma_f32_16x16x32_bf16 v[6:9], v[170:173], v[210:213], v[6:9]
	v_mfma_f32_16x16x32_bf16 v[2:5], v[178:181], v[210:213], v[2:5]
	v_mfma_f32_16x16x32_bf16 v[54:57], v[174:177], v[190:193], v[54:57]
	v_mfma_f32_16x16x32_bf16 v[50:53], v[182:185], v[190:193], v[50:53]
	v_mfma_f32_16x16x32_bf16 v[38:41], v[174:177], v[198:201], v[38:41]
	v_mfma_f32_16x16x32_bf16 v[34:37], v[182:185], v[198:201], v[34:37]
	v_mfma_f32_16x16x32_bf16 v[22:25], v[174:177], v[206:209], v[22:25]
	v_mfma_f32_16x16x32_bf16 v[18:21], v[182:185], v[206:209], v[18:21]
	v_mfma_f32_16x16x32_bf16 v[6:9], v[174:177], v[214:217], v[6:9]
	v_mfma_f32_16x16x32_bf16 v[2:5], v[182:185], v[214:217], v[2:5]
	s_setprio 0
	s_barrier
; #define PG8_STAGE(bufoff, gbase, voff) do { _Pragma("unroll") for (int _i = 0; _i < 2; ++_i) \
;         __builtin_amdgcn_global_load_lds((const unsigned*)((const char*)(gbase) + (voff)[_i]), (PG8_LAS unsigned*)(lds + (bufoff) + ldsw + _i * 8192), 16, 0, 0); } while (0)
; #define PG8_LDA(dst, b, h) do { if constexpr (DT != 1) { _Pragma("unroll") for (int m = 0; m < 4; ++m) _Pragma("unroll") for (int k = 0; k < 2; ++k) dst[m][k] = *(const PG8_LAS bf16x8*)(lds + PG8_SA(b, h) + aoff + m * 2048 + k * 1024); } \
;         else { _Pragma("unroll") for (int m = 0; m < 4; ++m) dst##8[m] = ld32(lds + PG8_SA(b, h) + aoff + m * 2048); } } while (0)
; #define PG8_LDB(dst, b, h) do { if constexpr (DT != 1) { _Pragma("unroll") for (int n = 0; n < 2; ++n) _Pragma("unroll") for (int k = 0; k < 2; ++k) dst[n][k] = *(const PG8_LAS bf16x8*)(lds + PG8_SB(b, h) + boff + n * 2048 + k * 1024); } \
;         else { _Pragma("unroll") for (int n = 0; n < 2; ++n) dst##8[n] = ld32(lds + PG8_SB(b, h) + boff + n * 2048); } } while (0)
; #define PG8_WAIT_V(n) asm volatile("s_waitcnt vmcnt(" #n ")" ::: "memory")
; #define PG8_WAIT_L(n) asm volatile("s_waitcnt lgkmcnt(" #n ")" ::: "memory")
; #define PG8_BAR __builtin_amdgcn_s_barrier()
; #define PG8_SCHED __builtin_amdgcn_sched_barrier(0)
;     ...
;         for (int t = 0; t < nt; t += 2) {
;             const bool last = (t == nt - 2);
;             const char* a1 = cA + (size_t)(t + 1) * kstep;
;             const char* a2 = last ? nA : cA + (size_t)(t + 2) * kstep; const char* b2 = last ? nB : cB + (size_t)(t + 2) * kstep;
;     ...
;             PG8_LDB(B0, 1, 0); PG8_LDB(B1, 1, 1); PG8_SCHED; PG8_LDA(At, 1, 0); PG8_STAGE(PG8_SA(0, 1), a2 + hstepA, voffA);
;             PG8_WAIT_V(8); PG8_WAIT_L(0); PG8_BAR; PG8_MMA(0, 0, At, B0); PG8_MMA(0, 1, At, B1); PG8_BAR; PG8_SCHED;
;             PG8_LDA(At, 1, 1); PG8_STAGE(PG8_SB(1, 0), b3, voffB); PG8_STAGE(PG8_SB(1, 1), b3 + hstepB, voffB); PG8_STAGE(PG8_SA(1, 0), a3, voffA);
;             PG8_WAIT_V(8); PG8_WAIT_L(0); PG8_BAR; PG8_MMA(1, 0, At, B0); PG8_MMA(1, 1, At, B1); PG8_BAR; PG8_SCHED;
	ds_read_b128 v[154:157], v151
	ds_read_b128 v[158:161], v151 offset:1024
	ds_read_b128 v[162:165], v151 offset:2048
	ds_read_b128 v[166:169], v151 offset:3072
	ds_read_b128 v[170:173], v152
	ds_read_b128 v[174:177], v152 offset:1024
	ds_read_b128 v[178:181], v152 offset:2048
	ds_read_b128 v[182:185], v152 offset:3072
	s_add_u32 s30, s30, 0x80000
	s_addc_u32 s31, s31, 0
	s_mov_b32 m0, s46
	ds_read_b128 v[186:189], v150 offset:32768
	ds_read_b128 v[190:193], v150 offset:33792
	ds_read_b128 v[194:197], v150 offset:34816
	ds_read_b128 v[198:201], v150 offset:35840
	ds_read_b128 v[202:205], v150 offset:36864
	ds_read_b128 v[206:209], v150 offset:37888
	ds_read_b128 v[210:213], v150 offset:38912
	ds_read_b128 v[214:217], v150 offset:39936
	global_load_lds_dwordx4 v130, s[30:31]
	s_mov_b32 m0, s47
	s_nop 0
	global_load_lds_dwordx4 v134, s[30:31]
	s_waitcnt vmcnt(8)
	s_waitcnt lgkmcnt(0)
	s_barrier
	s_setprio 1
	s_waitcnt lgkmcnt(0)
	v_mfma_f32_16x16x32_bf16 v[126:129], v[154:157], v[186:189], v[126:129]
	v_mfma_f32_16x16x32_bf16 v[122:125], v[162:165], v[186:189], v[122:125]
	v_mfma_f32_16x16x32_bf16 v[110:113], v[154:157], v[194:197], v[110:113]
	v_mfma_f32_16x16x32_bf16 v[106:109], v[162:165], v[194:197], v[106:109]
	v_mfma_f32_16x16x32_bf16 v[94:97], v[154:157], v[202:205], v[94:97]
	v_mfma_f32_16x16x32_bf16 v[90:93], v[162:165], v[202:205], v[90:93]
	v_mfma_f32_16x16x32_bf16 v[78:81], v[154:157], v[210:213], v[78:81]
	v_mfma_f32_16x16x32_bf16 v[74:77], v[162:165], v[210:213], v[74:77]
	v_mfma_f32_16x16x32_bf16 v[126:129], v[158:161], v[190:193], v[126:129]
	v_mfma_f32_16x16x32_bf16 v[122:125], v[166:169], v[190:193], v[122:125]
	v_mfma_f32_16x16x32_bf16 v[110:113], v[158:161], v[198:201], v[110:113]
	v_mfma_f32_16x16x32_bf16 v[106:109], v[166:169], v[198:201], v[106:109]
	v_mfma_f32_16x16x32_bf16 v[94:97], v[158:161], v[206:209], v[94:97]
	v_mfma_f32_16x16x32_bf16 v[90:93], v[166:169], v[206:209], v[90:93]
	v_mfma_f32_16x16x32_bf16 v[78:81], v[158:161], v[214:217], v[78:81]
	v_mfma_f32_16x16x32_bf16 v[74:77], v[166:169], v[214:217], v[74:77]
	v_mfma_f32_16x16x32_bf16 v[118:121], v[170:173], v[186:189], v[118:121]
	v_mfma_f32_16x16x32_bf16 v[114:117], v[178:181], v[186:189], v[114:117]
	v_mfma_f32_16x16x32_bf16 v[102:105], v[170:173], v[194:197], v[102:105]
	v_mfma_f32_16x16x32_bf16 v[98:101], v[178:181], v[194:197], v[98:101]
	v_mfma_f32_16x16x32_bf16 v[86:89], v[170:173], v[202:205], v[86:89]
	v_mfma_f32_16x16x32_bf16 v[82:85], v[178:181], v[202:205], v[82:85]
	v_mfma_f32_16x16x32_bf16 v[70:73], v[170:173], v[210:213], v[70:73]
	v_mfma_f32_16x16x32_bf16 v[66:69], v[178:181], v[210:213], v[66:69]
	v_mfma_f32_16x16x32_bf16 v[118:121], v[174:177], v[190:193], v[118:121]
	v_mfma_f32_16x16x32_bf16 v[114:117], v[182:185], v[190:193], v[114:117]
	v_mfma_f32_16x16x32_bf16 v[102:105], v[174:177], v[198:201], v[102:105]
	v_mfma_f32_16x16x32_bf16 v[98:101], v[182:185], v[198:201], v[98:101]
	v_mfma_f32_16x16x32_bf16 v[86:89], v[174:177], v[206:209], v[86:89]
	v_mfma_f32_16x16x32_bf16 v[82:85], v[182:185], v[206:209], v[82:85]
	v_mfma_f32_16x16x32_bf16 v[70:73], v[174:177], v[214:217], v[70:73]
	v_mfma_f32_16x16x32_bf16 v[66:69], v[182:185], v[214:217], v[66:69]
	s_setprio 0
	s_barrier
	s_mov_b32 m0, s53
	s_add_u32 s28, s28, 0x80080
	ds_read_b128 v[186:189], v150 offset:49152
	ds_read_b128 v[190:193], v150 offset:50176
	ds_read_b128 v[194:197], v150 offset:51200
	ds_read_b128 v[198:201], v150 offset:52224
	ds_read_b128 v[202:205], v150 offset:53248
	ds_read_b128 v[206:209], v150 offset:54272
	ds_read_b128 v[210:213], v150 offset:55296
	ds_read_b128 v[214:217], v150 offset:56320
	global_load_lds_dwordx4 v132, s[98:99]
	s_mov_b32 m0, s54
	s_addc_u32 s29, s29, 0
	global_load_lds_dwordx4 v136, s[98:99]
	s_mov_b32 m0, s57
	s_nop 0
	global_load_lds_dwordx4 v132, s[28:29]
	s_mov_b32 m0, s58
	s_nop 0
	global_load_lds_dwordx4 v136, s[28:29]
	s_mov_b32 m0, s55
	s_nop 0
	global_load_lds_dwordx4 v130, s[100:101]
	s_mov_b32 m0, s56
	s_nop 0
	global_load_lds_dwordx4 v134, s[100:101]
	s_waitcnt vmcnt(8)
	s_waitcnt lgkmcnt(0)
	s_barrier
	s_setprio 1
	s_waitcnt lgkmcnt(0)
	v_mfma_f32_16x16x32_bf16 v[62:65], v[154:157], v[186:189], v[62:65]
	v_mfma_f32_16x16x32_bf16 v[58:61], v[162:165], v[186:189], v[58:61]
	v_mfma_f32_16x16x32_bf16 v[46:49], v[154:157], v[194:197], v[46:49]
	v_mfma_f32_16x16x32_bf16 v[42:45], v[162:165], v[194:197], v[42:45]
	v_mfma_f32_16x16x32_bf16 v[30:33], v[154:157], v[202:205], v[30:33]
	v_mfma_f32_16x16x32_bf16 v[26:29], v[162:165], v[202:205], v[26:29]
	v_mfma_f32_16x16x32_bf16 v[14:17], v[154:157], v[210:213], v[14:17]
	v_mfma_f32_16x16x32_bf16 v[10:13], v[162:165], v[210:213], v[10:13]
	v_mfma_f32_16x16x32_bf16 v[62:65], v[158:161], v[190:193], v[62:65]
	v_mfma_f32_16x16x32_bf16 v[58:61], v[166:169], v[190:193], v[58:61]
	v_mfma_f32_16x16x32_bf16 v[46:49], v[158:161], v[198:201], v[46:49]
	v_mfma_f32_16x16x32_bf16 v[42:45], v[166:169], v[198:201], v[42:45]
	v_mfma_f32_16x16x32_bf16 v[30:33], v[158:161], v[206:209], v[30:33]
	v_mfma_f32_16x16x32_bf16 v[26:29], v[166:169], v[206:209], v[26:29]
	v_mfma_f32_16x16x32_bf16 v[14:17], v[158:161], v[214:217], v[14:17]
	v_mfma_f32_16x16x32_bf16 v[10:13], v[166:169], v[214:217], v[10:13]
	v_mfma_f32_16x16x32_bf16 v[54:57], v[170:173], v[186:189], v[54:57]
	v_mfma_f32_16x16x32_bf16 v[50:53], v[178:181], v[186:189], v[50:53]
	v_mfma_f32_16x16x32_bf16 v[38:41], v[170:173], v[194:197], v[38:41]
	v_mfma_f32_16x16x32_bf16 v[34:37], v[178:181], v[194:197], v[34:37]
	v_mfma_f32_16x16x32_bf16 v[22:25], v[170:173], v[202:205], v[22:25]
	v_mfma_f32_16x16x32_bf16 v[18:21], v[178:181], v[202:205], v[18:21]
	v_mfma_f32_16x16x32_bf16 v[6:9], v[170:173], v[210:213], v[6:9]
	v_mfma_f32_16x16x32_bf16 v[2:5], v[178:181], v[210:213], v[2:5]
	v_mfma_f32_16x16x32_bf16 v[54:57], v[174:177], v[190:193], v[54:57]
	v_mfma_f32_16x16x32_bf16 v[50:53], v[182:185], v[190:193], v[50:53]
	v_mfma_f32_16x16x32_bf16 v[38:41], v[174:177], v[198:201], v[38:41]
	v_mfma_f32_16x16x32_bf16 v[34:37], v[182:185], v[198:201], v[34:37]
	v_mfma_f32_16x16x32_bf16 v[22:25], v[174:177], v[206:209], v[22:25]
	v_mfma_f32_16x16x32_bf16 v[18:21], v[182:185], v[206:209], v[18:21]
	v_mfma_f32_16x16x32_bf16 v[6:9], v[174:177], v[214:217], v[6:9]
	v_mfma_f32_16x16x32_bf16 v[2:5], v[182:185], v[214:217], v[2:5]
	s_setprio 0
	s_barrier
	s_add_u32 s25, s25, 0x100
	s_addc_u32 s64, s64, 0
	s_add_u32 s26, s26, 0x100
	s_addc_u32 s27, s27, 0
	s_cmp_ge_i32 s65, s52
	s_mov_b32 s28, s65
	s_cbranch_scc0 .LBB0_2262

; #define PG8_STAGE(bufoff, gbase, voff) do { _Pragma("unroll") for (int _i = 0; _i < 2; ++_i) \
;         __builtin_amdgcn_global_load_lds((const unsigned*)((const char*)(gbase) + (voff)[_i]), (PG8_LAS unsigned*)(lds + (bufoff) + ldsw + _i * 8192), 16, 0, 0); } while (0)
; #define PG8_LDA(dst, b, h) do { if constexpr (DT != 1) { _Pragma("unroll") for (int m = 0; m < 4; ++m) _Pragma("unroll") for (int k = 0; k < 2; ++k) dst[m][k] = *(const PG8_LAS bf16x8*)(lds + PG8_SA(b, h) + aoff + m * 2048 + k * 1024); } \
;         else { _Pragma("unroll") for (int m = 0; m < 4; ++m) dst##8[m] = ld32(lds + PG8_SA(b, h) + aoff + m * 2048); } } while (0)
; #define PG8_LDB(dst, b, h) do { if constexpr (DT != 1) { _Pragma("unroll") for (int n = 0; n < 2; ++n) _Pragma("unroll") for (int k = 0; k < 2; ++k) dst[n][k] = *(const PG8_LAS bf16x8*)(lds + PG8_SB(b, h) + boff + n * 2048 + k * 1024); } \
;         else { _Pragma("unroll") for (int n = 0; n < 2; ++n) dst##8[n] = ld32(lds + PG8_SB(b, h) + boff + n * 2048); } } while (0)
; #define PG8_WAIT_V(n) asm volatile("s_waitcnt vmcnt(" #n ")" ::: "memory")
; #define PG8_WAIT_L(n) asm volatile("s_waitcnt lgkmcnt(" #n ")" ::: "memory")
; #define PG8_BAR __builtin_amdgcn_s_barrier()
; #define PG8_SCHED __builtin_amdgcn_sched_barrier(0)
;     ...
;             PG8_LDB(B0, 0, 0); PG8_LDB(B1, 0, 1); PG8_SCHED; PG8_LDA(At, 0, 0); PG8_STAGE(PG8_SA(1, 1), a1 + hstepA, voffA);
;             PG8_WAIT_V(8); PG8_WAIT_L(0); PG8_BAR; PG8_MMA(0, 0, At, B0); PG8_MMA(0, 1, At, B1); PG8_BAR; PG8_SCHED;
;             PG8_LDA(At, 0, 1); PG8_STAGE(PG8_SB(0, 0), b2, voffB); PG8_STAGE(PG8_SB(0, 1), b2 + hstepB, voffB); PG8_STAGE(PG8_SA(0, 0), a2, voffA);
;             PG8_WAIT_V(8); PG8_WAIT_L(0); PG8_BAR; PG8_MMA(1, 0, At, B0); PG8_MMA(1, 1, At, B1); PG8_BAR; PG8_SCHED;
.LBB0_3356:
	ds_read_b128 v[130:133], v173
	ds_read_b128 v[134:137], v173 offset:1024
	ds_read_b128 v[138:141], v173 offset:2048
	ds_read_b128 v[142:145], v173 offset:3072
	ds_read_b128 v[164:167], v174
	ds_read_b128 v[168:171], v174 offset:1024
	ds_read_b128 v[178:181], v174 offset:2048
	ds_read_b128 v[182:185], v174 offset:3072
	s_add_i32 s78, s42, 2
	s_add_u32 s43, s40, 0xffff0080
	s_addc_u32 s44, s41, -1
	s_cmp_eq_u32 s74, s42
	s_cselect_b32 s42, s39, s76
	s_cselect_b32 s45, s3, s44
	s_cselect_b32 s44, s29, s43
	s_cselect_b32 s43, s31, s77
	s_add_i32 m0, s56, 0xc000
	ds_read_b128 v[186:189], v175
	ds_read_b128 v[190:193], v175 offset:1024
	ds_read_b128 v[194:197], v175 offset:2048
	ds_read_b128 v[198:201], v175 offset:3072
	ds_read_b128 v[202:205], v175 offset:4096
	ds_read_b128 v[206:209], v175 offset:5120
	ds_read_b128 v[210:213], v175 offset:6144
	ds_read_b128 v[214:217], v175 offset:7168
	global_load_lds_dwordx4 v158, s[40:41]
	s_add_i32 m0, s56, 0xe000
	s_nop 0
	global_load_lds_dwordx4 v156, s[40:41]
	s_waitcnt vmcnt(8)
	s_waitcnt lgkmcnt(0)
	s_barrier
	s_setprio 1
	s_waitcnt lgkmcnt(0)
	v_mfma_f32_16x16x32_bf16 v[126:129], v[130:133], v[186:189], v[126:129]
	v_mfma_f32_16x16x32_bf16 v[122:125], v[138:141], v[186:189], v[122:125]
	v_mfma_f32_16x16x32_bf16 v[110:113], v[130:133], v[194:197], v[110:113]
	v_mfma_f32_16x16x32_bf16 v[106:109], v[138:141], v[194:197], v[106:109]
	v_mfma_f32_16x16x32_bf16 v[94:97], v[130:133], v[202:205], v[94:97]
	v_mfma_f32_16x16x32_bf16 v[90:93], v[138:141], v[202:205], v[90:93]
	v_mfma_f32_16x16x32_bf16 v[78:81], v[130:133], v[210:213], v[78:81]
	v_mfma_f32_16x16x32_bf16 v[74:77], v[138:141], v[210:213], v[74:77]
	v_mfma_f32_16x16x32_bf16 v[126:129], v[134:137], v[190:193], v[126:129]
	v_mfma_f32_16x16x32_bf16 v[122:125], v[142:145], v[190:193], v[122:125]
	v_mfma_f32_16x16x32_bf16 v[110:113], v[134:137], v[198:201], v[110:113]
	v_mfma_f32_16x16x32_bf16 v[106:109], v[142:145], v[198:201], v[106:109]
	v_mfma_f32_16x16x32_bf16 v[94:97], v[134:137], v[206:209], v[94:97]
	v_mfma_f32_16x16x32_bf16 v[90:93], v[142:145], v[206:209], v[90:93]
	v_mfma_f32_16x16x32_bf16 v[78:81], v[134:137], v[214:217], v[78:81]
	v_mfma_f32_16x16x32_bf16 v[74:77], v[142:145], v[214:217], v[74:77]
	v_mfma_f32_16x16x32_bf16 v[118:121], v[164:167], v[186:189], v[118:121]
	v_mfma_f32_16x16x32_bf16 v[114:117], v[178:181], v[186:189], v[114:117]
	v_mfma_f32_16x16x32_bf16 v[102:105], v[164:167], v[194:197], v[102:105]
	v_mfma_f32_16x16x32_bf16 v[98:101], v[178:181], v[194:197], v[98:101]
	v_mfma_f32_16x16x32_bf16 v[86:89], v[164:167], v[202:205], v[86:89]
	v_mfma_f32_16x16x32_bf16 v[82:85], v[178:181], v[202:205], v[82:85]
	v_mfma_f32_16x16x32_bf16 v[70:73], v[164:167], v[210:213], v[70:73]
	v_mfma_f32_16x16x32_bf16 v[66:69], v[178:181], v[210:213], v[66:69]
	v_mfma_f32_16x16x32_bf16 v[118:121], v[168:171], v[190:193], v[118:121]
	v_mfma_f32_16x16x32_bf16 v[114:117], v[182:185], v[190:193], v[114:117]
	v_mfma_f32_16x16x32_bf16 v[102:105], v[168:171], v[198:201], v[102:105]
	v_mfma_f32_16x16x32_bf16 v[98:101], v[182:185], v[198:201], v[98:101]
	v_mfma_f32_16x16x32_bf16 v[86:89], v[168:171], v[206:209], v[86:89]
	v_mfma_f32_16x16x32_bf16 v[82:85], v[182:185], v[206:209], v[82:85]
	v_mfma_f32_16x16x32_bf16 v[70:73], v[168:171], v[214:217], v[70:73]
	v_mfma_f32_16x16x32_bf16 v[66:69], v[182:185], v[214:217], v[66:69]
	s_setprio 0
	s_barrier
	s_mov_b32 m0, s52
	s_add_u32 s98, s42, 0x80
	s_addc_u32 s99, s43, 0
	s_add_u32 s80, s42, 0x10000
	ds_read_b128 v[186:189], v175 offset:16384
	ds_read_b128 v[190:193], v175 offset:17408
	ds_read_b128 v[194:197], v175 offset:18432
	ds_read_b128 v[198:201], v175 offset:19456
	ds_read_b128 v[202:205], v175 offset:20480
	ds_read_b128 v[206:209], v175 offset:21504
	ds_read_b128 v[210:213], v175 offset:22528
	ds_read_b128 v[214:217], v175 offset:23552
	global_load_lds_dwordx4 v148, s[42:43]
	s_mov_b32 m0, s53
	s_addc_u32 s81, s43, 0
	global_load_lds_dwordx4 v152, s[42:43]
	s_mov_b32 m0, s54
	s_nop 0
	global_load_lds_dwordx4 v148, s[80:81]
	s_mov_b32 m0, s55
	s_nop 0
	global_load_lds_dwordx4 v152, s[80:81]
	s_add_u32 s100, s44, 0x80
	s_addc_u32 s101, s45, 0
	s_mov_b32 m0, s56
	s_nop 0
	global_load_lds_dwordx4 v146, s[44:45]
	s_mov_b32 m0, s57
	s_nop 0
	global_load_lds_dwordx4 v150, s[44:45]
	s_waitcnt vmcnt(8)
	s_waitcnt lgkmcnt(0)
	s_barrier
	s_setprio 1
	s_waitcnt lgkmcnt(0)
	v_mfma_f32_16x16x32_bf16 v[62:65], v[130:133], v[186:189], v[62:65]
	v_mfma_f32_16x16x32_bf16 v[58:61], v[138:141], v[186:189], v[58:61]
	v_mfma_f32_16x16x32_bf16 v[46:49], v[130:133], v[194:197], v[46:49]
	v_mfma_f32_16x16x32_bf16 v[42:45], v[138:141], v[194:197], v[42:45]
	v_mfma_f32_16x16x32_bf16 v[30:33], v[130:133], v[202:205], v[30:33]
	v_mfma_f32_16x16x32_bf16 v[26:29], v[138:141], v[202:205], v[26:29]
	v_mfma_f32_16x16x32_bf16 v[14:17], v[130:133], v[210:213], v[14:17]
	v_mfma_f32_16x16x32_bf16 v[10:13], v[138:141], v[210:213], v[10:13]
	v_mfma_f32_16x16x32_bf16 v[62:65], v[134:137], v[190:193], v[62:65]
	v_mfma_f32_16x16x32_bf16 v[58:61], v[142:145], v[190:193], v[58:61]
	v_mfma_f32_16x16x32_bf16 v[46:49], v[134:137], v[198:201], v[46:49]
	v_mfma_f32_16x16x32_bf16 v[42:45], v[142:145], v[198:201], v[42:45]
	v_mfma_f32_16x16x32_bf16 v[30:33], v[134:137], v[206:209], v[30:33]
	v_mfma_f32_16x16x32_bf16 v[26:29], v[142:145], v[206:209], v[26:29]
	v_mfma_f32_16x16x32_bf16 v[14:17], v[134:137], v[214:217], v[14:17]
	v_mfma_f32_16x16x32_bf16 v[10:13], v[142:145], v[214:217], v[10:13]
	v_mfma_f32_16x16x32_bf16 v[54:57], v[164:167], v[186:189], v[54:57]
	v_mfma_f32_16x16x32_bf16 v[50:53], v[178:181], v[186:189], v[50:53]
	v_mfma_f32_16x16x32_bf16 v[38:41], v[164:167], v[194:197], v[38:41]
	v_mfma_f32_16x16x32_bf16 v[34:37], v[178:181], v[194:197], v[34:37]
	v_mfma_f32_16x16x32_bf16 v[22:25], v[164:167], v[202:205], v[22:25]
	v_mfma_f32_16x16x32_bf16 v[18:21], v[178:181], v[202:205], v[18:21]
	v_mfma_f32_16x16x32_bf16 v[6:9], v[164:167], v[210:213], v[6:9]
	v_mfma_f32_16x16x32_bf16 v[2:5], v[178:181], v[210:213], v[2:5]
	v_mfma_f32_16x16x32_bf16 v[54:57], v[168:171], v[190:193], v[54:57]
	v_mfma_f32_16x16x32_bf16 v[50:53], v[182:185], v[190:193], v[50:53]
	v_mfma_f32_16x16x32_bf16 v[38:41], v[168:171], v[198:201], v[38:41]
	v_mfma_f32_16x16x32_bf16 v[34:37], v[182:185], v[198:201], v[34:37]
	v_mfma_f32_16x16x32_bf16 v[22:25], v[168:171], v[206:209], v[22:25]
	v_mfma_f32_16x16x32_bf16 v[18:21], v[182:185], v[206:209], v[18:21]
	v_mfma_f32_16x16x32_bf16 v[6:9], v[168:171], v[214:217], v[6:9]
	v_mfma_f32_16x16x32_bf16 v[2:5], v[182:185], v[214:217], v[2:5]
	s_setprio 0
	s_barrier
; #define PG8_STAGE(bufoff, gbase, voff) do { _Pragma("unroll") for (int _i = 0; _i < 2; ++_i) \
;         __builtin_amdgcn_global_load_lds((const unsigned*)((const char*)(gbase) + (voff)[_i]), (PG8_LAS unsigned*)(lds + (bufoff) + ldsw + _i * 8192), 16, 0, 0); } while (0)
; #define PG8_LDA(dst, b, h) do { if constexpr (DT != 1) { _Pragma("unroll") for (int m = 0; m < 4; ++m) _Pragma("unroll") for (int k = 0; k < 2; ++k) dst[m][k] = *(const PG8_LAS bf16x8*)(lds + PG8_SA(b, h) + aoff + m * 2048 + k * 1024); } \
;         else { _Pragma("unroll") for (int m = 0; m < 4; ++m) dst##8[m] = ld32(lds + PG8_SA(b, h) + aoff + m * 2048); } } while (0)
; #define PG8_LDB(dst, b, h) do { if constexpr (DT != 1) { _Pragma("unroll") for (int n = 0; n < 2; ++n) _Pragma("unroll") for (int k = 0; k < 2; ++k) dst[n][k] = *(const PG8_LAS bf16x8*)(lds + PG8_SB(b, h) + boff + n * 2048 + k * 1024); } \
;         else { _Pragma("unroll") for (int n = 0; n < 2; ++n) dst##8[n] = ld32(lds + PG8_SB(b, h) + boff + n * 2048); } } while (0)
; #define PG8_WAIT_V(n) asm volatile("s_waitcnt vmcnt(" #n ")" ::: "memory")
; #define PG8_WAIT_L(n) asm volatile("s_waitcnt lgkmcnt(" #n ")" ::: "memory")
; #define PG8_BAR __builtin_amdgcn_s_barrier()
; #define PG8_SCHED __builtin_amdgcn_sched_barrier(0)
;     ...
;         for (int t = 0; t < nt; t += 2) {
;             const bool last = (t == nt - 2);
;             const char* a1 = cA + (size_t)(t + 1) * kstep;
;             const char* a2 = last ? nA : cA + (size_t)(t + 2) * kstep; const char* b2 = last ? nB : cB + (size_t)(t + 2) * kstep;
;     ...
;             PG8_LDB(B0, 1, 0); PG8_LDB(B1, 1, 1); PG8_SCHED; PG8_LDA(At, 1, 0); PG8_STAGE(PG8_SA(0, 1), a2 + hstepA, voffA);
;             PG8_WAIT_V(8); PG8_WAIT_L(0); PG8_BAR; PG8_MMA(0, 0, At, B0); PG8_MMA(0, 1, At, B1); PG8_BAR; PG8_SCHED;
;             PG8_LDA(At, 1, 1); PG8_STAGE(PG8_SB(1, 0), b3, voffB); PG8_STAGE(PG8_SB(1, 1), b3 + hstepB, voffB); PG8_STAGE(PG8_SA(1, 0), a3, voffA);
;             PG8_WAIT_V(8); PG8_WAIT_L(0); PG8_BAR; PG8_MMA(1, 0, At, B0); PG8_MMA(1, 1, At, B1); PG8_BAR; PG8_SCHED;
	ds_read_b128 v[130:133], v176
	ds_read_b128 v[134:137], v176 offset:1024
	ds_read_b128 v[138:141], v176 offset:2048
	ds_read_b128 v[142:145], v176 offset:3072
	ds_read_b128 v[164:167], v177
	ds_read_b128 v[168:171], v177 offset:1024
	ds_read_b128 v[178:181], v177 offset:2048
	ds_read_b128 v[182:185], v177 offset:3072
	s_add_u32 s44, s44, 0x10000
	s_addc_u32 s45, s45, 0
	s_mov_b32 m0, s58
	ds_read_b128 v[186:189], v175 offset:32768
	ds_read_b128 v[190:193], v175 offset:33792
	ds_read_b128 v[194:197], v175 offset:34816
	ds_read_b128 v[198:201], v175 offset:35840
	ds_read_b128 v[202:205], v175 offset:36864
	ds_read_b128 v[206:209], v175 offset:37888
	ds_read_b128 v[210:213], v175 offset:38912
	ds_read_b128 v[214:217], v175 offset:39936
	global_load_lds_dwordx4 v146, s[44:45]
	s_mov_b32 m0, s59
	s_nop 0
	global_load_lds_dwordx4 v150, s[44:45]
	s_waitcnt vmcnt(8)
	s_waitcnt lgkmcnt(0)
	s_barrier
	s_setprio 1
	s_waitcnt lgkmcnt(0)
	v_mfma_f32_16x16x32_bf16 v[126:129], v[130:133], v[186:189], v[126:129]
	v_mfma_f32_16x16x32_bf16 v[122:125], v[138:141], v[186:189], v[122:125]
	v_mfma_f32_16x16x32_bf16 v[110:113], v[130:133], v[194:197], v[110:113]
	v_mfma_f32_16x16x32_bf16 v[106:109], v[138:141], v[194:197], v[106:109]
	v_mfma_f32_16x16x32_bf16 v[94:97], v[130:133], v[202:205], v[94:97]
	v_mfma_f32_16x16x32_bf16 v[90:93], v[138:141], v[202:205], v[90:93]
	v_mfma_f32_16x16x32_bf16 v[78:81], v[130:133], v[210:213], v[78:81]
	v_mfma_f32_16x16x32_bf16 v[74:77], v[138:141], v[210:213], v[74:77]
	v_mfma_f32_16x16x32_bf16 v[126:129], v[134:137], v[190:193], v[126:129]
	v_mfma_f32_16x16x32_bf16 v[122:125], v[142:145], v[190:193], v[122:125]
	v_mfma_f32_16x16x32_bf16 v[110:113], v[134:137], v[198:201], v[110:113]
	v_mfma_f32_16x16x32_bf16 v[106:109], v[142:145], v[198:201], v[106:109]
	v_mfma_f32_16x16x32_bf16 v[94:97], v[134:137], v[206:209], v[94:97]
	v_mfma_f32_16x16x32_bf16 v[90:93], v[142:145], v[206:209], v[90:93]
	v_mfma_f32_16x16x32_bf16 v[78:81], v[134:137], v[214:217], v[78:81]
	v_mfma_f32_16x16x32_bf16 v[74:77], v[142:145], v[214:217], v[74:77]
	v_mfma_f32_16x16x32_bf16 v[118:121], v[164:167], v[186:189], v[118:121]
	v_mfma_f32_16x16x32_bf16 v[114:117], v[178:181], v[186:189], v[114:117]
	v_mfma_f32_16x16x32_bf16 v[102:105], v[164:167], v[194:197], v[102:105]
	v_mfma_f32_16x16x32_bf16 v[98:101], v[178:181], v[194:197], v[98:101]
	v_mfma_f32_16x16x32_bf16 v[86:89], v[164:167], v[202:205], v[86:89]
	v_mfma_f32_16x16x32_bf16 v[82:85], v[178:181], v[202:205], v[82:85]
	v_mfma_f32_16x16x32_bf16 v[70:73], v[164:167], v[210:213], v[70:73]
	v_mfma_f32_16x16x32_bf16 v[66:69], v[178:181], v[210:213], v[66:69]
	v_mfma_f32_16x16x32_bf16 v[118:121], v[168:171], v[190:193], v[118:121]
	v_mfma_f32_16x16x32_bf16 v[114:117], v[182:185], v[190:193], v[114:117]
	v_mfma_f32_16x16x32_bf16 v[102:105], v[168:171], v[198:201], v[102:105]
	v_mfma_f32_16x16x32_bf16 v[98:101], v[182:185], v[198:201], v[98:101]
	v_mfma_f32_16x16x32_bf16 v[86:89], v[168:171], v[206:209], v[86:89]
	v_mfma_f32_16x16x32_bf16 v[82:85], v[182:185], v[206:209], v[82:85]
	v_mfma_f32_16x16x32_bf16 v[70:73], v[168:171], v[214:217], v[70:73]
	v_mfma_f32_16x16x32_bf16 v[66:69], v[182:185], v[214:217], v[66:69]
	s_setprio 0
	s_barrier
	s_mov_b32 m0, s66
	s_add_u32 s42, s42, 0x10080
	ds_read_b128 v[186:189], v175 offset:49152
	ds_read_b128 v[190:193], v175 offset:50176
	ds_read_b128 v[194:197], v175 offset:51200
	ds_read_b128 v[198:201], v175 offset:52224
	ds_read_b128 v[202:205], v175 offset:53248
	ds_read_b128 v[206:209], v175 offset:54272
	ds_read_b128 v[210:213], v175 offset:55296
	ds_read_b128 v[214:217], v175 offset:56320
	global_load_lds_dwordx4 v148, s[98:99]
	s_mov_b32 m0, s67
	s_addc_u32 s43, s43, 0
	global_load_lds_dwordx4 v152, s[98:99]
	s_mov_b32 m0, s70
	s_nop 0
	global_load_lds_dwordx4 v148, s[42:43]
	s_mov_b32 m0, s71
	s_nop 0
	global_load_lds_dwordx4 v152, s[42:43]
	s_mov_b32 m0, s68
	s_nop 0
	global_load_lds_dwordx4 v146, s[100:101]
	s_mov_b32 m0, s69
	s_nop 0
	global_load_lds_dwordx4 v150, s[100:101]
	s_waitcnt vmcnt(8)
	s_waitcnt lgkmcnt(0)
	s_barrier
	s_setprio 1
	s_waitcnt lgkmcnt(0)
	v_mfma_f32_16x16x32_bf16 v[62:65], v[130:133], v[186:189], v[62:65]
	v_mfma_f32_16x16x32_bf16 v[58:61], v[138:141], v[186:189], v[58:61]
	v_mfma_f32_16x16x32_bf16 v[46:49], v[130:133], v[194:197], v[46:49]
	v_mfma_f32_16x16x32_bf16 v[42:45], v[138:141], v[194:197], v[42:45]
	v_mfma_f32_16x16x32_bf16 v[30:33], v[130:133], v[202:205], v[30:33]
	v_mfma_f32_16x16x32_bf16 v[26:29], v[138:141], v[202:205], v[26:29]
	v_mfma_f32_16x16x32_bf16 v[14:17], v[130:133], v[210:213], v[14:17]
	v_mfma_f32_16x16x32_bf16 v[10:13], v[138:141], v[210:213], v[10:13]
	v_mfma_f32_16x16x32_bf16 v[62:65], v[134:137], v[190:193], v[62:65]
	v_mfma_f32_16x16x32_bf16 v[58:61], v[142:145], v[190:193], v[58:61]
	v_mfma_f32_16x16x32_bf16 v[46:49], v[134:137], v[198:201], v[46:49]
	v_mfma_f32_16x16x32_bf16 v[42:45], v[142:145], v[198:201], v[42:45]
	v_mfma_f32_16x16x32_bf16 v[30:33], v[134:137], v[206:209], v[30:33]
	v_mfma_f32_16x16x32_bf16 v[26:29], v[142:145], v[206:209], v[26:29]
	v_mfma_f32_16x16x32_bf16 v[14:17], v[134:137], v[214:217], v[14:17]
	v_mfma_f32_16x16x32_bf16 v[10:13], v[142:145], v[214:217], v[10:13]
	v_mfma_f32_16x16x32_bf16 v[54:57], v[164:167], v[186:189], v[54:57]
	v_mfma_f32_16x16x32_bf16 v[50:53], v[178:181], v[186:189], v[50:53]
	v_mfma_f32_16x16x32_bf16 v[38:41], v[164:167], v[194:197], v[38:41]
	v_mfma_f32_16x16x32_bf16 v[34:37], v[178:181], v[194:197], v[34:37]
	v_mfma_f32_16x16x32_bf16 v[22:25], v[164:167], v[202:205], v[22:25]
	v_mfma_f32_16x16x32_bf16 v[18:21], v[178:181], v[202:205], v[18:21]
	v_mfma_f32_16x16x32_bf16 v[6:9], v[164:167], v[210:213], v[6:9]
	v_mfma_f32_16x16x32_bf16 v[2:5], v[178:181], v[210:213], v[2:5]
	v_mfma_f32_16x16x32_bf16 v[54:57], v[168:171], v[190:193], v[54:57]
	v_mfma_f32_16x16x32_bf16 v[50:53], v[182:185], v[190:193], v[50:53]
	v_mfma_f32_16x16x32_bf16 v[38:41], v[168:171], v[198:201], v[38:41]
	v_mfma_f32_16x16x32_bf16 v[34:37], v[182:185], v[198:201], v[34:37]
	v_mfma_f32_16x16x32_bf16 v[22:25], v[168:171], v[206:209], v[22:25]
	v_mfma_f32_16x16x32_bf16 v[18:21], v[182:185], v[206:209], v[18:21]
	v_mfma_f32_16x16x32_bf16 v[6:9], v[168:171], v[214:217], v[6:9]
	v_mfma_f32_16x16x32_bf16 v[2:5], v[182:185], v[214:217], v[2:5]
	s_setprio 0
	s_barrier
	s_add_u32 s76, s76, 0x100
	s_addc_u32 s77, s77, 0
	s_add_u32 s40, s40, 0x100
	s_addc_u32 s41, s41, 0
	s_cmp_ge_i32 s78, s65
	s_mov_b32 s42, s78
	s_cbranch_scc0 .LBB0_3356
	v_readlane_b32 s76, v247, 9

; #define PG8_STAGE(bufoff, gbase, voff) do { _Pragma("unroll") for (int _i = 0; _i < 2; ++_i) \
;         __builtin_amdgcn_global_load_lds((const unsigned*)((const char*)(gbase) + (voff)[_i]), (PG8_LAS unsigned*)(lds + (bufoff) + ldsw + _i * 8192), 16, 0, 0); } while (0)
; #define PG8_LDA(dst, b, h) do { if constexpr (DT != 1) { _Pragma("unroll") for (int m = 0; m < 4; ++m) _Pragma("unroll") for (int k = 0; k < 2; ++k) dst[m][k] = *(const PG8_LAS bf16x8*)(lds + PG8_SA(b, h) + aoff + m * 2048 + k * 1024); } \
;         else { _Pragma("unroll") for (int m = 0; m < 4; ++m) dst##8[m] = ld32(lds + PG8_SA(b, h) + aoff + m * 2048); } } while (0)
; #define PG8_LDB(dst, b, h) do { if constexpr (DT != 1) { _Pragma("unroll") for (int n = 0; n < 2; ++n) _Pragma("unroll") for (int k = 0; k < 2; ++k) dst[n][k] = *(const PG8_LAS bf16x8*)(lds + PG8_SB(b, h) + boff + n * 2048 + k * 1024); } \
;         else { _Pragma("unroll") for (int n = 0; n < 2; ++n) dst##8[n] = ld32(lds + PG8_SB(b, h) + boff + n * 2048); } } while (0)
; #define PG8_WAIT_V(n) asm volatile("s_waitcnt vmcnt(" #n ")" ::: "memory")
; #define PG8_WAIT_L(n) asm volatile("s_waitcnt lgkmcnt(" #n ")" ::: "memory")
; #define PG8_BAR __builtin_amdgcn_s_barrier()
; #define PG8_SCHED __builtin_amdgcn_sched_barrier(0)
;     ...
;             PG8_LDB(B0, 0, 0); PG8_LDB(B1, 0, 1); PG8_SCHED; PG8_LDA(At, 0, 0); PG8_STAGE(PG8_SA(1, 1), a1 + hstepA, voffA);
;             PG8_WAIT_V(8); PG8_WAIT_L(0); PG8_BAR; PG8_MMA(0, 0, At, B0); PG8_MMA(0, 1, At, B1); PG8_BAR; PG8_SCHED;
;             PG8_LDA(At, 0, 1); PG8_STAGE(PG8_SB(0, 0), b2, voffB); PG8_STAGE(PG8_SB(0, 1), b2 + hstepB, voffB); PG8_STAGE(PG8_SA(0, 0), a2, voffA);
;             PG8_WAIT_V(8); PG8_WAIT_L(0); PG8_BAR; PG8_MMA(1, 0, At, B0); PG8_MMA(1, 1, At, B1); PG8_BAR; PG8_SCHED;
.LBB0_4141:
	v_add_u32_e32 v160, s35, v164
	ds_read_b128 v[122:125], v160
	ds_read_b128 v[126:129], v160 offset:1024
	ds_read_b128 v[130:133], v160 offset:2048
	ds_read_b128 v[170:173], v160 offset:3072
	v_add_u32_e32 v160, s36, v164
	ds_read_b128 v[174:177], v160
	ds_read_b128 v[178:181], v160 offset:1024
	ds_read_b128 v[182:185], v160 offset:2048
	ds_read_b128 v[186:189], v160 offset:3072
	s_add_i32 s69, s26, 2
	s_add_u32 s27, s24, 0xfffc0080
	s_addc_u32 s28, s25, -1
	s_cmp_eq_u32 s61, s26
	s_cselect_b32 s26, s66, s67
	s_cselect_b32 s29, s15, s28
	s_cselect_b32 s28, s17, s27
	s_cselect_b32 s27, s65, s68
	s_add_i32 m0, s46, 0xc000
	ds_read_b128 v[190:193], v167
	ds_read_b128 v[194:197], v167 offset:1024
	ds_read_b128 v[198:201], v167 offset:2048
	ds_read_b128 v[202:205], v167 offset:3072
	ds_read_b128 v[206:209], v167 offset:4096
	ds_read_b128 v[210:213], v167 offset:5120
	ds_read_b128 v[214:217], v167 offset:6144
	ds_read_b128 v[218:221], v167 offset:7168
	global_load_lds_dwordx4 v154, s[24:25]
	s_add_i32 m0, s46, 0xe000
	s_nop 0
	global_load_lds_dwordx4 v152, s[24:25]
	s_waitcnt vmcnt(8)
	s_waitcnt lgkmcnt(0)
	s_barrier
	s_setprio 1
	s_waitcnt lgkmcnt(0)
	v_mfma_i32_16x16x64_i8 v[134:137], v[122:125], v[190:193], v[134:137]
	v_mfma_i32_16x16x64_i8 v[114:117], v[130:133], v[190:193], v[114:117]
	v_mfma_i32_16x16x64_i8 v[106:109], v[122:125], v[198:201], v[106:109]
	v_mfma_i32_16x16x64_i8 v[98:101], v[130:133], v[198:201], v[98:101]
	v_mfma_i32_16x16x64_i8 v[90:93], v[122:125], v[206:209], v[90:93]
	v_mfma_i32_16x16x64_i8 v[82:85], v[130:133], v[206:209], v[82:85]
	v_mfma_i32_16x16x64_i8 v[74:77], v[122:125], v[214:217], v[74:77]
	v_mfma_i32_16x16x64_i8 v[66:69], v[130:133], v[214:217], v[66:69]
	v_mfma_i32_16x16x64_i8 v[134:137], v[126:129], v[194:197], v[134:137]
	v_mfma_i32_16x16x64_i8 v[114:117], v[170:173], v[194:197], v[114:117]
	v_mfma_i32_16x16x64_i8 v[106:109], v[126:129], v[202:205], v[106:109]
	v_mfma_i32_16x16x64_i8 v[98:101], v[170:173], v[202:205], v[98:101]
	v_mfma_i32_16x16x64_i8 v[90:93], v[126:129], v[210:213], v[90:93]
	v_mfma_i32_16x16x64_i8 v[82:85], v[170:173], v[210:213], v[82:85]
	v_mfma_i32_16x16x64_i8 v[74:77], v[126:129], v[218:221], v[74:77]
	v_mfma_i32_16x16x64_i8 v[66:69], v[170:173], v[218:221], v[66:69]
	v_mfma_i32_16x16x64_i8 v[138:141], v[174:177], v[190:193], v[138:141]
	v_mfma_i32_16x16x64_i8 v[118:121], v[182:185], v[190:193], v[118:121]
	v_mfma_i32_16x16x64_i8 v[110:113], v[174:177], v[198:201], v[110:113]
	v_mfma_i32_16x16x64_i8 v[102:105], v[182:185], v[198:201], v[102:105]
	v_mfma_i32_16x16x64_i8 v[94:97], v[174:177], v[206:209], v[94:97]
	v_mfma_i32_16x16x64_i8 v[86:89], v[182:185], v[206:209], v[86:89]
	v_mfma_i32_16x16x64_i8 v[78:81], v[174:177], v[214:217], v[78:81]
	v_mfma_i32_16x16x64_i8 v[70:73], v[182:185], v[214:217], v[70:73]
	v_mfma_i32_16x16x64_i8 v[138:141], v[178:181], v[194:197], v[138:141]
	v_mfma_i32_16x16x64_i8 v[118:121], v[186:189], v[194:197], v[118:121]
	v_mfma_i32_16x16x64_i8 v[110:113], v[178:181], v[202:205], v[110:113]
	v_mfma_i32_16x16x64_i8 v[102:105], v[186:189], v[202:205], v[102:105]
	v_mfma_i32_16x16x64_i8 v[94:97], v[178:181], v[210:213], v[94:97]
	v_mfma_i32_16x16x64_i8 v[86:89], v[186:189], v[210:213], v[86:89]
	v_mfma_i32_16x16x64_i8 v[78:81], v[178:181], v[218:221], v[78:81]
	v_mfma_i32_16x16x64_i8 v[70:73], v[186:189], v[218:221], v[70:73]
	s_setprio 0
	s_barrier
	s_mov_b32 m0, s23
	s_add_u32 s98, s26, 0x80
	s_addc_u32 s99, s27, 0
	s_add_u32 s70, s26, 0x40000
	ds_read_b128 v[190:193], v167 offset:16384
	ds_read_b128 v[194:197], v167 offset:17408
	ds_read_b128 v[198:201], v167 offset:18432
	ds_read_b128 v[202:205], v167 offset:19456
	ds_read_b128 v[206:209], v167 offset:20480
	ds_read_b128 v[210:213], v167 offset:21504
	ds_read_b128 v[214:217], v167 offset:22528
	ds_read_b128 v[218:221], v167 offset:23552
	global_load_lds_dwordx4 v144, s[26:27]
	s_mov_b32 m0, s43
	s_addc_u32 s71, s27, 0
	global_load_lds_dwordx4 v148, s[26:27]
	s_mov_b32 m0, s44
	s_nop 0
	global_load_lds_dwordx4 v144, s[70:71]
	s_mov_b32 m0, s45
	s_nop 0
	global_load_lds_dwordx4 v148, s[70:71]
	s_add_u32 s100, s28, 0x80
	s_addc_u32 s101, s29, 0
	s_mov_b32 m0, s46
	s_nop 0
	global_load_lds_dwordx4 v142, s[28:29]
	s_mov_b32 m0, s47
	s_nop 0
	global_load_lds_dwordx4 v146, s[28:29]
	s_waitcnt vmcnt(8)
	s_waitcnt lgkmcnt(0)
	s_barrier
	s_setprio 1
	s_waitcnt lgkmcnt(0)
	v_mfma_i32_16x16x64_i8 v[58:61], v[122:125], v[190:193], v[58:61]
	v_mfma_i32_16x16x64_i8 v[50:53], v[130:133], v[190:193], v[50:53]
	v_mfma_i32_16x16x64_i8 v[42:45], v[122:125], v[198:201], v[42:45]
	v_mfma_i32_16x16x64_i8 v[34:37], v[130:133], v[198:201], v[34:37]
	v_mfma_i32_16x16x64_i8 v[26:29], v[122:125], v[206:209], v[26:29]
	v_mfma_i32_16x16x64_i8 v[18:21], v[130:133], v[206:209], v[18:21]
	v_mfma_i32_16x16x64_i8 v[10:13], v[122:125], v[214:217], v[10:13]
	v_mfma_i32_16x16x64_i8 v[2:5], v[130:133], v[214:217], v[2:5]
	v_mfma_i32_16x16x64_i8 v[58:61], v[126:129], v[194:197], v[58:61]
	v_mfma_i32_16x16x64_i8 v[50:53], v[170:173], v[194:197], v[50:53]
	v_mfma_i32_16x16x64_i8 v[42:45], v[126:129], v[202:205], v[42:45]
	v_mfma_i32_16x16x64_i8 v[34:37], v[170:173], v[202:205], v[34:37]
	v_mfma_i32_16x16x64_i8 v[26:29], v[126:129], v[210:213], v[26:29]
	v_mfma_i32_16x16x64_i8 v[18:21], v[170:173], v[210:213], v[18:21]
	v_mfma_i32_16x16x64_i8 v[10:13], v[126:129], v[218:221], v[10:13]
	v_mfma_i32_16x16x64_i8 v[2:5], v[170:173], v[218:221], v[2:5]
	v_mfma_i32_16x16x64_i8 v[62:65], v[174:177], v[190:193], v[62:65]
	v_mfma_i32_16x16x64_i8 v[54:57], v[182:185], v[190:193], v[54:57]
	v_mfma_i32_16x16x64_i8 v[46:49], v[174:177], v[198:201], v[46:49]
	v_mfma_i32_16x16x64_i8 v[38:41], v[182:185], v[198:201], v[38:41]
	v_mfma_i32_16x16x64_i8 v[30:33], v[174:177], v[206:209], v[30:33]
	v_mfma_i32_16x16x64_i8 v[22:25], v[182:185], v[206:209], v[22:25]
	v_mfma_i32_16x16x64_i8 v[14:17], v[174:177], v[214:217], v[14:17]
	v_mfma_i32_16x16x64_i8 v[6:9], v[182:185], v[214:217], v[6:9]
	v_mfma_i32_16x16x64_i8 v[62:65], v[178:181], v[194:197], v[62:65]
	v_mfma_i32_16x16x64_i8 v[54:57], v[186:189], v[194:197], v[54:57]
	v_mfma_i32_16x16x64_i8 v[46:49], v[178:181], v[202:205], v[46:49]
	v_mfma_i32_16x16x64_i8 v[38:41], v[186:189], v[202:205], v[38:41]
	v_mfma_i32_16x16x64_i8 v[30:33], v[178:181], v[210:213], v[30:33]
	v_mfma_i32_16x16x64_i8 v[22:25], v[186:189], v[210:213], v[22:25]
	v_mfma_i32_16x16x64_i8 v[14:17], v[178:181], v[218:221], v[14:17]
	v_mfma_i32_16x16x64_i8 v[6:9], v[186:189], v[218:221], v[6:9]
	s_setprio 0
	s_barrier
; #define PG8_STAGE(bufoff, gbase, voff) do { _Pragma("unroll") for (int _i = 0; _i < 2; ++_i) \
;         __builtin_amdgcn_global_load_lds((const unsigned*)((const char*)(gbase) + (voff)[_i]), (PG8_LAS unsigned*)(lds + (bufoff) + ldsw + _i * 8192), 16, 0, 0); } while (0)
; #define PG8_LDA(dst, b, h) do { if constexpr (DT != 1) { _Pragma("unroll") for (int m = 0; m < 4; ++m) _Pragma("unroll") for (int k = 0; k < 2; ++k) dst[m][k] = *(const PG8_LAS bf16x8*)(lds + PG8_SA(b, h) + aoff + m * 2048 + k * 1024); } \
;         else { _Pragma("unroll") for (int m = 0; m < 4; ++m) dst##8[m] = ld32(lds + PG8_SA(b, h) + aoff + m * 2048); } } while (0)
; #define PG8_LDB(dst, b, h) do { if constexpr (DT != 1) { _Pragma("unroll") for (int n = 0; n < 2; ++n) _Pragma("unroll") for (int k = 0; k < 2; ++k) dst[n][k] = *(const PG8_LAS bf16x8*)(lds + PG8_SB(b, h) + boff + n * 2048 + k * 1024); } \
;         else { _Pragma("unroll") for (int n = 0; n < 2; ++n) dst##8[n] = ld32(lds + PG8_SB(b, h) + boff + n * 2048); } } while (0)
; #define PG8_WAIT_V(n) asm volatile("s_waitcnt vmcnt(" #n ")" ::: "memory")
; #define PG8_WAIT_L(n) asm volatile("s_waitcnt lgkmcnt(" #n ")" ::: "memory")
; #define PG8_BAR __builtin_amdgcn_s_barrier()
; #define PG8_SCHED __builtin_amdgcn_sched_barrier(0)
;     ...
;         for (int t = 0; t < nt; t += 2) {
;             const bool last = (t == nt - 2);
;             const char* a1 = cA + (size_t)(t + 1) * kstep;
;             const char* a2 = last ? nA : cA + (size_t)(t + 2) * kstep; const char* b2 = last ? nB : cB + (size_t)(t + 2) * kstep;
;     ...
;             PG8_LDB(B0, 1, 0); PG8_LDB(B1, 1, 1); PG8_SCHED; PG8_LDA(At, 1, 0); PG8_STAGE(PG8_SA(0, 1), a2 + hstepA, voffA);
;             PG8_WAIT_V(8); PG8_WAIT_L(0); PG8_BAR; PG8_MMA(0, 0, At, B0); PG8_MMA(0, 1, At, B1); PG8_BAR; PG8_SCHED;
;             PG8_LDA(At, 1, 1); PG8_STAGE(PG8_SB(1, 0), b3, voffB); PG8_STAGE(PG8_SB(1, 1), b3 + hstepB, voffB); PG8_STAGE(PG8_SA(1, 0), a3, voffA);
;             PG8_WAIT_V(8); PG8_WAIT_L(0); PG8_BAR; PG8_MMA(1, 0, At, B0); PG8_MMA(1, 1, At, B1); PG8_BAR; PG8_SCHED;
	v_add_u32_e32 v160, s51, v164
	ds_read_b128 v[122:125], v160
	ds_read_b128 v[126:129], v160 offset:1024
	ds_read_b128 v[130:133], v160 offset:2048
	ds_read_b128 v[170:173], v160 offset:3072
	v_add_u32_e32 v160, s52, v164
	ds_read_b128 v[174:177], v160
	ds_read_b128 v[178:181], v160 offset:1024
	ds_read_b128 v[182:185], v160 offset:2048
	ds_read_b128 v[186:189], v160 offset:3072
	s_add_u32 s28, s28, 0x40000
	s_addc_u32 s29, s29, 0
	s_mov_b32 m0, s48
	ds_read_b128 v[190:193], v167 offset:32768
	ds_read_b128 v[194:197], v167 offset:33792
	ds_read_b128 v[198:201], v167 offset:34816
	ds_read_b128 v[202:205], v167 offset:35840
	ds_read_b128 v[206:209], v167 offset:36864
	ds_read_b128 v[210:213], v167 offset:37888
	ds_read_b128 v[214:217], v167 offset:38912
	ds_read_b128 v[218:221], v167 offset:39936
	global_load_lds_dwordx4 v142, s[28:29]
	s_mov_b32 m0, s49
	s_nop 0
	global_load_lds_dwordx4 v146, s[28:29]
	s_waitcnt vmcnt(8)
	s_waitcnt lgkmcnt(0)
	s_barrier
	s_setprio 1
	s_waitcnt lgkmcnt(0)
	v_mfma_i32_16x16x64_i8 v[134:137], v[122:125], v[190:193], v[134:137]
	v_mfma_i32_16x16x64_i8 v[114:117], v[130:133], v[190:193], v[114:117]
	v_mfma_i32_16x16x64_i8 v[106:109], v[122:125], v[198:201], v[106:109]
	v_mfma_i32_16x16x64_i8 v[98:101], v[130:133], v[198:201], v[98:101]
	v_mfma_i32_16x16x64_i8 v[90:93], v[122:125], v[206:209], v[90:93]
	v_mfma_i32_16x16x64_i8 v[82:85], v[130:133], v[206:209], v[82:85]
	v_mfma_i32_16x16x64_i8 v[74:77], v[122:125], v[214:217], v[74:77]
	v_mfma_i32_16x16x64_i8 v[66:69], v[130:133], v[214:217], v[66:69]
	v_mfma_i32_16x16x64_i8 v[134:137], v[126:129], v[194:197], v[134:137]
	v_mfma_i32_16x16x64_i8 v[114:117], v[170:173], v[194:197], v[114:117]
	v_mfma_i32_16x16x64_i8 v[106:109], v[126:129], v[202:205], v[106:109]
	v_mfma_i32_16x16x64_i8 v[98:101], v[170:173], v[202:205], v[98:101]
	v_mfma_i32_16x16x64_i8 v[90:93], v[126:129], v[210:213], v[90:93]
	v_mfma_i32_16x16x64_i8 v[82:85], v[170:173], v[210:213], v[82:85]
	v_mfma_i32_16x16x64_i8 v[74:77], v[126:129], v[218:221], v[74:77]
	v_mfma_i32_16x16x64_i8 v[66:69], v[170:173], v[218:221], v[66:69]
	v_mfma_i32_16x16x64_i8 v[138:141], v[174:177], v[190:193], v[138:141]
	v_mfma_i32_16x16x64_i8 v[118:121], v[182:185], v[190:193], v[118:121]
	v_mfma_i32_16x16x64_i8 v[110:113], v[174:177], v[198:201], v[110:113]
	v_mfma_i32_16x16x64_i8 v[102:105], v[182:185], v[198:201], v[102:105]
	v_mfma_i32_16x16x64_i8 v[94:97], v[174:177], v[206:209], v[94:97]
	v_mfma_i32_16x16x64_i8 v[86:89], v[182:185], v[206:209], v[86:89]
	v_mfma_i32_16x16x64_i8 v[78:81], v[174:177], v[214:217], v[78:81]
	v_mfma_i32_16x16x64_i8 v[70:73], v[182:185], v[214:217], v[70:73]
	v_mfma_i32_16x16x64_i8 v[138:141], v[178:181], v[194:197], v[138:141]
	v_mfma_i32_16x16x64_i8 v[118:121], v[186:189], v[194:197], v[118:121]
	v_mfma_i32_16x16x64_i8 v[110:113], v[178:181], v[202:205], v[110:113]
	v_mfma_i32_16x16x64_i8 v[102:105], v[186:189], v[202:205], v[102:105]
	v_mfma_i32_16x16x64_i8 v[94:97], v[178:181], v[210:213], v[94:97]
	v_mfma_i32_16x16x64_i8 v[86:89], v[186:189], v[210:213], v[86:89]
	v_mfma_i32_16x16x64_i8 v[78:81], v[178:181], v[218:221], v[78:81]
	v_mfma_i32_16x16x64_i8 v[70:73], v[186:189], v[218:221], v[70:73]
	s_setprio 0
	s_barrier
	s_mov_b32 m0, s55
	s_add_u32 s26, s26, 0x40080
	ds_read_b128 v[190:193], v167 offset:49152
	ds_read_b128 v[194:197], v167 offset:50176
	ds_read_b128 v[198:201], v167 offset:51200
	ds_read_b128 v[202:205], v167 offset:52224
	ds_read_b128 v[206:209], v167 offset:53248
	ds_read_b128 v[210:213], v167 offset:54272
	ds_read_b128 v[214:217], v167 offset:55296
	ds_read_b128 v[218:221], v167 offset:56320
	global_load_lds_dwordx4 v144, s[98:99]
	s_mov_b32 m0, s56
	s_addc_u32 s27, s27, 0
	global_load_lds_dwordx4 v148, s[98:99]
	s_mov_b32 m0, s59
	s_nop 0
	global_load_lds_dwordx4 v144, s[26:27]
	s_mov_b32 m0, s60
	s_nop 0
	global_load_lds_dwordx4 v148, s[26:27]
	s_mov_b32 m0, s57
	s_nop 0
	global_load_lds_dwordx4 v142, s[100:101]
	s_mov_b32 m0, s58
	s_nop 0
	global_load_lds_dwordx4 v146, s[100:101]
	s_waitcnt vmcnt(8)
	s_waitcnt lgkmcnt(0)
	s_barrier
	s_setprio 1
	s_waitcnt lgkmcnt(0)
	v_mfma_i32_16x16x64_i8 v[58:61], v[122:125], v[190:193], v[58:61]
	v_mfma_i32_16x16x64_i8 v[50:53], v[130:133], v[190:193], v[50:53]
	v_mfma_i32_16x16x64_i8 v[42:45], v[122:125], v[198:201], v[42:45]
	v_mfma_i32_16x16x64_i8 v[34:37], v[130:133], v[198:201], v[34:37]
	v_mfma_i32_16x16x64_i8 v[26:29], v[122:125], v[206:209], v[26:29]
	v_mfma_i32_16x16x64_i8 v[18:21], v[130:133], v[206:209], v[18:21]
	v_mfma_i32_16x16x64_i8 v[10:13], v[122:125], v[214:217], v[10:13]
	v_mfma_i32_16x16x64_i8 v[2:5], v[130:133], v[214:217], v[2:5]
	v_mfma_i32_16x16x64_i8 v[58:61], v[126:129], v[194:197], v[58:61]
	v_mfma_i32_16x16x64_i8 v[50:53], v[170:173], v[194:197], v[50:53]
	v_mfma_i32_16x16x64_i8 v[42:45], v[126:129], v[202:205], v[42:45]
	v_mfma_i32_16x16x64_i8 v[34:37], v[170:173], v[202:205], v[34:37]
	v_mfma_i32_16x16x64_i8 v[26:29], v[126:129], v[210:213], v[26:29]
	v_mfma_i32_16x16x64_i8 v[18:21], v[170:173], v[210:213], v[18:21]
	v_mfma_i32_16x16x64_i8 v[10:13], v[126:129], v[218:221], v[10:13]
	v_mfma_i32_16x16x64_i8 v[2:5], v[170:173], v[218:221], v[2:5]
	v_mfma_i32_16x16x64_i8 v[62:65], v[174:177], v[190:193], v[62:65]
	v_mfma_i32_16x16x64_i8 v[54:57], v[182:185], v[190:193], v[54:57]
	v_mfma_i32_16x16x64_i8 v[46:49], v[174:177], v[198:201], v[46:49]
	v_mfma_i32_16x16x64_i8 v[38:41], v[182:185], v[198:201], v[38:41]
	v_mfma_i32_16x16x64_i8 v[30:33], v[174:177], v[206:209], v[30:33]
	v_mfma_i32_16x16x64_i8 v[22:25], v[182:185], v[206:209], v[22:25]
	v_mfma_i32_16x16x64_i8 v[14:17], v[174:177], v[214:217], v[14:17]
	v_mfma_i32_16x16x64_i8 v[6:9], v[182:185], v[214:217], v[6:9]
	v_mfma_i32_16x16x64_i8 v[62:65], v[178:181], v[194:197], v[62:65]
	v_mfma_i32_16x16x64_i8 v[54:57], v[186:189], v[194:197], v[54:57]
	v_mfma_i32_16x16x64_i8 v[46:49], v[178:181], v[202:205], v[46:49]
	v_mfma_i32_16x16x64_i8 v[38:41], v[186:189], v[202:205], v[38:41]
	v_mfma_i32_16x16x64_i8 v[30:33], v[178:181], v[210:213], v[30:33]
	v_mfma_i32_16x16x64_i8 v[22:25], v[186:189], v[210:213], v[22:25]
	v_mfma_i32_16x16x64_i8 v[14:17], v[178:181], v[218:221], v[14:17]
	v_mfma_i32_16x16x64_i8 v[6:9], v[186:189], v[218:221], v[6:9]
	s_setprio 0
	s_barrier
	s_add_u32 s67, s67, 0x100
	s_addc_u32 s68, s68, 0
	s_add_u32 s24, s24, 0x100
	s_addc_u32 s25, s25, 0
	s_cmp_ge_i32 s69, s54
	s_mov_b32 s26, s69
	s_cbranch_scc0 .LBB0_4141

; #define PG8_STAGE(bufoff, gbase, voff) do { _Pragma("unroll") for (int _i = 0; _i < 2; ++_i) \
;         __builtin_amdgcn_global_load_lds((const unsigned*)((const char*)(gbase) + (voff)[_i]), (PG8_LAS unsigned*)(lds + (bufoff) + ldsw + _i * 8192), 16, 0, 0); } while (0)
; #define PG8_LDA(dst, b, h) do { if constexpr (DT != 1) { _Pragma("unroll") for (int m = 0; m < 4; ++m) _Pragma("unroll") for (int k = 0; k < 2; ++k) dst[m][k] = *(const PG8_LAS bf16x8*)(lds + PG8_SA(b, h) + aoff + m * 2048 + k * 1024); } \
;         else { _Pragma("unroll") for (int m = 0; m < 4; ++m) dst##8[m] = ld32(lds + PG8_SA(b, h) + aoff + m * 2048); } } while (0)
; #define PG8_LDB(dst, b, h) do { if constexpr (DT != 1) { _Pragma("unroll") for (int n = 0; n < 2; ++n) _Pragma("unroll") for (int k = 0; k < 2; ++k) dst[n][k] = *(const PG8_LAS bf16x8*)(lds + PG8_SB(b, h) + boff + n * 2048 + k * 1024); } \
;         else { _Pragma("unroll") for (int n = 0; n < 2; ++n) dst##8[n] = ld32(lds + PG8_SB(b, h) + boff + n * 2048); } } while (0)
; #define PG8_WAIT_V(n) asm volatile("s_waitcnt vmcnt(" #n ")" ::: "memory")
; #define PG8_WAIT_L(n) asm volatile("s_waitcnt lgkmcnt(" #n ")" ::: "memory")
; #define PG8_BAR __builtin_amdgcn_s_barrier()
; #define PG8_SCHED __builtin_amdgcn_sched_barrier(0)
;     ...
;             PG8_LDB(B0, 0, 0); PG8_LDB(B1, 0, 1); PG8_SCHED; PG8_LDA(At, 0, 0); PG8_STAGE(PG8_SA(1, 1), a1 + hstepA, voffA);
;             PG8_WAIT_V(8); PG8_WAIT_L(0); PG8_BAR; PG8_MMA(0, 0, At, B0); PG8_MMA(0, 1, At, B1); PG8_BAR; PG8_SCHED;
;             PG8_LDA(At, 0, 1); PG8_STAGE(PG8_SB(0, 0), b2, voffB); PG8_STAGE(PG8_SB(0, 1), b2 + hstepB, voffB); PG8_STAGE(PG8_SA(0, 0), a2, voffA);
;             PG8_WAIT_V(8); PG8_WAIT_L(0); PG8_BAR; PG8_MMA(1, 0, At, B0); PG8_MMA(1, 1, At, B1); PG8_BAR; PG8_SCHED;
.LBB0_4217:
	ds_read_b128 v[18:21], v187
	ds_read_b128 v[22:25], v187 offset:16
	ds_read_b128 v[26:29], v187 offset:2048
	ds_read_b128 v[30:33], v187 offset:2064
	ds_read_b128 v[2:5], v188
	ds_read_b128 v[6:9], v188 offset:16
	ds_read_b128 v[10:13], v188 offset:2048
	ds_read_b128 v[14:17], v188 offset:2064
	s_add_i32 s68, s34, 2
	s_add_u32 s30, s28, 0x100
	s_addc_u32 s31, s29, 0
	s_cmp_eq_u32 s59, s34
	s_cselect_b32 s34, s26, s66
	s_cselect_b32 s37, s3, s31
	s_cselect_b32 s36, s2, s30
	s_cselect_b32 s35, s27, s67
	v_lshl_add_u64 v[218:219], s[28:29], 0, v[172:173]
	s_add_i32 m0, s47, 0xc000
	ds_read_b128 v[178:181], v189
	ds_read_b128 v[182:185], v189 offset:16
	ds_read_b128 v[194:197], v189 offset:2048
	ds_read_b128 v[198:201], v189 offset:2064
	ds_read_b128 v[202:205], v189 offset:4096
	ds_read_b128 v[206:209], v189 offset:4112
	ds_read_b128 v[210:213], v189 offset:6144
	ds_read_b128 v[214:217], v189 offset:6160
	global_load_lds_dwordx4 v[218:219], off
	v_lshl_add_u64 v[218:219], s[28:29], 0, v[170:171]
	s_add_i32 m0, s47, 0xe000
	s_nop 0
	global_load_lds_dwordx4 v[218:219], off
	s_waitcnt vmcnt(8)
	s_waitcnt lgkmcnt(0)
	s_barrier
	s_setprio 1
	s_waitcnt lgkmcnt(0)
	v_mfma_scale_f32_16x16x128_f8f6f4 v[158:161], v[18:25], v[178:185], v[158:161], v190, v190 op_sel_hi:[0,0,0]
	v_mfma_scale_f32_16x16x128_f8f6f4 v[154:157], v[26:33], v[178:185], v[154:157], v190, v190 op_sel_hi:[0,0,0]
	v_mfma_scale_f32_16x16x128_f8f6f4 v[150:153], v[18:25], v[194:201], v[150:153], v190, v190 op_sel_hi:[0,0,0]
	v_mfma_scale_f32_16x16x128_f8f6f4 v[146:149], v[26:33], v[194:201], v[146:149], v190, v190 op_sel_hi:[0,0,0]
	v_mfma_scale_f32_16x16x128_f8f6f4 v[126:129], v[18:25], v[202:209], v[126:129], v190, v190 op_sel_hi:[0,0,0]
	v_mfma_scale_f32_16x16x128_f8f6f4 v[122:125], v[26:33], v[202:209], v[122:125], v190, v190 op_sel_hi:[0,0,0]
	v_mfma_scale_f32_16x16x128_f8f6f4 v[118:121], v[18:25], v[210:217], v[118:121], v190, v190 op_sel_hi:[0,0,0]
	v_mfma_scale_f32_16x16x128_f8f6f4 v[110:113], v[26:33], v[210:217], v[110:113], v190, v190 op_sel_hi:[0,0,0]
	v_mfma_scale_f32_16x16x128_f8f6f4 v[142:145], v[2:9], v[178:185], v[142:145], v190, v190 op_sel_hi:[0,0,0]
	v_mfma_scale_f32_16x16x128_f8f6f4 v[138:141], v[10:17], v[178:185], v[138:141], v190, v190 op_sel_hi:[0,0,0]
	v_mfma_scale_f32_16x16x128_f8f6f4 v[134:137], v[2:9], v[194:201], v[134:137], v190, v190 op_sel_hi:[0,0,0]
	v_mfma_scale_f32_16x16x128_f8f6f4 v[130:133], v[10:17], v[194:201], v[130:133], v190, v190 op_sel_hi:[0,0,0]
	v_mfma_scale_f32_16x16x128_f8f6f4 v[114:117], v[2:9], v[202:209], v[114:117], v190, v190 op_sel_hi:[0,0,0]
	v_mfma_scale_f32_16x16x128_f8f6f4 v[106:109], v[10:17], v[202:209], v[106:109], v190, v190 op_sel_hi:[0,0,0]
	v_mfma_scale_f32_16x16x128_f8f6f4 v[102:105], v[2:9], v[210:217], v[102:105], v190, v190 op_sel_hi:[0,0,0]
	v_mfma_scale_f32_16x16x128_f8f6f4 v[98:101], v[10:17], v[210:217], v[98:101], v190, v190 op_sel_hi:[0,0,0]
	s_setprio 0
	s_barrier
	s_mov_b32 m0, s43
	s_add_u32 s98, s34, 0x80
	s_addc_u32 s99, s35, 0
	s_add_u32 s28, s34, 0xb0000
	ds_read_b128 v[194:197], v189 offset:16384
	ds_read_b128 v[198:201], v189 offset:16400
	ds_read_b128 v[202:205], v189 offset:18432
	ds_read_b128 v[206:209], v189 offset:18448
	ds_read_b128 v[210:213], v189 offset:20480
	ds_read_b128 v[214:217], v189 offset:20496
	ds_read_b128 v[218:221], v189 offset:22528
	ds_read_b128 v[222:225], v189 offset:22544
	global_load_lds_dwordx4 v164, s[34:35]
	s_mov_b32 m0, s44
	s_addc_u32 s29, s35, 0
	global_load_lds_dwordx4 v168, s[34:35]
	s_mov_b32 m0, s45
	s_nop 0
	global_load_lds_dwordx4 v164, s[28:29]
	s_mov_b32 m0, s46
	s_nop 0
	global_load_lds_dwordx4 v168, s[28:29]
	s_add_u32 s100, s36, 0x80
	s_addc_u32 s101, s37, 0
	s_mov_b32 m0, s47
	s_nop 0
	global_load_lds_dwordx4 v162, s[36:37]
	s_mov_b32 m0, s48
	s_nop 0
	global_load_lds_dwordx4 v166, s[36:37]
	s_waitcnt vmcnt(8)
	s_waitcnt lgkmcnt(0)
	s_barrier
	s_setprio 1
	s_waitcnt lgkmcnt(0)
	v_mfma_scale_f32_16x16x128_f8f6f4 v[94:97], v[18:25], v[194:201], v[94:97], v190, v190 op_sel_hi:[0,0,0]
	v_mfma_scale_f32_16x16x128_f8f6f4 v[90:93], v[26:33], v[194:201], v[90:93], v190, v190 op_sel_hi:[0,0,0]
	v_mfma_scale_f32_16x16x128_f8f6f4 v[78:81], v[18:25], v[202:209], v[78:81], v190, v190 op_sel_hi:[0,0,0]
	v_mfma_scale_f32_16x16x128_f8f6f4 v[74:77], v[26:33], v[202:209], v[74:77], v190, v190 op_sel_hi:[0,0,0]
	v_mfma_scale_f32_16x16x128_f8f6f4 v[226:229], v[18:25], v[210:217], v[62:65], v190, v190 op_sel_hi:[0,0,0]
	v_mfma_scale_f32_16x16x128_f8f6f4 v[230:233], v[26:33], v[210:217], v[58:61], v190, v190 op_sel_hi:[0,0,0]
	v_mfma_scale_f32_16x16x128_f8f6f4 v[234:237], v[18:25], v[218:225], v[46:49], v190, v190 op_sel_hi:[0,0,0]
	v_mfma_scale_f32_16x16x128_f8f6f4 v[238:241], v[26:33], v[218:225], v[42:45], v190, v190 op_sel_hi:[0,0,0]
	v_mfma_scale_f32_16x16x128_f8f6f4 v[86:89], v[2:9], v[194:201], v[86:89], v190, v190 op_sel_hi:[0,0,0]
	v_mfma_scale_f32_16x16x128_f8f6f4 v[82:85], v[10:17], v[194:201], v[82:85], v190, v190 op_sel_hi:[0,0,0]
	v_mfma_scale_f32_16x16x128_f8f6f4 v[70:73], v[2:9], v[202:209], v[70:73], v190, v190 op_sel_hi:[0,0,0]
	v_mfma_scale_f32_16x16x128_f8f6f4 v[66:69], v[10:17], v[202:209], v[66:69], v190, v190 op_sel_hi:[0,0,0]
	v_mfma_scale_f32_16x16x128_f8f6f4 v[242:245], v[2:9], v[210:217], v[54:57], v190, v190 op_sel_hi:[0,0,0]
	v_mfma_scale_f32_16x16x128_f8f6f4 v[210:213], v[10:17], v[210:217], v[50:53], v190, v190 op_sel_hi:[0,0,0]
	v_mfma_scale_f32_16x16x128_f8f6f4 v[214:217], v[2:9], v[218:225], v[38:41], v190, v190 op_sel_hi:[0,0,0]
	v_mfma_scale_f32_16x16x128_f8f6f4 v[218:221], v[10:17], v[218:225], v[34:37], v190, v190 op_sel_hi:[0,0,0]
	s_setprio 0
	s_barrier
; #define PG8_STAGE(bufoff, gbase, voff) do { _Pragma("unroll") for (int _i = 0; _i < 2; ++_i) \
;         __builtin_amdgcn_global_load_lds((const unsigned*)((const char*)(gbase) + (voff)[_i]), (PG8_LAS unsigned*)(lds + (bufoff) + ldsw + _i * 8192), 16, 0, 0); } while (0)
; #define PG8_LDA(dst, b, h) do { if constexpr (DT != 1) { _Pragma("unroll") for (int m = 0; m < 4; ++m) _Pragma("unroll") for (int k = 0; k < 2; ++k) dst[m][k] = *(const PG8_LAS bf16x8*)(lds + PG8_SA(b, h) + aoff + m * 2048 + k * 1024); } \
;         else { _Pragma("unroll") for (int m = 0; m < 4; ++m) dst##8[m] = ld32(lds + PG8_SA(b, h) + aoff + m * 2048); } } while (0)
; #define PG8_LDB(dst, b, h) do { if constexpr (DT != 1) { _Pragma("unroll") for (int n = 0; n < 2; ++n) _Pragma("unroll") for (int k = 0; k < 2; ++k) dst[n][k] = *(const PG8_LAS bf16x8*)(lds + PG8_SB(b, h) + boff + n * 2048 + k * 1024); } \
;         else { _Pragma("unroll") for (int n = 0; n < 2; ++n) dst##8[n] = ld32(lds + PG8_SB(b, h) + boff + n * 2048); } } while (0)
; #define PG8_WAIT_V(n) asm volatile("s_waitcnt vmcnt(" #n ")" ::: "memory")
; #define PG8_WAIT_L(n) asm volatile("s_waitcnt lgkmcnt(" #n ")" ::: "memory")
; #define PG8_BAR __builtin_amdgcn_s_barrier()
; #define PG8_SCHED __builtin_amdgcn_sched_barrier(0)
;     ...
;             PG8_LDB(B0, 1, 0); PG8_LDB(B1, 1, 1); PG8_SCHED; PG8_LDA(At, 1, 0); PG8_STAGE(PG8_SA(0, 1), a2 + hstepA, voffA);
;             PG8_WAIT_V(8); PG8_WAIT_L(0); PG8_BAR; PG8_MMA(0, 0, At, B0); PG8_MMA(0, 1, At, B1); PG8_BAR; PG8_SCHED;
;             PG8_LDA(At, 1, 1); PG8_STAGE(PG8_SB(1, 0), b3, voffB); PG8_STAGE(PG8_SB(1, 1), b3 + hstepB, voffB); PG8_STAGE(PG8_SA(1, 0), a3, voffA);
;             PG8_WAIT_V(8); PG8_WAIT_L(0); PG8_BAR; PG8_MMA(1, 0, At, B0); PG8_MMA(1, 1, At, B1); PG8_BAR; PG8_SCHED;
	ds_read_b128 v[2:5], v191
	ds_read_b128 v[6:9], v191 offset:16
	ds_read_b128 v[10:13], v191 offset:2048
	ds_read_b128 v[14:17], v191 offset:2064
	ds_read_b128 v[18:21], v192
	ds_read_b128 v[22:25], v192 offset:16
	ds_read_b128 v[26:29], v192 offset:2048
	ds_read_b128 v[30:33], v192 offset:2064
	s_add_u32 s28, s36, 0xb0000
	s_addc_u32 s29, s37, 0
	s_mov_b32 m0, s49
	ds_read_b128 v[34:37], v189 offset:32768
	ds_read_b128 v[38:41], v189 offset:32784
	ds_read_b128 v[42:45], v189 offset:34816
	ds_read_b128 v[46:49], v189 offset:34832
	ds_read_b128 v[50:53], v189 offset:36864
	ds_read_b128 v[54:57], v189 offset:36880
	ds_read_b128 v[58:61], v189 offset:38912
	ds_read_b128 v[62:65], v189 offset:38928
	global_load_lds_dwordx4 v162, s[28:29]
	s_mov_b32 m0, s50
	s_nop 0
	global_load_lds_dwordx4 v166, s[28:29]
	s_waitcnt vmcnt(8)
	s_waitcnt lgkmcnt(0)
	s_barrier
	s_setprio 1
	s_waitcnt lgkmcnt(0)
	v_mfma_scale_f32_16x16x128_f8f6f4 v[158:161], v[2:9], v[34:41], v[158:161], v190, v190 op_sel_hi:[0,0,0]
	v_mfma_scale_f32_16x16x128_f8f6f4 v[154:157], v[10:17], v[34:41], v[154:157], v190, v190 op_sel_hi:[0,0,0]
	v_mfma_scale_f32_16x16x128_f8f6f4 v[150:153], v[2:9], v[42:49], v[150:153], v190, v190 op_sel_hi:[0,0,0]
	v_mfma_scale_f32_16x16x128_f8f6f4 v[146:149], v[10:17], v[42:49], v[146:149], v190, v190 op_sel_hi:[0,0,0]
	v_mfma_scale_f32_16x16x128_f8f6f4 v[126:129], v[2:9], v[50:57], v[126:129], v190, v190 op_sel_hi:[0,0,0]
	v_mfma_scale_f32_16x16x128_f8f6f4 v[122:125], v[10:17], v[50:57], v[122:125], v190, v190 op_sel_hi:[0,0,0]
	v_mfma_scale_f32_16x16x128_f8f6f4 v[118:121], v[2:9], v[58:65], v[118:121], v190, v190 op_sel_hi:[0,0,0]
	v_mfma_scale_f32_16x16x128_f8f6f4 v[110:113], v[10:17], v[58:65], v[110:113], v190, v190 op_sel_hi:[0,0,0]
	v_mfma_scale_f32_16x16x128_f8f6f4 v[142:145], v[18:25], v[34:41], v[142:145], v190, v190 op_sel_hi:[0,0,0]
	v_mfma_scale_f32_16x16x128_f8f6f4 v[138:141], v[26:33], v[34:41], v[138:141], v190, v190 op_sel_hi:[0,0,0]
	v_mfma_scale_f32_16x16x128_f8f6f4 v[134:137], v[18:25], v[42:49], v[134:137], v190, v190 op_sel_hi:[0,0,0]
	v_mfma_scale_f32_16x16x128_f8f6f4 v[130:133], v[26:33], v[42:49], v[130:133], v190, v190 op_sel_hi:[0,0,0]
	v_mfma_scale_f32_16x16x128_f8f6f4 v[114:117], v[18:25], v[50:57], v[114:117], v190, v190 op_sel_hi:[0,0,0]
	v_mfma_scale_f32_16x16x128_f8f6f4 v[106:109], v[26:33], v[50:57], v[106:109], v190, v190 op_sel_hi:[0,0,0]
	v_mfma_scale_f32_16x16x128_f8f6f4 v[102:105], v[18:25], v[58:65], v[102:105], v190, v190 op_sel_hi:[0,0,0]
	v_mfma_scale_f32_16x16x128_f8f6f4 v[98:101], v[26:33], v[58:65], v[98:101], v190, v190 op_sel_hi:[0,0,0]
	s_setprio 0
	s_barrier
	s_mov_b32 m0, s53
	s_add_u32 s28, s34, 0xb0080
	ds_read_b128 v[34:37], v189 offset:49152
	ds_read_b128 v[38:41], v189 offset:49168
	ds_read_b128 v[50:53], v189 offset:51200
	ds_read_b128 v[54:57], v189 offset:51216
	ds_read_b128 v[194:197], v189 offset:53248
	ds_read_b128 v[198:201], v189 offset:53264
	ds_read_b128 v[202:205], v189 offset:55296
	ds_read_b128 v[206:209], v189 offset:55312
	global_load_lds_dwordx4 v164, s[98:99]
	s_mov_b32 m0, s54
	s_addc_u32 s29, s35, 0
	global_load_lds_dwordx4 v168, s[98:99]
	s_mov_b32 m0, s57
	s_nop 0
	global_load_lds_dwordx4 v164, s[28:29]
	s_mov_b32 m0, s58
	s_nop 0
	global_load_lds_dwordx4 v168, s[28:29]
	s_mov_b32 m0, s55
	s_nop 0
	global_load_lds_dwordx4 v162, s[100:101]
	s_mov_b32 m0, s56
	s_nop 0
	global_load_lds_dwordx4 v166, s[100:101]
	s_waitcnt vmcnt(8)
	s_waitcnt lgkmcnt(0)
	s_barrier
	s_setprio 1
	s_waitcnt lgkmcnt(0)
	v_mfma_scale_f32_16x16x128_f8f6f4 v[94:97], v[2:9], v[34:41], v[94:97], v190, v190 op_sel_hi:[0,0,0]
	v_mfma_scale_f32_16x16x128_f8f6f4 v[90:93], v[10:17], v[34:41], v[90:93], v190, v190 op_sel_hi:[0,0,0]
	v_mfma_scale_f32_16x16x128_f8f6f4 v[78:81], v[2:9], v[50:57], v[78:81], v190, v190 op_sel_hi:[0,0,0]
	v_mfma_scale_f32_16x16x128_f8f6f4 v[74:77], v[10:17], v[50:57], v[74:77], v190, v190 op_sel_hi:[0,0,0]
	v_mfma_scale_f32_16x16x128_f8f6f4 v[62:65], v[2:9], v[194:201], v[226:229], v190, v190 op_sel_hi:[0,0,0]
	v_mfma_scale_f32_16x16x128_f8f6f4 v[58:61], v[10:17], v[194:201], v[230:233], v190, v190 op_sel_hi:[0,0,0]
	v_mfma_scale_f32_16x16x128_f8f6f4 v[46:49], v[2:9], v[202:209], v[234:237], v190, v190 op_sel_hi:[0,0,0]
	v_mfma_scale_f32_16x16x128_f8f6f4 v[42:45], v[10:17], v[202:209], v[238:241], v190, v190 op_sel_hi:[0,0,0]
	v_mfma_scale_f32_16x16x128_f8f6f4 v[86:89], v[18:25], v[34:41], v[86:89], v190, v190 op_sel_hi:[0,0,0]
	v_mfma_scale_f32_16x16x128_f8f6f4 v[82:85], v[26:33], v[34:41], v[82:85], v190, v190 op_sel_hi:[0,0,0]
	v_mfma_scale_f32_16x16x128_f8f6f4 v[70:73], v[18:25], v[50:57], v[70:73], v190, v190 op_sel_hi:[0,0,0]
	v_mfma_scale_f32_16x16x128_f8f6f4 v[66:69], v[26:33], v[50:57], v[66:69], v190, v190 op_sel_hi:[0,0,0]
	v_mfma_scale_f32_16x16x128_f8f6f4 v[54:57], v[18:25], v[194:201], v[242:245], v190, v190 op_sel_hi:[0,0,0]
	v_mfma_scale_f32_16x16x128_f8f6f4 v[50:53], v[26:33], v[194:201], v[210:213], v190, v190 op_sel_hi:[0,0,0]
	v_mfma_scale_f32_16x16x128_f8f6f4 v[38:41], v[18:25], v[202:209], v[214:217], v190, v190 op_sel_hi:[0,0,0]
	v_mfma_scale_f32_16x16x128_f8f6f4 v[34:37], v[26:33], v[202:209], v[218:221], v190, v190 op_sel_hi:[0,0,0]
	s_setprio 0
	s_barrier
	s_add_u32 s66, s66, 0x100
	s_addc_u32 s67, s67, 0
	s_cmp_ge_i32 s68, s52
	s_mov_b64 s[28:29], s[30:31]
	s_mov_b32 s34, s68
	s_cbranch_scc0 .LBB0_4217

; #define PG8_STAGE(bufoff, gbase, voff) do { _Pragma("unroll") for (int _i = 0; _i < 2; ++_i) \
;         __builtin_amdgcn_global_load_lds((const unsigned*)((const char*)(gbase) + (voff)[_i]), (PG8_LAS unsigned*)(lds + (bufoff) + ldsw + _i * 8192), 16, 0, 0); } while (0)
; #define PG8_LDA(dst, b, h) do { if constexpr (DT != 1) { _Pragma("unroll") for (int m = 0; m < 4; ++m) _Pragma("unroll") for (int k = 0; k < 2; ++k) dst[m][k] = *(const PG8_LAS bf16x8*)(lds + PG8_SA(b, h) + aoff + m * 2048 + k * 1024); } \
;         else { _Pragma("unroll") for (int m = 0; m < 4; ++m) dst##8[m] = ld32(lds + PG8_SA(b, h) + aoff + m * 2048); } } while (0)
; #define PG8_LDB(dst, b, h) do { if constexpr (DT != 1) { _Pragma("unroll") for (int n = 0; n < 2; ++n) _Pragma("unroll") for (int k = 0; k < 2; ++k) dst[n][k] = *(const PG8_LAS bf16x8*)(lds + PG8_SB(b, h) + boff + n * 2048 + k * 1024); } \
;         else { _Pragma("unroll") for (int n = 0; n < 2; ++n) dst##8[n] = ld32(lds + PG8_SB(b, h) + boff + n * 2048); } } while (0)
; #define PG8_WAIT_V(n) asm volatile("s_waitcnt vmcnt(" #n ")" ::: "memory")
; #define PG8_WAIT_L(n) asm volatile("s_waitcnt lgkmcnt(" #n ")" ::: "memory")
; #define PG8_BAR __builtin_amdgcn_s_barrier()
; #define PG8_SCHED __builtin_amdgcn_sched_barrier(0)
;     ...
;             PG8_LDB(B0, 0, 0); PG8_LDB(B1, 0, 1); PG8_SCHED; PG8_LDA(At, 0, 0); PG8_STAGE(PG8_SA(1, 1), a1 + hstepA, voffA);
;             PG8_WAIT_V(8); PG8_WAIT_L(0); PG8_BAR; PG8_MMA(0, 0, At, B0); PG8_MMA(0, 1, At, B1); PG8_BAR; PG8_SCHED;
;             PG8_LDA(At, 0, 1); PG8_STAGE(PG8_SB(0, 0), b2, voffB); PG8_STAGE(PG8_SB(0, 1), b2 + hstepB, voffB); PG8_STAGE(PG8_SA(0, 0), a2, voffA);
;             PG8_WAIT_V(8); PG8_WAIT_L(0); PG8_BAR; PG8_MMA(1, 0, At, B0); PG8_MMA(1, 1, At, B1); PG8_BAR; PG8_SCHED;
.LBB0_4350:
	v_add_u32_e32 v164, s37, v170
	v_add_u32_e32 v168, s38, v170
	ds_read_b128 v[152:155], v164
	ds_read_b128 v[156:159], v164 offset:1024
	ds_read_b128 v[160:163], v164 offset:2048
	ds_read_b128 v[164:167], v164 offset:3072
	ds_read_b128 v[180:183], v168
	ds_read_b128 v[184:187], v168 offset:1024
	ds_read_b128 v[188:191], v168 offset:2048
	ds_read_b128 v[192:195], v168 offset:3072
	s_add_i32 s70, s28, 2
	s_add_u32 s29, s26, 0xfffc0080
	s_addc_u32 s30, s27, -1
	s_cmp_eq_u32 s64, s28
	s_cselect_b32 s28, s67, s68
	s_cselect_b32 s31, s17, s30
	s_cselect_b32 s30, s19, s29
	s_cselect_b32 s29, s66, s69
	s_add_i32 m0, s49, 0xc000
	ds_read_b128 v[196:199], v179
	ds_read_b128 v[200:203], v179 offset:1024
	ds_read_b128 v[204:207], v179 offset:2048
	ds_read_b128 v[208:211], v179 offset:3072
	ds_read_b128 v[212:215], v179 offset:4096
	ds_read_b128 v[216:219], v179 offset:5120
	ds_read_b128 v[220:223], v179 offset:6144
	ds_read_b128 v[224:227], v179 offset:7168
	global_load_lds_dwordx4 v146, s[26:27]
	s_add_i32 m0, s49, 0xe000
	s_nop 0
	global_load_lds_dwordx4 v144, s[26:27]
	s_waitcnt vmcnt(8)
	s_waitcnt lgkmcnt(0)
	s_barrier
	s_setprio 1
	s_waitcnt lgkmcnt(0)
	v_mfma_i32_16x16x64_i8 v[126:129], v[152:155], v[196:199], v[126:129]
	v_mfma_i32_16x16x64_i8 v[122:125], v[160:163], v[196:199], v[122:125]
	v_mfma_i32_16x16x64_i8 v[118:121], v[152:155], v[204:207], v[118:121]
	v_mfma_i32_16x16x64_i8 v[114:117], v[160:163], v[204:207], v[114:117]
	v_mfma_i32_16x16x64_i8 v[110:113], v[152:155], v[212:215], v[110:113]
	v_mfma_i32_16x16x64_i8 v[106:109], v[160:163], v[212:215], v[106:109]
	v_mfma_i32_16x16x64_i8 v[102:105], v[152:155], v[220:223], v[102:105]
	v_mfma_i32_16x16x64_i8 v[98:101], v[160:163], v[220:223], v[98:101]
	v_mfma_i32_16x16x64_i8 v[126:129], v[156:159], v[200:203], v[126:129]
	v_mfma_i32_16x16x64_i8 v[122:125], v[164:167], v[200:203], v[122:125]
	v_mfma_i32_16x16x64_i8 v[118:121], v[156:159], v[208:211], v[118:121]
	v_mfma_i32_16x16x64_i8 v[114:117], v[164:167], v[208:211], v[114:117]
	v_mfma_i32_16x16x64_i8 v[110:113], v[156:159], v[216:219], v[110:113]
	v_mfma_i32_16x16x64_i8 v[106:109], v[164:167], v[216:219], v[106:109]
	v_mfma_i32_16x16x64_i8 v[102:105], v[156:159], v[224:227], v[102:105]
	v_mfma_i32_16x16x64_i8 v[98:101], v[164:167], v[224:227], v[98:101]
	v_mfma_i32_16x16x64_i8 v[94:97], v[180:183], v[196:199], v[94:97]
	v_mfma_i32_16x16x64_i8 v[86:89], v[188:191], v[196:199], v[86:89]
	v_mfma_i32_16x16x64_i8 v[78:81], v[180:183], v[204:207], v[78:81]
	v_mfma_i32_16x16x64_i8 v[70:73], v[188:191], v[204:207], v[70:73]
	v_mfma_i32_16x16x64_i8 v[62:65], v[180:183], v[212:215], v[62:65]
	v_mfma_i32_16x16x64_i8 v[54:57], v[188:191], v[212:215], v[54:57]
	v_mfma_i32_16x16x64_i8 v[46:49], v[180:183], v[220:223], v[46:49]
	v_mfma_i32_16x16x64_i8 v[38:41], v[188:191], v[220:223], v[38:41]
	v_mfma_i32_16x16x64_i8 v[94:97], v[184:187], v[200:203], v[94:97]
	v_mfma_i32_16x16x64_i8 v[86:89], v[192:195], v[200:203], v[86:89]
	v_mfma_i32_16x16x64_i8 v[78:81], v[184:187], v[208:211], v[78:81]
	v_mfma_i32_16x16x64_i8 v[70:73], v[192:195], v[208:211], v[70:73]
	v_mfma_i32_16x16x64_i8 v[62:65], v[184:187], v[216:219], v[62:65]
	v_mfma_i32_16x16x64_i8 v[54:57], v[192:195], v[216:219], v[54:57]
	v_mfma_i32_16x16x64_i8 v[46:49], v[184:187], v[224:227], v[46:49]
	v_mfma_i32_16x16x64_i8 v[38:41], v[192:195], v[224:227], v[38:41]
	s_setprio 0
	s_barrier
	s_mov_b32 m0, s45
	s_add_u32 s98, s28, 0x80
	s_addc_u32 s99, s29, 0
	s_add_u32 s72, s28, 0x40000
	ds_read_b128 v[196:199], v179 offset:16384
	ds_read_b128 v[200:203], v179 offset:17408
	ds_read_b128 v[204:207], v179 offset:18432
	ds_read_b128 v[208:211], v179 offset:19456
	ds_read_b128 v[212:215], v179 offset:20480
	ds_read_b128 v[216:219], v179 offset:21504
	ds_read_b128 v[220:223], v179 offset:22528
	ds_read_b128 v[224:227], v179 offset:23552
	global_load_lds_dwordx4 v132, s[28:29]
	s_mov_b32 m0, s46
	s_addc_u32 s73, s29, 0
	global_load_lds_dwordx4 v136, s[28:29]
	s_mov_b32 m0, s47
	s_nop 0
	global_load_lds_dwordx4 v132, s[72:73]
	s_mov_b32 m0, s48
	s_nop 0
	global_load_lds_dwordx4 v136, s[72:73]
	s_add_u32 s100, s30, 0x80
	s_addc_u32 s101, s31, 0
	s_mov_b32 m0, s49
	s_nop 0
	global_load_lds_dwordx4 v130, s[30:31]
	s_mov_b32 m0, s50
	s_nop 0
	global_load_lds_dwordx4 v134, s[30:31]
	s_waitcnt vmcnt(8)
	s_waitcnt lgkmcnt(0)
	s_barrier
	s_setprio 1
	s_waitcnt lgkmcnt(0)
	v_mfma_i32_16x16x64_i8 v[90:93], v[152:155], v[196:199], v[90:93]
	v_mfma_i32_16x16x64_i8 v[82:85], v[160:163], v[196:199], v[82:85]
	v_mfma_i32_16x16x64_i8 v[74:77], v[152:155], v[204:207], v[74:77]
	v_mfma_i32_16x16x64_i8 v[66:69], v[160:163], v[204:207], v[66:69]
	v_mfma_i32_16x16x64_i8 v[58:61], v[152:155], v[212:215], v[58:61]
	v_mfma_i32_16x16x64_i8 v[50:53], v[160:163], v[212:215], v[50:53]
	v_mfma_i32_16x16x64_i8 v[42:45], v[152:155], v[220:223], v[42:45]
	v_mfma_i32_16x16x64_i8 v[34:37], v[160:163], v[220:223], v[34:37]
	v_mfma_i32_16x16x64_i8 v[90:93], v[156:159], v[200:203], v[90:93]
	v_mfma_i32_16x16x64_i8 v[82:85], v[164:167], v[200:203], v[82:85]
	v_mfma_i32_16x16x64_i8 v[74:77], v[156:159], v[208:211], v[74:77]
	v_mfma_i32_16x16x64_i8 v[66:69], v[164:167], v[208:211], v[66:69]
	v_mfma_i32_16x16x64_i8 v[58:61], v[156:159], v[216:219], v[58:61]
	v_mfma_i32_16x16x64_i8 v[50:53], v[164:167], v[216:219], v[50:53]
	v_mfma_i32_16x16x64_i8 v[42:45], v[156:159], v[224:227], v[42:45]
	v_mfma_i32_16x16x64_i8 v[34:37], v[164:167], v[224:227], v[34:37]
	v_mfma_i32_16x16x64_i8 v[30:33], v[180:183], v[196:199], v[30:33]
	v_mfma_i32_16x16x64_i8 v[26:29], v[188:191], v[196:199], v[26:29]
	v_mfma_i32_16x16x64_i8 v[22:25], v[180:183], v[204:207], v[22:25]
	v_mfma_i32_16x16x64_i8 v[18:21], v[188:191], v[204:207], v[18:21]
	v_mfma_i32_16x16x64_i8 v[14:17], v[180:183], v[212:215], v[14:17]
	v_mfma_i32_16x16x64_i8 v[10:13], v[188:191], v[212:215], v[10:13]
	v_mfma_i32_16x16x64_i8 v[6:9], v[180:183], v[220:223], v[6:9]
	v_mfma_i32_16x16x64_i8 v[2:5], v[188:191], v[220:223], v[2:5]
	v_mfma_i32_16x16x64_i8 v[30:33], v[184:187], v[200:203], v[30:33]
	v_mfma_i32_16x16x64_i8 v[26:29], v[192:195], v[200:203], v[26:29]
	v_mfma_i32_16x16x64_i8 v[22:25], v[184:187], v[208:211], v[22:25]
	v_mfma_i32_16x16x64_i8 v[18:21], v[192:195], v[208:211], v[18:21]
	v_mfma_i32_16x16x64_i8 v[14:17], v[184:187], v[216:219], v[14:17]
	v_mfma_i32_16x16x64_i8 v[10:13], v[192:195], v[216:219], v[10:13]
	v_mfma_i32_16x16x64_i8 v[6:9], v[184:187], v[224:227], v[6:9]
	v_mfma_i32_16x16x64_i8 v[2:5], v[192:195], v[224:227], v[2:5]
	s_setprio 0
	s_barrier
; #define PG8_STAGE(bufoff, gbase, voff) do { _Pragma("unroll") for (int _i = 0; _i < 2; ++_i) \
;         __builtin_amdgcn_global_load_lds((const unsigned*)((const char*)(gbase) + (voff)[_i]), (PG8_LAS unsigned*)(lds + (bufoff) + ldsw + _i * 8192), 16, 0, 0); } while (0)
; #define PG8_LDA(dst, b, h) do { if constexpr (DT != 1) { _Pragma("unroll") for (int m = 0; m < 4; ++m) _Pragma("unroll") for (int k = 0; k < 2; ++k) dst[m][k] = *(const PG8_LAS bf16x8*)(lds + PG8_SA(b, h) + aoff + m * 2048 + k * 1024); } \
;         else { _Pragma("unroll") for (int m = 0; m < 4; ++m) dst##8[m] = ld32(lds + PG8_SA(b, h) + aoff + m * 2048); } } while (0)
; #define PG8_LDB(dst, b, h) do { if constexpr (DT != 1) { _Pragma("unroll") for (int n = 0; n < 2; ++n) _Pragma("unroll") for (int k = 0; k < 2; ++k) dst[n][k] = *(const PG8_LAS bf16x8*)(lds + PG8_SB(b, h) + boff + n * 2048 + k * 1024); } \
;         else { _Pragma("unroll") for (int n = 0; n < 2; ++n) dst##8[n] = ld32(lds + PG8_SB(b, h) + boff + n * 2048); } } while (0)
; #define PG8_WAIT_V(n) asm volatile("s_waitcnt vmcnt(" #n ")" ::: "memory")
; #define PG8_WAIT_L(n) asm volatile("s_waitcnt lgkmcnt(" #n ")" ::: "memory")
; #define PG8_BAR __builtin_amdgcn_s_barrier()
; #define PG8_SCHED __builtin_amdgcn_sched_barrier(0)
;     ...
;             PG8_LDB(B0, 1, 0); PG8_LDB(B1, 1, 1); PG8_SCHED; PG8_LDA(At, 1, 0); PG8_STAGE(PG8_SA(0, 1), a2 + hstepA, voffA);
;             PG8_WAIT_V(8); PG8_WAIT_L(0); PG8_BAR; PG8_MMA(0, 0, At, B0); PG8_MMA(0, 1, At, B1); PG8_BAR; PG8_SCHED;
;             PG8_LDA(At, 1, 1); PG8_STAGE(PG8_SB(1, 0), b3, voffB); PG8_STAGE(PG8_SB(1, 1), b3 + hstepB, voffB); PG8_STAGE(PG8_SA(1, 0), a3, voffA);
	v_add_u32_e32 v164, s54, v170
	v_add_u32_e32 v192, s55, v170
	ds_read_b128 v[152:155], v164
	ds_read_b128 v[156:159], v164 offset:1024
	ds_read_b128 v[160:163], v164 offset:2048
	ds_read_b128 v[164:167], v164 offset:3072
	ds_read_b128 v[180:183], v192
	ds_read_b128 v[184:187], v192 offset:1024
	ds_read_b128 v[188:191], v192 offset:2048
	ds_read_b128 v[192:195], v192 offset:3072
	s_add_u32 s30, s30, 0x40000
	s_addc_u32 s31, s31, 0
	s_mov_b32 m0, s51
	ds_read_b128 v[196:199], v179 offset:32768
	ds_read_b128 v[200:203], v179 offset:33792
	ds_read_b128 v[204:207], v179 offset:34816
	ds_read_b128 v[208:211], v179 offset:35840
	ds_read_b128 v[212:215], v179 offset:36864
	ds_read_b128 v[216:219], v179 offset:37888
	ds_read_b128 v[220:223], v179 offset:38912
	ds_read_b128 v[224:227], v179 offset:39936
	global_load_lds_dwordx4 v130, s[30:31]
	s_mov_b32 m0, s52
	s_nop 0
	global_load_lds_dwordx4 v134, s[30:31]
	s_waitcnt vmcnt(8)
	s_waitcnt lgkmcnt(0)
	s_barrier
	s_setprio 1
	s_waitcnt lgkmcnt(0)
	v_mfma_i32_16x16x64_i8 v[126:129], v[152:155], v[196:199], v[126:129]
	v_mfma_i32_16x16x64_i8 v[122:125], v[160:163], v[196:199], v[122:125]
	v_mfma_i32_16x16x64_i8 v[118:121], v[152:155], v[204:207], v[118:121]
	v_mfma_i32_16x16x64_i8 v[114:117], v[160:163], v[204:207], v[114:117]
	v_mfma_i32_16x16x64_i8 v[110:113], v[152:155], v[212:215], v[110:113]
	v_mfma_i32_16x16x64_i8 v[106:109], v[160:163], v[212:215], v[106:109]
	v_mfma_i32_16x16x64_i8 v[102:105], v[152:155], v[220:223], v[102:105]
	v_mfma_i32_16x16x64_i8 v[98:101], v[160:163], v[220:223], v[98:101]
	v_mfma_i32_16x16x64_i8 v[126:129], v[156:159], v[200:203], v[126:129]
	v_mfma_i32_16x16x64_i8 v[122:125], v[164:167], v[200:203], v[122:125]
	v_mfma_i32_16x16x64_i8 v[118:121], v[156:159], v[208:211], v[118:121]
	v_mfma_i32_16x16x64_i8 v[114:117], v[164:167], v[208:211], v[114:117]
	v_mfma_i32_16x16x64_i8 v[110:113], v[156:159], v[216:219], v[110:113]
	v_mfma_i32_16x16x64_i8 v[106:109], v[164:167], v[216:219], v[106:109]
	v_mfma_i32_16x16x64_i8 v[102:105], v[156:159], v[224:227], v[102:105]
	v_mfma_i32_16x16x64_i8 v[98:101], v[164:167], v[224:227], v[98:101]
	v_mfma_i32_16x16x64_i8 v[94:97], v[180:183], v[196:199], v[94:97]
	v_mfma_i32_16x16x64_i8 v[86:89], v[188:191], v[196:199], v[86:89]
	v_mfma_i32_16x16x64_i8 v[78:81], v[180:183], v[204:207], v[78:81]
	v_mfma_i32_16x16x64_i8 v[70:73], v[188:191], v[204:207], v[70:73]
	v_mfma_i32_16x16x64_i8 v[62:65], v[180:183], v[212:215], v[62:65]
	v_mfma_i32_16x16x64_i8 v[54:57], v[188:191], v[212:215], v[54:57]
	v_mfma_i32_16x16x64_i8 v[46:49], v[180:183], v[220:223], v[46:49]
	v_mfma_i32_16x16x64_i8 v[38:41], v[188:191], v[220:223], v[38:41]
	v_mfma_i32_16x16x64_i8 v[94:97], v[184:187], v[200:203], v[94:97]
	v_mfma_i32_16x16x64_i8 v[86:89], v[192:195], v[200:203], v[86:89]
	v_mfma_i32_16x16x64_i8 v[78:81], v[184:187], v[208:211], v[78:81]
	v_mfma_i32_16x16x64_i8 v[70:73], v[192:195], v[208:211], v[70:73]
	v_mfma_i32_16x16x64_i8 v[62:65], v[184:187], v[216:219], v[62:65]
	v_mfma_i32_16x16x64_i8 v[54:57], v[192:195], v[216:219], v[54:57]
	v_mfma_i32_16x16x64_i8 v[46:49], v[184:187], v[224:227], v[46:49]
	v_mfma_i32_16x16x64_i8 v[38:41], v[192:195], v[224:227], v[38:41]
	s_setprio 0
	s_barrier
	s_mov_b32 m0, s58
	s_add_u32 s28, s28, 0x40080
	ds_read_b128 v[196:199], v179 offset:49152
	ds_read_b128 v[200:203], v179 offset:50176
	ds_read_b128 v[204:207], v179 offset:51200
	ds_read_b128 v[208:211], v179 offset:52224
	ds_read_b128 v[212:215], v179 offset:53248
	ds_read_b128 v[216:219], v179 offset:54272
	ds_read_b128 v[220:223], v179 offset:55296
	ds_read_b128 v[224:227], v179 offset:56320
	global_load_lds_dwordx4 v132, s[98:99]
	s_mov_b32 m0, s59
	s_addc_u32 s29, s29, 0
	global_load_lds_dwordx4 v136, s[98:99]
	s_mov_b32 m0, s62
	s_nop 0
	global_load_lds_dwordx4 v132, s[28:29]
	s_mov_b32 m0, s63
	s_nop 0
	global_load_lds_dwordx4 v136, s[28:29]
	s_mov_b32 m0, s60
	s_nop 0
	global_load_lds_dwordx4 v130, s[100:101]
	s_mov_b32 m0, s61
	s_nop 0
	global_load_lds_dwordx4 v134, s[100:101]
	s_waitcnt vmcnt(8)
	s_waitcnt lgkmcnt(0)
	s_barrier
; #define PG8_STAGE(bufoff, gbase, voff) do { _Pragma("unroll") for (int _i = 0; _i < 2; ++_i) \
;         __builtin_amdgcn_global_load_lds((const unsigned*)((const char*)(gbase) + (voff)[_i]), (PG8_LAS unsigned*)(lds + (bufoff) + ldsw + _i * 8192), 16, 0, 0); } while (0)
; #define PG8_LDA(dst, b, h) do { if constexpr (DT != 1) { _Pragma("unroll") for (int m = 0; m < 4; ++m) _Pragma("unroll") for (int k = 0; k < 2; ++k) dst[m][k] = *(const PG8_LAS bf16x8*)(lds + PG8_SA(b, h) + aoff + m * 2048 + k * 1024); } \
;         else { _Pragma("unroll") for (int m = 0; m < 4; ++m) dst##8[m] = ld32(lds + PG8_SA(b, h) + aoff + m * 2048); } } while (0)
; #define PG8_LDB(dst, b, h) do { if constexpr (DT != 1) { _Pragma("unroll") for (int n = 0; n < 2; ++n) _Pragma("unroll") for (int k = 0; k < 2; ++k) dst[n][k] = *(const PG8_LAS bf16x8*)(lds + PG8_SB(b, h) + boff + n * 2048 + k * 1024); } \
;         else { _Pragma("unroll") for (int n = 0; n < 2; ++n) dst##8[n] = ld32(lds + PG8_SB(b, h) + boff + n * 2048); } } while (0)
; #define PG8_WAIT_V(n) asm volatile("s_waitcnt vmcnt(" #n ")" ::: "memory")
; #define PG8_WAIT_L(n) asm volatile("s_waitcnt lgkmcnt(" #n ")" ::: "memory")
; #define PG8_BAR __builtin_amdgcn_s_barrier()
; #define PG8_SCHED __builtin_amdgcn_sched_barrier(0)
; __device__ __forceinline__ f32x4 i32bits_to_f32(f32x4 v) { return (f32x4){(float)__float_as_int(v.x), (float)__float_as_int(v.y), (float)__float_as_int(v.z), (float)__float_as_int(v.w)}; }
;     ...
;             PG8_WAIT_V(8); PG8_WAIT_L(0); PG8_BAR; PG8_MMA(1, 0, At, B0); PG8_MMA(1, 1, At, B1); PG8_BAR; PG8_SCHED;
;             PG8_LDB(B0, 1, 0); PG8_LDB(B1, 1, 1); PG8_SCHED; PG8_LDA(At, 1, 0); PG8_STAGE(PG8_SA(0, 1), a2 + hstepA, voffA);
;             PG8_WAIT_V(8); PG8_WAIT_L(0); PG8_BAR; PG8_MMA(0, 0, At, B0); PG8_MMA(0, 1, At, B1); PG8_BAR; PG8_SCHED;
;             PG8_LDA(At, 1, 1); PG8_STAGE(PG8_SB(1, 0), b3, voffB); PG8_STAGE(PG8_SB(1, 1), b3 + hstepB, voffB); PG8_STAGE(PG8_SA(1, 0), a3, voffA);
;             PG8_WAIT_V(8); PG8_WAIT_L(0); PG8_BAR; PG8_MMA(1, 0, At, B0); PG8_MMA(1, 1, At, B1); PG8_BAR; PG8_SCHED;
	s_setprio 1
	s_waitcnt lgkmcnt(0)
	v_mfma_i32_16x16x64_i8 v[90:93], v[152:155], v[196:199], v[90:93]
	v_mfma_i32_16x16x64_i8 v[82:85], v[160:163], v[196:199], v[82:85]
	v_mfma_i32_16x16x64_i8 v[74:77], v[152:155], v[204:207], v[74:77]
	v_mfma_i32_16x16x64_i8 v[66:69], v[160:163], v[204:207], v[66:69]
	v_mfma_i32_16x16x64_i8 v[58:61], v[152:155], v[212:215], v[58:61]
	v_mfma_i32_16x16x64_i8 v[50:53], v[160:163], v[212:215], v[50:53]
	v_mfma_i32_16x16x64_i8 v[42:45], v[152:155], v[220:223], v[42:45]
	v_mfma_i32_16x16x64_i8 v[34:37], v[160:163], v[220:223], v[34:37]
	v_mfma_i32_16x16x64_i8 v[90:93], v[156:159], v[200:203], v[90:93]
	v_mfma_i32_16x16x64_i8 v[82:85], v[164:167], v[200:203], v[82:85]
	v_mfma_i32_16x16x64_i8 v[74:77], v[156:159], v[208:211], v[74:77]
	v_mfma_i32_16x16x64_i8 v[66:69], v[164:167], v[208:211], v[66:69]
	v_mfma_i32_16x16x64_i8 v[58:61], v[156:159], v[216:219], v[58:61]
	v_mfma_i32_16x16x64_i8 v[50:53], v[164:167], v[216:219], v[50:53]
	v_mfma_i32_16x16x64_i8 v[42:45], v[156:159], v[224:227], v[42:45]
	v_mfma_i32_16x16x64_i8 v[34:37], v[164:167], v[224:227], v[34:37]
	v_mfma_i32_16x16x64_i8 v[30:33], v[180:183], v[196:199], v[30:33]
	v_mfma_i32_16x16x64_i8 v[26:29], v[188:191], v[196:199], v[26:29]
	v_mfma_i32_16x16x64_i8 v[22:25], v[180:183], v[204:207], v[22:25]
	v_mfma_i32_16x16x64_i8 v[18:21], v[188:191], v[204:207], v[18:21]
	v_mfma_i32_16x16x64_i8 v[14:17], v[180:183], v[212:215], v[14:17]
	v_mfma_i32_16x16x64_i8 v[10:13], v[188:191], v[212:215], v[10:13]
	v_mfma_i32_16x16x64_i8 v[6:9], v[180:183], v[220:223], v[6:9]
	v_mfma_i32_16x16x64_i8 v[2:5], v[188:191], v[220:223], v[2:5]
	v_mfma_i32_16x16x64_i8 v[30:33], v[184:187], v[200:203], v[30:33]
	v_mfma_i32_16x16x64_i8 v[26:29], v[192:195], v[200:203], v[26:29]
	v_mfma_i32_16x16x64_i8 v[22:25], v[184:187], v[208:211], v[22:25]
	v_mfma_i32_16x16x64_i8 v[18:21], v[192:195], v[208:211], v[18:21]
	v_mfma_i32_16x16x64_i8 v[14:17], v[184:187], v[216:219], v[14:17]
	v_mfma_i32_16x16x64_i8 v[10:13], v[192:195], v[216:219], v[10:13]
	v_mfma_i32_16x16x64_i8 v[6:9], v[184:187], v[224:227], v[6:9]
	v_mfma_i32_16x16x64_i8 v[2:5], v[192:195], v[224:227], v[2:5]
	s_setprio 0
	s_barrier
	s_add_u32 s68, s68, 0x100
	s_addc_u32 s69, s69, 0
	s_add_u32 s26, s26, 0x100
	s_addc_u32 s27, s27, 0
	s_cmp_ge_i32 s70, s57
	s_mov_b32 s28, s70
	s_cbranch_scc0 .LBB0_4350
	v_cvt_f32_i32_e32 v166, v126
	v_cvt_f32_i32_e32 v167, v127
	v_cvt_f32_i32_e32 v160, v128
	v_cvt_f32_i32_e32 v161, v129
	v_cvt_f32_i32_e32 v162, v122
	v_cvt_f32_i32_e32 v163, v123
	v_cvt_f32_i32_e32 v164, v124
	v_cvt_f32_i32_e32 v165, v125
	v_cvt_f32_i32_e32 v152, v118
	v_cvt_f32_i32_e32 v153, v119
	v_cvt_f32_i32_e32 v154, v120
	v_cvt_f32_i32_e32 v155, v121
	v_cvt_f32_i32_e32 v156, v114
	v_cvt_f32_i32_e32 v157, v115
	v_cvt_f32_i32_e32 v158, v116
	v_cvt_f32_i32_e32 v159, v117
	v_cvt_f32_i32_e32 v110, v110
	v_cvt_f32_i32_e32 v111, v111
	v_cvt_f32_i32_e32 v112, v112
	v_cvt_f32_i32_e32 v113, v113
	v_cvt_f32_i32_e32 v106, v106
	v_cvt_f32_i32_e32 v107, v107
	v_cvt_f32_i32_e32 v108, v108
	v_cvt_f32_i32_e32 v109, v109
	v_cvt_f32_i32_e32 v102, v102
	v_cvt_f32_i32_e32 v103, v103
	v_cvt_f32_i32_e32 v104, v104
	v_cvt_f32_i32_e32 v105, v105
	v_cvt_f32_i32_e32 v98, v98
	v_cvt_f32_i32_e32 v99, v99
	v_cvt_f32_i32_e32 v100, v100
	v_cvt_f32_i32_e32 v101, v101
	v_cvt_f32_i32_e32 v90, v90
	v_cvt_f32_i32_e32 v91, v91
	v_cvt_f32_i32_e32 v92, v92
	v_cvt_f32_i32_e32 v93, v93
	v_cvt_f32_i32_e32 v82, v82
	v_cvt_f32_i32_e32 v83, v83
	v_cvt_f32_i32_e32 v84, v84
	v_cvt_f32_i32_e32 v85, v85
	v_cvt_f32_i32_e32 v74, v74
	v_cvt_f32_i32_e32 v75, v75
	v_cvt_f32_i32_e32 v76, v76
	v_cvt_f32_i32_e32 v77, v77
	v_cvt_f32_i32_e32 v66, v66
	v_cvt_f32_i32_e32 v67, v67
	v_cvt_f32_i32_e32 v68, v68
	v_cvt_f32_i32_e32 v69, v69
	v_cvt_f32_i32_e32 v58, v58
	v_cvt_f32_i32_e32 v59, v59
	v_cvt_f32_i32_e32 v60, v60
	v_cvt_f32_i32_e32 v61, v61
	v_cvt_f32_i32_e32 v50, v50
	v_cvt_f32_i32_e32 v51, v51
	v_cvt_f32_i32_e32 v52, v52
	v_cvt_f32_i32_e32 v53, v53
	v_cvt_f32_i32_e32 v42, v42
	v_cvt_f32_i32_e32 v43, v43
	v_cvt_f32_i32_e32 v44, v44
	v_cvt_f32_i32_e32 v45, v45
	v_cvt_f32_i32_e32 v34, v34
	v_cvt_f32_i32_e32 v35, v35
	v_cvt_f32_i32_e32 v36, v36
	v_cvt_f32_i32_e32 v37, v37
	v_cvt_f32_i32_e32 v114, v94
	v_cvt_f32_i32_e32 v115, v95
	v_cvt_f32_i32_e32 v116, v96
	v_cvt_f32_i32_e32 v117, v97
	v_cvt_f32_i32_e32 v118, v86
	v_cvt_f32_i32_e32 v119, v87
	v_cvt_f32_i32_e32 v120, v88
	v_cvt_f32_i32_e32 v121, v89
	v_cvt_f32_i32_e32 v122, v78
	v_cvt_f32_i32_e32 v123, v79
	v_cvt_f32_i32_e32 v124, v80
	v_cvt_f32_i32_e32 v125, v81
	v_cvt_f32_i32_e32 v126, v70
	v_cvt_f32_i32_e32 v127, v71
	v_cvt_f32_i32_e32 v128, v72
	v_cvt_f32_i32_e32 v129, v73
	v_cvt_f32_i32_e32 v88, v62
	v_cvt_f32_i32_e32 v89, v63
	v_cvt_f32_i32_e32 v96, v64
	v_cvt_f32_i32_e32 v97, v65
	v_cvt_f32_i32_e32 v86, v54
	v_cvt_f32_i32_e32 v87, v55
	v_cvt_f32_i32_e32 v94, v56
	v_cvt_f32_i32_e32 v95, v57
	v_cvt_f32_i32_e32 v72, v46
	v_cvt_f32_i32_e32 v73, v47
	v_cvt_f32_i32_e32 v80, v48
	v_cvt_f32_i32_e32 v81, v49
	v_cvt_f32_i32_e32 v70, v38
	v_cvt_f32_i32_e32 v71, v39
	v_cvt_f32_i32_e32 v78, v40
	v_cvt_f32_i32_e32 v79, v41
	v_cvt_f32_i32_e32 v56, v30
	v_cvt_f32_i32_e32 v57, v31
	v_cvt_f32_i32_e32 v64, v32
	v_cvt_f32_i32_e32 v65, v33
	v_cvt_f32_i32_e32 v54, v26
	v_cvt_f32_i32_e32 v55, v27
	v_cvt_f32_i32_e32 v62, v28
	v_cvt_f32_i32_e32 v63, v29
	v_cvt_f32_i32_e32 v40, v22
	v_cvt_f32_i32_e32 v41, v23
	v_cvt_f32_i32_e32 v48, v24
	v_cvt_f32_i32_e32 v49, v25
	v_cvt_f32_i32_e32 v38, v18
	v_cvt_f32_i32_e32 v39, v19
	v_cvt_f32_i32_e32 v46, v20
	v_cvt_f32_i32_e32 v47, v21
	v_cvt_f32_i32_e32 v28, v14
	v_cvt_f32_i32_e32 v29, v15
	v_cvt_f32_i32_e32 v32, v16
	v_cvt_f32_i32_e32 v33, v17
	v_cvt_f32_i32_e32 v26, v10
	v_cvt_f32_i32_e32 v27, v11
	v_cvt_f32_i32_e32 v30, v12
	v_cvt_f32_i32_e32 v31, v13
	v_cvt_f32_i32_e32 v20, v6
	v_cvt_f32_i32_e32 v21, v7
	v_cvt_f32_i32_e32 v24, v8
	v_cvt_f32_i32_e32 v25, v9
	v_cvt_f32_i32_e32 v18, v2
	v_cvt_f32_i32_e32 v19, v3
	v_cvt_f32_i32_e32 v22, v4
	v_cvt_f32_i32_e32 v23, v5

; #define PG8_STAGE(bufoff, gbase, voff) do { _Pragma("unroll") for (int _i = 0; _i < 2; ++_i) \
;         __builtin_amdgcn_global_load_lds((const unsigned*)((const char*)(gbase) + (voff)[_i]), (PG8_LAS unsigned*)(lds + (bufoff) + ldsw + _i * 8192), 16, 0, 0); } while (0)
; #define PG8_LDA(dst, b, h) do { if constexpr (DT != 1) { _Pragma("unroll") for (int m = 0; m < 4; ++m) _Pragma("unroll") for (int k = 0; k < 2; ++k) dst[m][k] = *(const PG8_LAS bf16x8*)(lds + PG8_SA(b, h) + aoff + m * 2048 + k * 1024); } \
;         else { _Pragma("unroll") for (int m = 0; m < 4; ++m) dst##8[m] = ld32(lds + PG8_SA(b, h) + aoff + m * 2048); } } while (0)
; #define PG8_LDB(dst, b, h) do { if constexpr (DT != 1) { _Pragma("unroll") for (int n = 0; n < 2; ++n) _Pragma("unroll") for (int k = 0; k < 2; ++k) dst[n][k] = *(const PG8_LAS bf16x8*)(lds + PG8_SB(b, h) + boff + n * 2048 + k * 1024); } \
;         else { _Pragma("unroll") for (int n = 0; n < 2; ++n) dst##8[n] = ld32(lds + PG8_SB(b, h) + boff + n * 2048); } } while (0)
; #define PG8_WAIT_V(n) asm volatile("s_waitcnt vmcnt(" #n ")" ::: "memory")
; #define PG8_WAIT_L(n) asm volatile("s_waitcnt lgkmcnt(" #n ")" ::: "memory")
; #define PG8_BAR __builtin_amdgcn_s_barrier()
; #define PG8_SCHED __builtin_amdgcn_sched_barrier(0)
;     ...
;             PG8_LDB(B0, 0, 0); PG8_LDB(B1, 0, 1); PG8_SCHED; PG8_LDA(At, 0, 0); PG8_STAGE(PG8_SA(1, 1), a1 + hstepA, voffA);
;             PG8_WAIT_V(8); PG8_WAIT_L(0); PG8_BAR; PG8_MMA(0, 0, At, B0); PG8_MMA(0, 1, At, B1); PG8_BAR; PG8_SCHED;
;             PG8_LDA(At, 0, 1); PG8_STAGE(PG8_SB(0, 0), b2, voffB); PG8_STAGE(PG8_SB(0, 1), b2 + hstepB, voffB); PG8_STAGE(PG8_SA(0, 0), a2, voffA);
;             PG8_WAIT_V(8); PG8_WAIT_L(0); PG8_BAR; PG8_MMA(1, 0, At, B0); PG8_MMA(1, 1, At, B1); PG8_BAR; PG8_SCHED;
.LBB0_4646:
	ds_read_b128 v[146:149], v157
	ds_read_b128 v[150:153], v157 offset:1024
	ds_read_b128 v[162:165], v157 offset:2048
	ds_read_b128 v[166:169], v157 offset:3072
	ds_read_b128 v[170:173], v158
	ds_read_b128 v[174:177], v158 offset:1024
	ds_read_b128 v[178:181], v158 offset:2048
	ds_read_b128 v[182:185], v158 offset:3072
	s_add_i32 s71, s38, 2
	s_add_u32 s39, s36, 0xfff80080
	s_addc_u32 s40, s37, -1
	s_cmp_eq_u32 s63, s38
	s_cselect_b32 s38, s68, s69
	s_cselect_b32 s41, s25, s40
	s_cselect_b32 s40, s27, s39
	s_cselect_b32 s39, s67, s70
	s_add_i32 m0, s51, 0xc000
	ds_read_b128 v[186:189], v159
	ds_read_b128 v[190:193], v159 offset:1024
	ds_read_b128 v[194:197], v159 offset:2048
	ds_read_b128 v[198:201], v159 offset:3072
	ds_read_b128 v[202:205], v159 offset:4096
	ds_read_b128 v[206:209], v159 offset:5120
	ds_read_b128 v[210:213], v159 offset:6144
	ds_read_b128 v[214:217], v159 offset:7168
	global_load_lds_dwordx4 v140, s[36:37]
	s_add_i32 m0, s51, 0xe000
	s_nop 0
	global_load_lds_dwordx4 v138, s[36:37]
	s_waitcnt vmcnt(8)
	s_waitcnt lgkmcnt(0)
	s_barrier
	s_setprio 1
	s_waitcnt lgkmcnt(0)
	v_mfma_f32_16x16x32_bf16 v[122:125], v[146:149], v[186:189], v[122:125]
	v_mfma_f32_16x16x32_bf16 v[126:129], v[162:165], v[186:189], v[126:129]
	v_mfma_f32_16x16x32_bf16 v[110:113], v[146:149], v[194:197], v[110:113]
	v_mfma_f32_16x16x32_bf16 v[106:109], v[162:165], v[194:197], v[106:109]
	v_mfma_f32_16x16x32_bf16 v[94:97], v[146:149], v[202:205], v[94:97]
	v_mfma_f32_16x16x32_bf16 v[90:93], v[162:165], v[202:205], v[90:93]
	v_mfma_f32_16x16x32_bf16 v[78:81], v[146:149], v[210:213], v[78:81]
	v_mfma_f32_16x16x32_bf16 v[74:77], v[162:165], v[210:213], v[74:77]
	v_mfma_f32_16x16x32_bf16 v[122:125], v[150:153], v[190:193], v[122:125]
	v_mfma_f32_16x16x32_bf16 v[126:129], v[166:169], v[190:193], v[126:129]
	v_mfma_f32_16x16x32_bf16 v[110:113], v[150:153], v[198:201], v[110:113]
	v_mfma_f32_16x16x32_bf16 v[106:109], v[166:169], v[198:201], v[106:109]
	v_mfma_f32_16x16x32_bf16 v[94:97], v[150:153], v[206:209], v[94:97]
	v_mfma_f32_16x16x32_bf16 v[90:93], v[166:169], v[206:209], v[90:93]
	v_mfma_f32_16x16x32_bf16 v[78:81], v[150:153], v[214:217], v[78:81]
	v_mfma_f32_16x16x32_bf16 v[74:77], v[166:169], v[214:217], v[74:77]
	v_mfma_f32_16x16x32_bf16 v[118:121], v[170:173], v[186:189], v[118:121]
	v_mfma_f32_16x16x32_bf16 v[114:117], v[178:181], v[186:189], v[114:117]
	v_mfma_f32_16x16x32_bf16 v[102:105], v[170:173], v[194:197], v[102:105]
	v_mfma_f32_16x16x32_bf16 v[98:101], v[178:181], v[194:197], v[98:101]
	v_mfma_f32_16x16x32_bf16 v[86:89], v[170:173], v[202:205], v[86:89]
	v_mfma_f32_16x16x32_bf16 v[82:85], v[178:181], v[202:205], v[82:85]
	v_mfma_f32_16x16x32_bf16 v[70:73], v[170:173], v[210:213], v[70:73]
	v_mfma_f32_16x16x32_bf16 v[66:69], v[178:181], v[210:213], v[66:69]
	v_mfma_f32_16x16x32_bf16 v[118:121], v[174:177], v[190:193], v[118:121]
	v_mfma_f32_16x16x32_bf16 v[114:117], v[182:185], v[190:193], v[114:117]
	v_mfma_f32_16x16x32_bf16 v[102:105], v[174:177], v[198:201], v[102:105]
	v_mfma_f32_16x16x32_bf16 v[98:101], v[182:185], v[198:201], v[98:101]
	v_mfma_f32_16x16x32_bf16 v[86:89], v[174:177], v[206:209], v[86:89]
	v_mfma_f32_16x16x32_bf16 v[82:85], v[182:185], v[206:209], v[82:85]
	v_mfma_f32_16x16x32_bf16 v[70:73], v[174:177], v[214:217], v[70:73]
	v_mfma_f32_16x16x32_bf16 v[66:69], v[182:185], v[214:217], v[66:69]
	s_setprio 0
	s_barrier
	s_mov_b32 m0, s35
	s_add_u32 s98, s38, 0x80
	s_addc_u32 s99, s39, 0
	s_add_u32 s72, s38, 0x80000
	ds_read_b128 v[186:189], v159 offset:16384
	ds_read_b128 v[190:193], v159 offset:17408
	ds_read_b128 v[194:197], v159 offset:18432
	ds_read_b128 v[198:201], v159 offset:19456
	ds_read_b128 v[202:205], v159 offset:20480
	ds_read_b128 v[206:209], v159 offset:21504
	ds_read_b128 v[210:213], v159 offset:22528
	ds_read_b128 v[214:217], v159 offset:23552
	global_load_lds_dwordx4 v132, s[38:39]
	s_mov_b32 m0, s48
	s_addc_u32 s73, s39, 0
	global_load_lds_dwordx4 v136, s[38:39]
	s_mov_b32 m0, s49
	s_nop 0
	global_load_lds_dwordx4 v132, s[72:73]
	s_mov_b32 m0, s50
	s_nop 0
	global_load_lds_dwordx4 v136, s[72:73]
	s_add_u32 s100, s40, 0x80
	s_addc_u32 s101, s41, 0
	s_mov_b32 m0, s51
	s_nop 0
	global_load_lds_dwordx4 v130, s[40:41]
	s_mov_b32 m0, s52
	s_nop 0
	global_load_lds_dwordx4 v134, s[40:41]
	s_waitcnt vmcnt(8)
	s_waitcnt lgkmcnt(0)
	s_barrier
	s_setprio 1
	s_waitcnt lgkmcnt(0)
	v_mfma_f32_16x16x32_bf16 v[62:65], v[146:149], v[186:189], v[62:65]
	v_mfma_f32_16x16x32_bf16 v[58:61], v[162:165], v[186:189], v[58:61]
	v_mfma_f32_16x16x32_bf16 v[46:49], v[146:149], v[194:197], v[46:49]
	v_mfma_f32_16x16x32_bf16 v[42:45], v[162:165], v[194:197], v[42:45]
	v_mfma_f32_16x16x32_bf16 v[30:33], v[146:149], v[202:205], v[30:33]
	v_mfma_f32_16x16x32_bf16 v[26:29], v[162:165], v[202:205], v[26:29]
	v_mfma_f32_16x16x32_bf16 v[14:17], v[146:149], v[210:213], v[14:17]
	v_mfma_f32_16x16x32_bf16 v[10:13], v[162:165], v[210:213], v[10:13]
	v_mfma_f32_16x16x32_bf16 v[62:65], v[150:153], v[190:193], v[62:65]
	v_mfma_f32_16x16x32_bf16 v[58:61], v[166:169], v[190:193], v[58:61]
	v_mfma_f32_16x16x32_bf16 v[46:49], v[150:153], v[198:201], v[46:49]
	v_mfma_f32_16x16x32_bf16 v[42:45], v[166:169], v[198:201], v[42:45]
	v_mfma_f32_16x16x32_bf16 v[30:33], v[150:153], v[206:209], v[30:33]
	v_mfma_f32_16x16x32_bf16 v[26:29], v[166:169], v[206:209], v[26:29]
	v_mfma_f32_16x16x32_bf16 v[14:17], v[150:153], v[214:217], v[14:17]
	v_mfma_f32_16x16x32_bf16 v[10:13], v[166:169], v[214:217], v[10:13]
	v_mfma_f32_16x16x32_bf16 v[54:57], v[170:173], v[186:189], v[54:57]
	v_mfma_f32_16x16x32_bf16 v[50:53], v[178:181], v[186:189], v[50:53]
	v_mfma_f32_16x16x32_bf16 v[38:41], v[170:173], v[194:197], v[38:41]
	v_mfma_f32_16x16x32_bf16 v[34:37], v[178:181], v[194:197], v[34:37]
	v_mfma_f32_16x16x32_bf16 v[22:25], v[170:173], v[202:205], v[22:25]
	v_mfma_f32_16x16x32_bf16 v[18:21], v[178:181], v[202:205], v[18:21]
	v_mfma_f32_16x16x32_bf16 v[6:9], v[170:173], v[210:213], v[6:9]
	v_mfma_f32_16x16x32_bf16 v[2:5], v[178:181], v[210:213], v[2:5]
	v_mfma_f32_16x16x32_bf16 v[54:57], v[174:177], v[190:193], v[54:57]
	v_mfma_f32_16x16x32_bf16 v[50:53], v[182:185], v[190:193], v[50:53]
	v_mfma_f32_16x16x32_bf16 v[38:41], v[174:177], v[198:201], v[38:41]
	v_mfma_f32_16x16x32_bf16 v[34:37], v[182:185], v[198:201], v[34:37]
	v_mfma_f32_16x16x32_bf16 v[22:25], v[174:177], v[206:209], v[22:25]
	v_mfma_f32_16x16x32_bf16 v[18:21], v[182:185], v[206:209], v[18:21]
	v_mfma_f32_16x16x32_bf16 v[6:9], v[174:177], v[214:217], v[6:9]
	v_mfma_f32_16x16x32_bf16 v[2:5], v[182:185], v[214:217], v[2:5]
	s_setprio 0
	s_barrier
; #define PG8_STAGE(bufoff, gbase, voff) do { _Pragma("unroll") for (int _i = 0; _i < 2; ++_i) \
;         __builtin_amdgcn_global_load_lds((const unsigned*)((const char*)(gbase) + (voff)[_i]), (PG8_LAS unsigned*)(lds + (bufoff) + ldsw + _i * 8192), 16, 0, 0); } while (0)
; #define PG8_LDA(dst, b, h) do { if constexpr (DT != 1) { _Pragma("unroll") for (int m = 0; m < 4; ++m) _Pragma("unroll") for (int k = 0; k < 2; ++k) dst[m][k] = *(const PG8_LAS bf16x8*)(lds + PG8_SA(b, h) + aoff + m * 2048 + k * 1024); } \
;         else { _Pragma("unroll") for (int m = 0; m < 4; ++m) dst##8[m] = ld32(lds + PG8_SA(b, h) + aoff + m * 2048); } } while (0)
; #define PG8_LDB(dst, b, h) do { if constexpr (DT != 1) { _Pragma("unroll") for (int n = 0; n < 2; ++n) _Pragma("unroll") for (int k = 0; k < 2; ++k) dst[n][k] = *(const PG8_LAS bf16x8*)(lds + PG8_SB(b, h) + boff + n * 2048 + k * 1024); } \
;         else { _Pragma("unroll") for (int n = 0; n < 2; ++n) dst##8[n] = ld32(lds + PG8_SB(b, h) + boff + n * 2048); } } while (0)
; #define PG8_WAIT_V(n) asm volatile("s_waitcnt vmcnt(" #n ")" ::: "memory")
; #define PG8_WAIT_L(n) asm volatile("s_waitcnt lgkmcnt(" #n ")" ::: "memory")
; #define PG8_BAR __builtin_amdgcn_s_barrier()
; #define PG8_SCHED __builtin_amdgcn_sched_barrier(0)
;     ...
;             PG8_LDB(B0, 1, 0); PG8_LDB(B1, 1, 1); PG8_SCHED; PG8_LDA(At, 1, 0); PG8_STAGE(PG8_SA(0, 1), a2 + hstepA, voffA);
;             PG8_WAIT_V(8); PG8_WAIT_L(0); PG8_BAR; PG8_MMA(0, 0, At, B0); PG8_MMA(0, 1, At, B1); PG8_BAR; PG8_SCHED;
;             PG8_LDA(At, 1, 1); PG8_STAGE(PG8_SB(1, 0), b3, voffB); PG8_STAGE(PG8_SB(1, 1), b3 + hstepB, voffB); PG8_STAGE(PG8_SA(1, 0), a3, voffA);
;             PG8_WAIT_V(8); PG8_WAIT_L(0); PG8_BAR; PG8_MMA(1, 0, At, B0); PG8_MMA(1, 1, At, B1); PG8_BAR; PG8_SCHED;
	ds_read_b128 v[146:149], v160
	ds_read_b128 v[150:153], v160 offset:1024
	ds_read_b128 v[162:165], v160 offset:2048
	ds_read_b128 v[166:169], v160 offset:3072
	ds_read_b128 v[170:173], v161
	ds_read_b128 v[174:177], v161 offset:1024
	ds_read_b128 v[178:181], v161 offset:2048
	ds_read_b128 v[182:185], v161 offset:3072
	s_add_u32 s40, s40, 0x80000
	s_addc_u32 s41, s41, 0
	s_mov_b32 m0, s53
	ds_read_b128 v[186:189], v159 offset:32768
	ds_read_b128 v[190:193], v159 offset:33792
	ds_read_b128 v[194:197], v159 offset:34816
	ds_read_b128 v[198:201], v159 offset:35840
	ds_read_b128 v[202:205], v159 offset:36864
	ds_read_b128 v[206:209], v159 offset:37888
	ds_read_b128 v[210:213], v159 offset:38912
	ds_read_b128 v[214:217], v159 offset:39936
	global_load_lds_dwordx4 v130, s[40:41]
	s_mov_b32 m0, s54
	s_nop 0
	global_load_lds_dwordx4 v134, s[40:41]
	s_waitcnt vmcnt(8)
	s_waitcnt lgkmcnt(0)
	s_barrier
	s_setprio 1
	s_waitcnt lgkmcnt(0)
	v_mfma_f32_16x16x32_bf16 v[122:125], v[146:149], v[186:189], v[122:125]
	v_mfma_f32_16x16x32_bf16 v[126:129], v[162:165], v[186:189], v[126:129]
	v_mfma_f32_16x16x32_bf16 v[110:113], v[146:149], v[194:197], v[110:113]
	v_mfma_f32_16x16x32_bf16 v[106:109], v[162:165], v[194:197], v[106:109]
	v_mfma_f32_16x16x32_bf16 v[94:97], v[146:149], v[202:205], v[94:97]
	v_mfma_f32_16x16x32_bf16 v[90:93], v[162:165], v[202:205], v[90:93]
	v_mfma_f32_16x16x32_bf16 v[78:81], v[146:149], v[210:213], v[78:81]
	v_mfma_f32_16x16x32_bf16 v[74:77], v[162:165], v[210:213], v[74:77]
	v_mfma_f32_16x16x32_bf16 v[122:125], v[150:153], v[190:193], v[122:125]
	v_mfma_f32_16x16x32_bf16 v[126:129], v[166:169], v[190:193], v[126:129]
	v_mfma_f32_16x16x32_bf16 v[110:113], v[150:153], v[198:201], v[110:113]
	v_mfma_f32_16x16x32_bf16 v[106:109], v[166:169], v[198:201], v[106:109]
	v_mfma_f32_16x16x32_bf16 v[94:97], v[150:153], v[206:209], v[94:97]
	v_mfma_f32_16x16x32_bf16 v[90:93], v[166:169], v[206:209], v[90:93]
	v_mfma_f32_16x16x32_bf16 v[78:81], v[150:153], v[214:217], v[78:81]
	v_mfma_f32_16x16x32_bf16 v[74:77], v[166:169], v[214:217], v[74:77]
	v_mfma_f32_16x16x32_bf16 v[118:121], v[170:173], v[186:189], v[118:121]
	v_mfma_f32_16x16x32_bf16 v[114:117], v[178:181], v[186:189], v[114:117]
	v_mfma_f32_16x16x32_bf16 v[102:105], v[170:173], v[194:197], v[102:105]
	v_mfma_f32_16x16x32_bf16 v[98:101], v[178:181], v[194:197], v[98:101]
	v_mfma_f32_16x16x32_bf16 v[86:89], v[170:173], v[202:205], v[86:89]
	v_mfma_f32_16x16x32_bf16 v[82:85], v[178:181], v[202:205], v[82:85]
	v_mfma_f32_16x16x32_bf16 v[70:73], v[170:173], v[210:213], v[70:73]
	v_mfma_f32_16x16x32_bf16 v[66:69], v[178:181], v[210:213], v[66:69]
	v_mfma_f32_16x16x32_bf16 v[118:121], v[174:177], v[190:193], v[118:121]
	v_mfma_f32_16x16x32_bf16 v[114:117], v[182:185], v[190:193], v[114:117]
	v_mfma_f32_16x16x32_bf16 v[102:105], v[174:177], v[198:201], v[102:105]
	v_mfma_f32_16x16x32_bf16 v[98:101], v[182:185], v[198:201], v[98:101]
	v_mfma_f32_16x16x32_bf16 v[86:89], v[174:177], v[206:209], v[86:89]
	v_mfma_f32_16x16x32_bf16 v[82:85], v[182:185], v[206:209], v[82:85]
	v_mfma_f32_16x16x32_bf16 v[70:73], v[174:177], v[214:217], v[70:73]
	v_mfma_f32_16x16x32_bf16 v[66:69], v[182:185], v[214:217], v[66:69]
	s_setprio 0
	s_barrier
	s_mov_b32 m0, s57
	s_add_u32 s38, s38, 0x80080
	ds_read_b128 v[186:189], v159 offset:49152
	ds_read_b128 v[190:193], v159 offset:50176
	ds_read_b128 v[194:197], v159 offset:51200
	ds_read_b128 v[198:201], v159 offset:52224
	ds_read_b128 v[202:205], v159 offset:53248
	ds_read_b128 v[206:209], v159 offset:54272
	ds_read_b128 v[210:213], v159 offset:55296
	ds_read_b128 v[214:217], v159 offset:56320
	global_load_lds_dwordx4 v132, s[98:99]
	s_mov_b32 m0, s58
	s_addc_u32 s39, s39, 0
	global_load_lds_dwordx4 v136, s[98:99]
	s_mov_b32 m0, s61
	s_nop 0
	global_load_lds_dwordx4 v132, s[38:39]
	s_mov_b32 m0, s62
	s_nop 0
	global_load_lds_dwordx4 v136, s[38:39]
	s_mov_b32 m0, s59
	s_nop 0
	global_load_lds_dwordx4 v130, s[100:101]
	s_mov_b32 m0, s60
	s_nop 0
	global_load_lds_dwordx4 v134, s[100:101]
	s_waitcnt vmcnt(8)
	s_waitcnt lgkmcnt(0)
	s_barrier
	s_setprio 1
	s_waitcnt lgkmcnt(0)
	v_mfma_f32_16x16x32_bf16 v[62:65], v[146:149], v[186:189], v[62:65]
	v_mfma_f32_16x16x32_bf16 v[58:61], v[162:165], v[186:189], v[58:61]
	v_mfma_f32_16x16x32_bf16 v[46:49], v[146:149], v[194:197], v[46:49]
	v_mfma_f32_16x16x32_bf16 v[42:45], v[162:165], v[194:197], v[42:45]
	v_mfma_f32_16x16x32_bf16 v[30:33], v[146:149], v[202:205], v[30:33]
	v_mfma_f32_16x16x32_bf16 v[26:29], v[162:165], v[202:205], v[26:29]
	v_mfma_f32_16x16x32_bf16 v[14:17], v[146:149], v[210:213], v[14:17]
	v_mfma_f32_16x16x32_bf16 v[10:13], v[162:165], v[210:213], v[10:13]
	v_mfma_f32_16x16x32_bf16 v[62:65], v[150:153], v[190:193], v[62:65]
	v_mfma_f32_16x16x32_bf16 v[58:61], v[166:169], v[190:193], v[58:61]
	v_mfma_f32_16x16x32_bf16 v[46:49], v[150:153], v[198:201], v[46:49]
	v_mfma_f32_16x16x32_bf16 v[42:45], v[166:169], v[198:201], v[42:45]
	v_mfma_f32_16x16x32_bf16 v[30:33], v[150:153], v[206:209], v[30:33]
	v_mfma_f32_16x16x32_bf16 v[26:29], v[166:169], v[206:209], v[26:29]
	v_mfma_f32_16x16x32_bf16 v[14:17], v[150:153], v[214:217], v[14:17]
	v_mfma_f32_16x16x32_bf16 v[10:13], v[166:169], v[214:217], v[10:13]
	v_mfma_f32_16x16x32_bf16 v[54:57], v[170:173], v[186:189], v[54:57]
	v_mfma_f32_16x16x32_bf16 v[50:53], v[178:181], v[186:189], v[50:53]
	v_mfma_f32_16x16x32_bf16 v[38:41], v[170:173], v[194:197], v[38:41]
	v_mfma_f32_16x16x32_bf16 v[34:37], v[178:181], v[194:197], v[34:37]
	v_mfma_f32_16x16x32_bf16 v[22:25], v[170:173], v[202:205], v[22:25]
	v_mfma_f32_16x16x32_bf16 v[18:21], v[178:181], v[202:205], v[18:21]
	v_mfma_f32_16x16x32_bf16 v[6:9], v[170:173], v[210:213], v[6:9]
	v_mfma_f32_16x16x32_bf16 v[2:5], v[178:181], v[210:213], v[2:5]
	v_mfma_f32_16x16x32_bf16 v[54:57], v[174:177], v[190:193], v[54:57]
	v_mfma_f32_16x16x32_bf16 v[50:53], v[182:185], v[190:193], v[50:53]
	v_mfma_f32_16x16x32_bf16 v[38:41], v[174:177], v[198:201], v[38:41]
	v_mfma_f32_16x16x32_bf16 v[34:37], v[182:185], v[198:201], v[34:37]
	v_mfma_f32_16x16x32_bf16 v[22:25], v[174:177], v[206:209], v[22:25]
	v_mfma_f32_16x16x32_bf16 v[18:21], v[182:185], v[206:209], v[18:21]
	v_mfma_f32_16x16x32_bf16 v[6:9], v[174:177], v[214:217], v[6:9]
	v_mfma_f32_16x16x32_bf16 v[2:5], v[182:185], v[214:217], v[2:5]
	s_setprio 0
	s_barrier
	s_add_u32 s69, s69, 0x100
	s_addc_u32 s70, s70, 0
	s_add_u32 s36, s36, 0x100
	s_addc_u32 s37, s37, 0
	s_cmp_ge_i32 s71, s56
	s_mov_b32 s38, s71
	s_cbranch_scc0 .LBB0_4646

; #define PG8_STAGE(bufoff, gbase, voff) do { _Pragma("unroll") for (int _i = 0; _i < 2; ++_i) \
;         __builtin_amdgcn_global_load_lds((const unsigned*)((const char*)(gbase) + (voff)[_i]), (PG8_LAS unsigned*)(lds + (bufoff) + ldsw + _i * 8192), 16, 0, 0); } while (0)
; #define PG8_LDA(dst, b, h) do { if constexpr (DT != 1) { _Pragma("unroll") for (int m = 0; m < 4; ++m) _Pragma("unroll") for (int k = 0; k < 2; ++k) dst[m][k] = *(const PG8_LAS bf16x8*)(lds + PG8_SA(b, h) + aoff + m * 2048 + k * 1024); } \
;         else { _Pragma("unroll") for (int m = 0; m < 4; ++m) dst##8[m] = ld32(lds + PG8_SA(b, h) + aoff + m * 2048); } } while (0)
; #define PG8_LDB(dst, b, h) do { if constexpr (DT != 1) { _Pragma("unroll") for (int n = 0; n < 2; ++n) _Pragma("unroll") for (int k = 0; k < 2; ++k) dst[n][k] = *(const PG8_LAS bf16x8*)(lds + PG8_SB(b, h) + boff + n * 2048 + k * 1024); } \
;         else { _Pragma("unroll") for (int n = 0; n < 2; ++n) dst##8[n] = ld32(lds + PG8_SB(b, h) + boff + n * 2048); } } while (0)
; #define PG8_WAIT_V(n) asm volatile("s_waitcnt vmcnt(" #n ")" ::: "memory")
; #define PG8_WAIT_L(n) asm volatile("s_waitcnt lgkmcnt(" #n ")" ::: "memory")
; #define PG8_BAR __builtin_amdgcn_s_barrier()
; #define PG8_SCHED __builtin_amdgcn_sched_barrier(0)
;     ...
;             PG8_LDB(B0, 0, 0); PG8_LDB(B1, 0, 1); PG8_SCHED; PG8_LDA(At, 0, 0); PG8_STAGE(PG8_SA(1, 1), a1 + hstepA, voffA);
;             PG8_WAIT_V(8); PG8_WAIT_L(0); PG8_BAR; PG8_MMA(0, 0, At, B0); PG8_MMA(0, 1, At, B1); PG8_BAR; PG8_SCHED;
;             PG8_LDA(At, 0, 1); PG8_STAGE(PG8_SB(0, 0), b2, voffB); PG8_STAGE(PG8_SB(0, 1), b2 + hstepB, voffB); PG8_STAGE(PG8_SA(0, 0), a2, voffA);
;             PG8_WAIT_V(8); PG8_WAIT_L(0); PG8_BAR; PG8_MMA(1, 0, At, B0); PG8_MMA(1, 1, At, B1); PG8_BAR; PG8_SCHED;
.LBB0_4855:
	ds_read_b128 v[16:19], v186
	ds_read_b128 v[20:23], v186 offset:16
	ds_read_b128 v[24:27], v186 offset:2048
	ds_read_b128 v[28:31], v186 offset:2064
	ds_read_b128 v[0:3], v187
	ds_read_b128 v[4:7], v187 offset:16
	ds_read_b128 v[8:11], v187 offset:2048
	ds_read_b128 v[12:15], v187 offset:2064
	s_add_i32 s61, s26, 2
	s_add_u32 s24, s22, 0x100
	s_addc_u32 s25, s23, 0
	s_cmp_eq_u32 s52, s26
	s_cselect_b32 s26, s20, s59
	s_cselect_b32 s29, s3, s25
	s_cselect_b32 s28, s2, s24
	s_cselect_b32 s27, s21, s60
	v_lshl_add_u64 v[216:217], s[22:23], 0, v[170:171]
	s_add_i32 m0, s40, 0xc000
	ds_read_b128 v[176:179], v188
	ds_read_b128 v[180:183], v188 offset:16
	ds_read_b128 v[192:195], v188 offset:2048
	ds_read_b128 v[196:199], v188 offset:2064
	ds_read_b128 v[200:203], v188 offset:4096
	ds_read_b128 v[204:207], v188 offset:4112
	ds_read_b128 v[208:211], v188 offset:6144
	ds_read_b128 v[212:215], v188 offset:6160
	global_load_lds_dwordx4 v[216:217], off
	v_lshl_add_u64 v[216:217], s[22:23], 0, v[168:169]
	s_add_i32 m0, s40, 0xe000
	s_nop 0
	global_load_lds_dwordx4 v[216:217], off
	s_waitcnt vmcnt(8)
	s_waitcnt lgkmcnt(0)
	s_barrier
	s_setprio 1
	s_waitcnt lgkmcnt(0)
	v_mfma_scale_f32_16x16x128_f8f6f4 v[156:159], v[16:23], v[176:183], v[156:159], v189, v189 op_sel_hi:[0,0,0]
	v_mfma_scale_f32_16x16x128_f8f6f4 v[152:155], v[24:31], v[176:183], v[152:155], v189, v189 op_sel_hi:[0,0,0]
	v_mfma_scale_f32_16x16x128_f8f6f4 v[148:151], v[16:23], v[192:199], v[148:151], v189, v189 op_sel_hi:[0,0,0]
	v_mfma_scale_f32_16x16x128_f8f6f4 v[144:147], v[24:31], v[192:199], v[144:147], v189, v189 op_sel_hi:[0,0,0]
	v_mfma_scale_f32_16x16x128_f8f6f4 v[128:131], v[16:23], v[200:207], v[128:131], v189, v189 op_sel_hi:[0,0,0]
	v_mfma_scale_f32_16x16x128_f8f6f4 v[120:123], v[24:31], v[200:207], v[120:123], v189, v189 op_sel_hi:[0,0,0]
	v_mfma_scale_f32_16x16x128_f8f6f4 v[108:111], v[16:23], v[208:215], v[108:111], v189, v189 op_sel_hi:[0,0,0]
	v_mfma_scale_f32_16x16x128_f8f6f4 v[104:107], v[24:31], v[208:215], v[104:107], v189, v189 op_sel_hi:[0,0,0]
	v_mfma_scale_f32_16x16x128_f8f6f4 v[140:143], v[0:7], v[176:183], v[140:143], v189, v189 op_sel_hi:[0,0,0]
	v_mfma_scale_f32_16x16x128_f8f6f4 v[136:139], v[8:15], v[176:183], v[136:139], v189, v189 op_sel_hi:[0,0,0]
	v_mfma_scale_f32_16x16x128_f8f6f4 v[132:135], v[0:7], v[192:199], v[132:135], v189, v189 op_sel_hi:[0,0,0]
	v_mfma_scale_f32_16x16x128_f8f6f4 v[124:127], v[8:15], v[192:199], v[124:127], v189, v189 op_sel_hi:[0,0,0]
	v_mfma_scale_f32_16x16x128_f8f6f4 v[116:119], v[0:7], v[200:207], v[116:119], v189, v189 op_sel_hi:[0,0,0]
	v_mfma_scale_f32_16x16x128_f8f6f4 v[112:115], v[8:15], v[200:207], v[112:115], v189, v189 op_sel_hi:[0,0,0]
	v_mfma_scale_f32_16x16x128_f8f6f4 v[100:103], v[0:7], v[208:215], v[100:103], v189, v189 op_sel_hi:[0,0,0]
	v_mfma_scale_f32_16x16x128_f8f6f4 v[96:99], v[8:15], v[208:215], v[96:99], v189, v189 op_sel_hi:[0,0,0]
	s_setprio 0
	s_barrier
	s_mov_b32 m0, s36
	s_add_u32 s98, s26, 0x80
	s_addc_u32 s99, s27, 0
	s_add_u32 s22, s26, 0xb0000
	ds_read_b128 v[192:195], v188 offset:16384
	ds_read_b128 v[196:199], v188 offset:16400
	ds_read_b128 v[200:203], v188 offset:18432
	ds_read_b128 v[204:207], v188 offset:18448
	ds_read_b128 v[208:211], v188 offset:20480
	ds_read_b128 v[212:215], v188 offset:20496
	ds_read_b128 v[216:219], v188 offset:22528
	ds_read_b128 v[220:223], v188 offset:22544
	global_load_lds_dwordx4 v162, s[26:27]
	s_mov_b32 m0, s37
	s_addc_u32 s23, s27, 0
	global_load_lds_dwordx4 v166, s[26:27]
	s_mov_b32 m0, s38
	s_nop 0
	global_load_lds_dwordx4 v162, s[22:23]
	s_mov_b32 m0, s39
	s_nop 0
	global_load_lds_dwordx4 v166, s[22:23]
	s_add_u32 s100, s28, 0x80
	s_addc_u32 s101, s29, 0
	s_mov_b32 m0, s40
	s_nop 0
	global_load_lds_dwordx4 v160, s[28:29]
	s_mov_b32 m0, s41
	s_nop 0
	global_load_lds_dwordx4 v164, s[28:29]
	s_waitcnt vmcnt(8)
	s_waitcnt lgkmcnt(0)
	s_barrier
	s_setprio 1
	s_waitcnt lgkmcnt(0)
	v_mfma_scale_f32_16x16x128_f8f6f4 v[92:95], v[16:23], v[192:199], v[92:95], v189, v189 op_sel_hi:[0,0,0]
	v_mfma_scale_f32_16x16x128_f8f6f4 v[88:91], v[24:31], v[192:199], v[88:91], v189, v189 op_sel_hi:[0,0,0]
	v_mfma_scale_f32_16x16x128_f8f6f4 v[76:79], v[16:23], v[200:207], v[76:79], v189, v189 op_sel_hi:[0,0,0]
	v_mfma_scale_f32_16x16x128_f8f6f4 v[72:75], v[24:31], v[200:207], v[72:75], v189, v189 op_sel_hi:[0,0,0]
	v_mfma_scale_f32_16x16x128_f8f6f4 v[224:227], v[16:23], v[208:215], v[60:63], v189, v189 op_sel_hi:[0,0,0]
	v_mfma_scale_f32_16x16x128_f8f6f4 v[228:231], v[24:31], v[208:215], v[56:59], v189, v189 op_sel_hi:[0,0,0]
	v_mfma_scale_f32_16x16x128_f8f6f4 v[232:235], v[16:23], v[216:223], v[44:47], v189, v189 op_sel_hi:[0,0,0]
	v_mfma_scale_f32_16x16x128_f8f6f4 v[236:239], v[24:31], v[216:223], v[40:43], v189, v189 op_sel_hi:[0,0,0]
	v_mfma_scale_f32_16x16x128_f8f6f4 v[84:87], v[0:7], v[192:199], v[84:87], v189, v189 op_sel_hi:[0,0,0]
	v_mfma_scale_f32_16x16x128_f8f6f4 v[80:83], v[8:15], v[192:199], v[80:83], v189, v189 op_sel_hi:[0,0,0]
	v_mfma_scale_f32_16x16x128_f8f6f4 v[68:71], v[0:7], v[200:207], v[68:71], v189, v189 op_sel_hi:[0,0,0]
	v_mfma_scale_f32_16x16x128_f8f6f4 v[64:67], v[8:15], v[200:207], v[64:67], v189, v189 op_sel_hi:[0,0,0]
	v_mfma_scale_f32_16x16x128_f8f6f4 v[240:243], v[0:7], v[208:215], v[52:55], v189, v189 op_sel_hi:[0,0,0]
	v_mfma_scale_f32_16x16x128_f8f6f4 v[208:211], v[8:15], v[208:215], v[48:51], v189, v189 op_sel_hi:[0,0,0]
	v_mfma_scale_f32_16x16x128_f8f6f4 v[212:215], v[0:7], v[216:223], v[36:39], v189, v189 op_sel_hi:[0,0,0]
	v_mfma_scale_f32_16x16x128_f8f6f4 v[216:219], v[8:15], v[216:223], v[32:35], v189, v189 op_sel_hi:[0,0,0]
	s_setprio 0
	s_barrier
; #define PG8_STAGE(bufoff, gbase, voff) do { _Pragma("unroll") for (int _i = 0; _i < 2; ++_i) \
;         __builtin_amdgcn_global_load_lds((const unsigned*)((const char*)(gbase) + (voff)[_i]), (PG8_LAS unsigned*)(lds + (bufoff) + ldsw + _i * 8192), 16, 0, 0); } while (0)
; #define PG8_LDA(dst, b, h) do { if constexpr (DT != 1) { _Pragma("unroll") for (int m = 0; m < 4; ++m) _Pragma("unroll") for (int k = 0; k < 2; ++k) dst[m][k] = *(const PG8_LAS bf16x8*)(lds + PG8_SA(b, h) + aoff + m * 2048 + k * 1024); } \
;         else { _Pragma("unroll") for (int m = 0; m < 4; ++m) dst##8[m] = ld32(lds + PG8_SA(b, h) + aoff + m * 2048); } } while (0)
; #define PG8_LDB(dst, b, h) do { if constexpr (DT != 1) { _Pragma("unroll") for (int n = 0; n < 2; ++n) _Pragma("unroll") for (int k = 0; k < 2; ++k) dst[n][k] = *(const PG8_LAS bf16x8*)(lds + PG8_SB(b, h) + boff + n * 2048 + k * 1024); } \
;         else { _Pragma("unroll") for (int n = 0; n < 2; ++n) dst##8[n] = ld32(lds + PG8_SB(b, h) + boff + n * 2048); } } while (0)
; #define PG8_WAIT_V(n) asm volatile("s_waitcnt vmcnt(" #n ")" ::: "memory")
; #define PG8_WAIT_L(n) asm volatile("s_waitcnt lgkmcnt(" #n ")" ::: "memory")
; #define PG8_BAR __builtin_amdgcn_s_barrier()
; #define PG8_SCHED __builtin_amdgcn_sched_barrier(0)
;     ...
;             PG8_LDB(B0, 1, 0); PG8_LDB(B1, 1, 1); PG8_SCHED; PG8_LDA(At, 1, 0); PG8_STAGE(PG8_SA(0, 1), a2 + hstepA, voffA);
;             PG8_WAIT_V(8); PG8_WAIT_L(0); PG8_BAR; PG8_MMA(0, 0, At, B0); PG8_MMA(0, 1, At, B1); PG8_BAR; PG8_SCHED;
;             PG8_LDA(At, 1, 1); PG8_STAGE(PG8_SB(1, 0), b3, voffB); PG8_STAGE(PG8_SB(1, 1), b3 + hstepB, voffB); PG8_STAGE(PG8_SA(1, 0), a3, voffA);
;             PG8_WAIT_V(8); PG8_WAIT_L(0); PG8_BAR; PG8_MMA(1, 0, At, B0); PG8_MMA(1, 1, At, B1); PG8_BAR; PG8_SCHED;
	ds_read_b128 v[0:3], v190
	ds_read_b128 v[4:7], v190 offset:16
	ds_read_b128 v[8:11], v190 offset:2048
	ds_read_b128 v[12:15], v190 offset:2064
	ds_read_b128 v[16:19], v191
	ds_read_b128 v[20:23], v191 offset:16
	ds_read_b128 v[24:27], v191 offset:2048
	ds_read_b128 v[28:31], v191 offset:2064
	s_add_u32 s22, s28, 0xb0000
	s_addc_u32 s23, s29, 0
	s_mov_b32 m0, s42
	ds_read_b128 v[32:35], v188 offset:32768
	ds_read_b128 v[36:39], v188 offset:32784
	ds_read_b128 v[40:43], v188 offset:34816
	ds_read_b128 v[44:47], v188 offset:34832
	ds_read_b128 v[48:51], v188 offset:36864
	ds_read_b128 v[52:55], v188 offset:36880
	ds_read_b128 v[56:59], v188 offset:38912
	ds_read_b128 v[60:63], v188 offset:38928
	global_load_lds_dwordx4 v160, s[22:23]
	s_mov_b32 m0, s43
	s_nop 0
	global_load_lds_dwordx4 v164, s[22:23]
	s_waitcnt vmcnt(8)
	s_waitcnt lgkmcnt(0)
	s_barrier
	s_setprio 1
	s_waitcnt lgkmcnt(0)
	v_mfma_scale_f32_16x16x128_f8f6f4 v[156:159], v[0:7], v[32:39], v[156:159], v189, v189 op_sel_hi:[0,0,0]
	v_mfma_scale_f32_16x16x128_f8f6f4 v[152:155], v[8:15], v[32:39], v[152:155], v189, v189 op_sel_hi:[0,0,0]
	v_mfma_scale_f32_16x16x128_f8f6f4 v[148:151], v[0:7], v[40:47], v[148:151], v189, v189 op_sel_hi:[0,0,0]
	v_mfma_scale_f32_16x16x128_f8f6f4 v[144:147], v[8:15], v[40:47], v[144:147], v189, v189 op_sel_hi:[0,0,0]
	v_mfma_scale_f32_16x16x128_f8f6f4 v[128:131], v[0:7], v[48:55], v[128:131], v189, v189 op_sel_hi:[0,0,0]
	v_mfma_scale_f32_16x16x128_f8f6f4 v[120:123], v[8:15], v[48:55], v[120:123], v189, v189 op_sel_hi:[0,0,0]
	v_mfma_scale_f32_16x16x128_f8f6f4 v[108:111], v[0:7], v[56:63], v[108:111], v189, v189 op_sel_hi:[0,0,0]
	v_mfma_scale_f32_16x16x128_f8f6f4 v[104:107], v[8:15], v[56:63], v[104:107], v189, v189 op_sel_hi:[0,0,0]
	v_mfma_scale_f32_16x16x128_f8f6f4 v[140:143], v[16:23], v[32:39], v[140:143], v189, v189 op_sel_hi:[0,0,0]
	v_mfma_scale_f32_16x16x128_f8f6f4 v[136:139], v[24:31], v[32:39], v[136:139], v189, v189 op_sel_hi:[0,0,0]
	v_mfma_scale_f32_16x16x128_f8f6f4 v[132:135], v[16:23], v[40:47], v[132:135], v189, v189 op_sel_hi:[0,0,0]
	v_mfma_scale_f32_16x16x128_f8f6f4 v[124:127], v[24:31], v[40:47], v[124:127], v189, v189 op_sel_hi:[0,0,0]
	v_mfma_scale_f32_16x16x128_f8f6f4 v[116:119], v[16:23], v[48:55], v[116:119], v189, v189 op_sel_hi:[0,0,0]
	v_mfma_scale_f32_16x16x128_f8f6f4 v[112:115], v[24:31], v[48:55], v[112:115], v189, v189 op_sel_hi:[0,0,0]
	v_mfma_scale_f32_16x16x128_f8f6f4 v[100:103], v[16:23], v[56:63], v[100:103], v189, v189 op_sel_hi:[0,0,0]
	v_mfma_scale_f32_16x16x128_f8f6f4 v[96:99], v[24:31], v[56:63], v[96:99], v189, v189 op_sel_hi:[0,0,0]
	s_setprio 0
	s_barrier
	s_mov_b32 m0, s46
	s_add_u32 s22, s26, 0xb0080
	ds_read_b128 v[32:35], v188 offset:49152
	ds_read_b128 v[36:39], v188 offset:49168
	ds_read_b128 v[48:51], v188 offset:51200
	ds_read_b128 v[52:55], v188 offset:51216
	ds_read_b128 v[192:195], v188 offset:53248
	ds_read_b128 v[196:199], v188 offset:53264
	ds_read_b128 v[200:203], v188 offset:55296
	ds_read_b128 v[204:207], v188 offset:55312
	global_load_lds_dwordx4 v162, s[98:99]
	s_mov_b32 m0, s47
	s_addc_u32 s23, s27, 0
	global_load_lds_dwordx4 v166, s[98:99]
	s_mov_b32 m0, s50
	s_nop 0
	global_load_lds_dwordx4 v162, s[22:23]
	s_mov_b32 m0, s51
	s_nop 0
	global_load_lds_dwordx4 v166, s[22:23]
	s_mov_b32 m0, s48
	s_nop 0
	global_load_lds_dwordx4 v160, s[100:101]
	s_mov_b32 m0, s49
	s_nop 0
	global_load_lds_dwordx4 v164, s[100:101]
	s_waitcnt vmcnt(8)
	s_waitcnt lgkmcnt(0)
	s_barrier
	s_setprio 1
	s_waitcnt lgkmcnt(0)
	v_mfma_scale_f32_16x16x128_f8f6f4 v[92:95], v[0:7], v[32:39], v[92:95], v189, v189 op_sel_hi:[0,0,0]
	v_mfma_scale_f32_16x16x128_f8f6f4 v[88:91], v[8:15], v[32:39], v[88:91], v189, v189 op_sel_hi:[0,0,0]
	v_mfma_scale_f32_16x16x128_f8f6f4 v[76:79], v[0:7], v[48:55], v[76:79], v189, v189 op_sel_hi:[0,0,0]
	v_mfma_scale_f32_16x16x128_f8f6f4 v[72:75], v[8:15], v[48:55], v[72:75], v189, v189 op_sel_hi:[0,0,0]
	v_mfma_scale_f32_16x16x128_f8f6f4 v[60:63], v[0:7], v[192:199], v[224:227], v189, v189 op_sel_hi:[0,0,0]
	v_mfma_scale_f32_16x16x128_f8f6f4 v[56:59], v[8:15], v[192:199], v[228:231], v189, v189 op_sel_hi:[0,0,0]
	v_mfma_scale_f32_16x16x128_f8f6f4 v[44:47], v[0:7], v[200:207], v[232:235], v189, v189 op_sel_hi:[0,0,0]
	v_mfma_scale_f32_16x16x128_f8f6f4 v[40:43], v[8:15], v[200:207], v[236:239], v189, v189 op_sel_hi:[0,0,0]
	v_mfma_scale_f32_16x16x128_f8f6f4 v[84:87], v[16:23], v[32:39], v[84:87], v189, v189 op_sel_hi:[0,0,0]
	v_mfma_scale_f32_16x16x128_f8f6f4 v[80:83], v[24:31], v[32:39], v[80:83], v189, v189 op_sel_hi:[0,0,0]
	v_mfma_scale_f32_16x16x128_f8f6f4 v[68:71], v[16:23], v[48:55], v[68:71], v189, v189 op_sel_hi:[0,0,0]
	v_mfma_scale_f32_16x16x128_f8f6f4 v[64:67], v[24:31], v[48:55], v[64:67], v189, v189 op_sel_hi:[0,0,0]
	v_mfma_scale_f32_16x16x128_f8f6f4 v[52:55], v[16:23], v[192:199], v[240:243], v189, v189 op_sel_hi:[0,0,0]
	v_mfma_scale_f32_16x16x128_f8f6f4 v[48:51], v[24:31], v[192:199], v[208:211], v189, v189 op_sel_hi:[0,0,0]
	v_mfma_scale_f32_16x16x128_f8f6f4 v[36:39], v[16:23], v[200:207], v[212:215], v189, v189 op_sel_hi:[0,0,0]
	v_mfma_scale_f32_16x16x128_f8f6f4 v[32:35], v[24:31], v[200:207], v[216:219], v189, v189 op_sel_hi:[0,0,0]
	s_setprio 0
	s_barrier
	s_add_u32 s59, s59, 0x100
	s_addc_u32 s60, s60, 0
	s_cmp_ge_i32 s61, s45
	s_mov_b64 s[22:23], s[24:25]
	s_mov_b32 s26, s61
	s_cbranch_scc0 .LBB0_4855
